# GEMM MMA segments: all s_setprio flips removed as well (segment = barrier, MFMAs, barrier)
# baseline (speedup 1.0000x reference)
; #define PG8_STAGE(bufoff, gbase, voff) do { _Pragma("unroll") for (int _i = 0; _i < 2; ++_i) \
;         __builtin_amdgcn_global_load_lds((const unsigned*)((const char*)(gbase) + (voff)[_i]), (LAS unsigned*)(lds + (bufoff) + ldsw + _i * 8192), 16, 0, 0); } while (0)
; #define PG8_LDA(dst, b, h) do { _Pragma("unroll") for (int m = 0; m < 4; ++m) dst[m] = PG8_LD32(lds + PG8_SA(b, h) + aoff + m * 2048); } while (0)
; #define PG8_LDB(dst, b, h) do { _Pragma("unroll") for (int n = 0; n < 2; ++n) dst[n] = PG8_LD32(lds + PG8_SB(b, h) + boff + n * 2048); } while (0)
; #define PG8_WAIT_V(n) asm volatile("s_waitcnt vmcnt(" #n ")" ::: "memory")
; #define PG8_WAIT_L(n) asm volatile("s_waitcnt lgkmcnt(" #n ")" ::: "memory")
; #define PG8_BAR __builtin_amdgcn_s_barrier()
; #define PG8_SCHED __builtin_amdgcn_sched_barrier(0)
; #define PG8_STA(bufoff, nextflag, h, koff) do { if constexpr (Sched::GATHER) { unsigned _o[2]; _o[0] = (nextflag) ? nxtA[h][0] : curA[h][0]; _o[1] = (nextflag) ? nxtA[h][1] : curA[h][1]; PG8_STAGE(bufoff, Ab + (koff), _o); } \
;         else { PG8_STAGE(bufoff, ((nextflag) ? nA : cA) + (size_t)(h) * hstep + (koff), voffA); } } while (0)
; template <class Epi, class Sched, bool ALIGN_EPI, int DT>
; __device__ __forceinline__ void gemm_phase(LAS unsigned char* lds, const int KB, const Sched& S, const Epi& E) {
;     ...
;         for (int t = 0; t < nt; t += 2) {
;             const bool last = (t == nt - 2);
;             const size_t k1 = (size_t)(t + 1) * kstep, k2 = last ? 0 : (size_t)(t + 2) * kstep, k3 = k2 + kstep;
;             const char* b2 = last ? nB : cB + (size_t)(t + 2) * kstep; const char* b3 = b2 + kstep;
;             PG8_LDB(B0, 0, 0); PG8_LDB(B1, 0, 1); PG8_SCHED; PG8_LDA(At, 0, 0); PG8_STA(PG8_SA(1, 1), false, 1, k1);
;             PG8_WAIT_V(8); PG8_WAIT_L(0); PG8_BAR; PG8_MMA(0, 0, At, B0); PG8_MMA(0, 1, At, B1); PG8_BAR; PG8_SCHED;
;             PG8_LDA(At, 0, 1); PG8_STAGE(PG8_SB(0, 0), b2, voffB); PG8_STAGE(PG8_SB(0, 1), b2 + hstep, voffB); PG8_STA(PG8_SA(0, 0), last, 0, k2);
;             PG8_WAIT_V(8); PG8_WAIT_L(0); PG8_BAR; PG8_MMA(1, 0, At, B0); PG8_MMA(1, 1, At, B1); PG8_BAR; PG8_SCHED;
.LBB0_193:
	ds_read_b128 v[152:155], v175
	ds_read_b128 v[156:159], v175 offset:1024
	ds_read_b128 v[160:163], v175 offset:2048
	ds_read_b128 v[164:167], v175 offset:3072
	ds_read_b128 v[168:171], v176
	ds_read_b128 v[182:185], v176 offset:1024
	ds_read_b128 v[186:189], v176 offset:2048
	ds_read_b128 v[190:193], v176 offset:3072
	s_add_u32 s38, s36, 0x100
	s_addc_u32 s39, s37, 0
	s_add_u32 s68, s25, s36
	s_addc_u32 s69, s66, s37
	s_cmp_eq_u32 s67, 12
	s_cselect_b64 s[42:43], -1, 0
	s_and_b64 s[40:41], s[42:43], exec
	s_cselect_b32 s70, 0, s38
	s_cselect_b32 s41, s0, s69
	s_cselect_b32 s40, s23, s68
	v_lshl_add_u64 v[228:229], v[148:149], 0, s[36:37]
	s_add_i32 m0, s45, 0xc000
	ds_read_b128 v[196:199], v177
	ds_read_b128 v[200:203], v177 offset:1024
	ds_read_b128 v[204:207], v177 offset:2048
	ds_read_b128 v[208:211], v177 offset:3072
	ds_read_b128 v[212:215], v177 offset:4096
	ds_read_b128 v[216:219], v177 offset:5120
	ds_read_b128 v[220:223], v177 offset:6144
	ds_read_b128 v[224:227], v177 offset:7168
	global_load_lds_dwordx4 v[228:229], off
	v_lshl_add_u64 v[228:229], v[150:151], 0, s[36:37]
	s_add_i32 m0, s45, 0xe000
	s_nop 0
	global_load_lds_dwordx4 v[228:229], off
	s_waitcnt vmcnt(8)
	s_waitcnt lgkmcnt(0)
	s_barrier
	v_mfma_i32_16x16x64_i8 v[126:129], v[152:155], v[196:199], v[126:129]
	v_mfma_i32_16x16x64_i8 v[122:125], v[160:163], v[196:199], v[122:125]
	v_mfma_i32_16x16x64_i8 v[110:113], v[152:155], v[204:207], v[110:113]
	v_mfma_i32_16x16x64_i8 v[106:109], v[160:163], v[204:207], v[106:109]
	v_mfma_i32_16x16x64_i8 v[94:97], v[152:155], v[212:215], v[94:97]
	v_mfma_i32_16x16x64_i8 v[90:93], v[160:163], v[212:215], v[90:93]
	v_mfma_i32_16x16x64_i8 v[78:81], v[152:155], v[220:223], v[78:81]
	v_mfma_i32_16x16x64_i8 v[74:77], v[160:163], v[220:223], v[74:77]
	v_mfma_i32_16x16x64_i8 v[126:129], v[156:159], v[200:203], v[126:129]
	v_mfma_i32_16x16x64_i8 v[122:125], v[164:167], v[200:203], v[122:125]
	v_mfma_i32_16x16x64_i8 v[110:113], v[156:159], v[208:211], v[110:113]
	v_mfma_i32_16x16x64_i8 v[106:109], v[164:167], v[208:211], v[106:109]
	v_mfma_i32_16x16x64_i8 v[94:97], v[156:159], v[216:219], v[94:97]
	v_mfma_i32_16x16x64_i8 v[90:93], v[164:167], v[216:219], v[90:93]
	v_mfma_i32_16x16x64_i8 v[78:81], v[156:159], v[224:227], v[78:81]
	v_mfma_i32_16x16x64_i8 v[74:77], v[164:167], v[224:227], v[74:77]
	v_mfma_i32_16x16x64_i8 v[118:121], v[168:171], v[196:199], v[118:121]
	v_mfma_i32_16x16x64_i8 v[114:117], v[186:189], v[196:199], v[114:117]
	v_mfma_i32_16x16x64_i8 v[102:105], v[168:171], v[204:207], v[102:105]
	v_mfma_i32_16x16x64_i8 v[98:101], v[186:189], v[204:207], v[98:101]
	v_mfma_i32_16x16x64_i8 v[86:89], v[168:171], v[212:215], v[86:89]
	v_mfma_i32_16x16x64_i8 v[82:85], v[186:189], v[212:215], v[82:85]
	v_mfma_i32_16x16x64_i8 v[70:73], v[168:171], v[220:223], v[70:73]
	v_mfma_i32_16x16x64_i8 v[66:69], v[186:189], v[220:223], v[66:69]
	v_mfma_i32_16x16x64_i8 v[118:121], v[182:185], v[200:203], v[118:121]
	v_mfma_i32_16x16x64_i8 v[114:117], v[190:193], v[200:203], v[114:117]
	v_mfma_i32_16x16x64_i8 v[102:105], v[182:185], v[208:211], v[102:105]
	v_mfma_i32_16x16x64_i8 v[98:101], v[190:193], v[208:211], v[98:101]
	v_mfma_i32_16x16x64_i8 v[86:89], v[182:185], v[216:219], v[86:89]
	v_mfma_i32_16x16x64_i8 v[82:85], v[190:193], v[216:219], v[82:85]
	v_mfma_i32_16x16x64_i8 v[70:73], v[182:185], v[224:227], v[70:73]
	v_mfma_i32_16x16x64_i8 v[66:69], v[190:193], v[224:227], v[66:69]
	s_barrier
	s_add_i32 s36, s62, s5
	v_lshl_add_u64 v[228:229], s[40:41], 0, v[134:135]
	s_mov_b32 m0, s36
	ds_read_b128 v[196:199], v177 offset:16384
	ds_read_b128 v[200:203], v177 offset:17408
	ds_read_b128 v[204:207], v177 offset:18432
	ds_read_b128 v[208:211], v177 offset:19456
	ds_read_b128 v[212:215], v177 offset:20480
	ds_read_b128 v[216:219], v177 offset:21504
	ds_read_b128 v[220:223], v177 offset:22528
	ds_read_b128 v[224:227], v177 offset:23552
	global_load_lds_dwordx4 v[228:229], off
	s_add_i32 m0, s36, 0x2000
	s_add_u32 s36, s40, 0x40000
	v_lshl_add_u64 v[230:231], s[40:41], 0, v[132:133]
	s_addc_u32 s37, s41, 0
	s_add_i32 s68, s63, s5
	global_load_lds_dwordx4 v[230:231], off
	v_lshl_add_u64 v[232:233], s[36:37], 0, v[134:135]
	s_mov_b32 m0, s68
	s_nop 0
	global_load_lds_dwordx4 v[232:233], off
	v_lshl_add_u64 v[232:233], s[36:37], 0, v[132:133]
	s_add_i32 m0, s68, 0x2000
	s_and_b64 s[36:37], s[8:9], s[42:43]
	s_and_b64 s[36:37], s[36:37], exec
	s_cselect_b32 s36, s26, s34
	s_cselect_b32 s37, s27, s35
	s_add_u32 s36, s36, s70
	s_addc_u32 s37, s37, 0
	global_load_lds_dwordx4 v[232:233], off
	v_lshl_add_u64 v[232:233], s[36:37], 0, v[136:137]
	s_mov_b32 m0, s45
	v_lshl_add_u64 v[234:235], s[36:37], 0, v[138:139]
	global_load_lds_dwordx4 v[232:233], off
	s_mov_b32 m0, s46
	s_nop 0
	global_load_lds_dwordx4 v[234:235], off
	s_waitcnt vmcnt(8)
	s_waitcnt lgkmcnt(0)
	s_barrier
; #define PG8_LDA(dst, b, h) do { _Pragma("unroll") for (int m = 0; m < 4; ++m) dst[m] = PG8_LD32(lds + PG8_SA(b, h) + aoff + m * 2048); } while (0)
; #define PG8_LDB(dst, b, h) do { _Pragma("unroll") for (int n = 0; n < 2; ++n) dst[n] = PG8_LD32(lds + PG8_SB(b, h) + boff + n * 2048); } while (0)
; #define PG8_WAIT_V(n) asm volatile("s_waitcnt vmcnt(" #n ")" ::: "memory")
; #define PG8_WAIT_L(n) asm volatile("s_waitcnt lgkmcnt(" #n ")" ::: "memory")
; #define PG8_BAR __builtin_amdgcn_s_barrier()
; #define PG8_SCHED __builtin_amdgcn_sched_barrier(0)
; #define PG8_STA(bufoff, nextflag, h, koff) do { if constexpr (Sched::GATHER) { unsigned _o[2]; _o[0] = (nextflag) ? nxtA[h][0] : curA[h][0]; _o[1] = (nextflag) ? nxtA[h][1] : curA[h][1]; PG8_STAGE(bufoff, Ab + (koff), _o); } \
;         else { PG8_STAGE(bufoff, ((nextflag) ? nA : cA) + (size_t)(h) * hstep + (koff), voffA); } } while (0)
; template <class Epi, class Sched, bool ALIGN_EPI, int DT>
; __device__ __forceinline__ void gemm_phase(LAS unsigned char* lds, const int KB, const Sched& S, const Epi& E) {
;     ...
;             PG8_WAIT_V(8); PG8_WAIT_L(0); PG8_BAR; PG8_MMA(1, 0, At, B0); PG8_MMA(1, 1, At, B1); PG8_BAR; PG8_SCHED;
;             PG8_LDB(B0, 1, 0); PG8_LDB(B1, 1, 1); PG8_SCHED; PG8_LDA(At, 1, 0); PG8_STA(PG8_SA(0, 1), last, 1, k2);
;             PG8_WAIT_V(8); PG8_WAIT_L(0); PG8_BAR; PG8_MMA(0, 0, At, B0); PG8_MMA(0, 1, At, B1); PG8_BAR; PG8_SCHED;
	v_mfma_i32_16x16x64_i8 v[62:65], v[152:155], v[196:199], v[62:65]
	v_mfma_i32_16x16x64_i8 v[58:61], v[160:163], v[196:199], v[58:61]
	v_mfma_i32_16x16x64_i8 v[46:49], v[152:155], v[204:207], v[46:49]
	v_mfma_i32_16x16x64_i8 v[42:45], v[160:163], v[204:207], v[42:45]
	v_mfma_i32_16x16x64_i8 v[30:33], v[152:155], v[212:215], v[30:33]
	v_mfma_i32_16x16x64_i8 v[26:29], v[160:163], v[212:215], v[26:29]
	v_mfma_i32_16x16x64_i8 v[6:9], v[152:155], v[220:223], v[6:9]
	v_mfma_i32_16x16x64_i8 v[2:5], v[160:163], v[220:223], v[2:5]
	v_mfma_i32_16x16x64_i8 v[62:65], v[156:159], v[200:203], v[62:65]
	v_mfma_i32_16x16x64_i8 v[58:61], v[164:167], v[200:203], v[58:61]
	v_mfma_i32_16x16x64_i8 v[46:49], v[156:159], v[208:211], v[46:49]
	v_mfma_i32_16x16x64_i8 v[42:45], v[164:167], v[208:211], v[42:45]
	v_mfma_i32_16x16x64_i8 v[30:33], v[156:159], v[216:219], v[30:33]
	v_mfma_i32_16x16x64_i8 v[26:29], v[164:167], v[216:219], v[26:29]
	v_mfma_i32_16x16x64_i8 v[6:9], v[156:159], v[224:227], v[6:9]
	v_mfma_i32_16x16x64_i8 v[2:5], v[164:167], v[224:227], v[2:5]
	v_mfma_i32_16x16x64_i8 v[54:57], v[168:171], v[196:199], v[54:57]
	v_mfma_i32_16x16x64_i8 v[50:53], v[186:189], v[196:199], v[50:53]
	v_mfma_i32_16x16x64_i8 v[38:41], v[168:171], v[204:207], v[38:41]
	v_mfma_i32_16x16x64_i8 v[34:37], v[186:189], v[204:207], v[34:37]
	v_mfma_i32_16x16x64_i8 v[14:17], v[168:171], v[212:215], v[14:17]
	v_mfma_i32_16x16x64_i8 v[10:13], v[186:189], v[212:215], v[10:13]
	v_mfma_i32_16x16x64_i8 v[22:25], v[168:171], v[220:223], v[22:25]
	v_mfma_i32_16x16x64_i8 v[18:21], v[186:189], v[220:223], v[18:21]
	v_mfma_i32_16x16x64_i8 v[54:57], v[182:185], v[200:203], v[54:57]
	v_mfma_i32_16x16x64_i8 v[50:53], v[190:193], v[200:203], v[50:53]
	v_mfma_i32_16x16x64_i8 v[38:41], v[182:185], v[208:211], v[38:41]
	v_mfma_i32_16x16x64_i8 v[34:37], v[190:193], v[208:211], v[34:37]
	v_mfma_i32_16x16x64_i8 v[14:17], v[182:185], v[216:219], v[14:17]
	v_mfma_i32_16x16x64_i8 v[10:13], v[190:193], v[216:219], v[10:13]
	v_mfma_i32_16x16x64_i8 v[22:25], v[182:185], v[224:227], v[22:25]
	v_mfma_i32_16x16x64_i8 v[18:21], v[190:193], v[224:227], v[18:21]
	s_barrier
	s_add_i32 s42, 0, 0x18000
	v_add_u32_e32 v1, s42, v173
	s_add_i32 s43, 0, 0x1c000
	ds_read_b128 v[152:155], v1
	ds_read_b128 v[156:159], v1 offset:1024
	ds_read_b128 v[160:163], v1 offset:2048
	ds_read_b128 v[164:167], v1 offset:3072
	v_add_u32_e32 v1, s43, v173
	ds_read_b128 v[168:171], v1
	ds_read_b128 v[182:185], v1 offset:1024
	ds_read_b128 v[186:189], v1 offset:2048
	ds_read_b128 v[190:193], v1 offset:3072
	s_add_u32 s36, s36, 0x40000
	s_addc_u32 s37, s37, 0
	s_mov_b32 m0, s47
	v_lshl_add_u64 v[236:237], s[36:37], 0, v[136:137]
	ds_read_b128 v[196:199], v177 offset:32768
	ds_read_b128 v[200:203], v177 offset:33792
	ds_read_b128 v[204:207], v177 offset:34816
	ds_read_b128 v[208:211], v177 offset:35840
	ds_read_b128 v[212:215], v177 offset:36864
	ds_read_b128 v[216:219], v177 offset:37888
	ds_read_b128 v[220:223], v177 offset:38912
	ds_read_b128 v[224:227], v177 offset:39936
	global_load_lds_dwordx4 v[236:237], off
	v_lshl_add_u64 v[236:237], s[36:37], 0, v[138:139]
	s_mov_b32 m0, s49
	s_nop 0
	global_load_lds_dwordx4 v[236:237], off
	s_waitcnt vmcnt(8)
	s_waitcnt lgkmcnt(0)
	s_barrier
	v_mfma_i32_16x16x64_i8 v[126:129], v[152:155], v[196:199], v[126:129]
	v_mfma_i32_16x16x64_i8 v[122:125], v[160:163], v[196:199], v[122:125]
	v_mfma_i32_16x16x64_i8 v[110:113], v[152:155], v[204:207], v[110:113]
	v_mfma_i32_16x16x64_i8 v[106:109], v[160:163], v[204:207], v[106:109]
	v_mfma_i32_16x16x64_i8 v[94:97], v[152:155], v[212:215], v[94:97]
	v_mfma_i32_16x16x64_i8 v[90:93], v[160:163], v[212:215], v[90:93]
	v_mfma_i32_16x16x64_i8 v[78:81], v[152:155], v[220:223], v[78:81]
	v_mfma_i32_16x16x64_i8 v[74:77], v[160:163], v[220:223], v[74:77]
	v_mfma_i32_16x16x64_i8 v[126:129], v[156:159], v[200:203], v[126:129]
	v_mfma_i32_16x16x64_i8 v[122:125], v[164:167], v[200:203], v[122:125]
	v_mfma_i32_16x16x64_i8 v[110:113], v[156:159], v[208:211], v[110:113]
	v_mfma_i32_16x16x64_i8 v[106:109], v[164:167], v[208:211], v[106:109]
	v_mfma_i32_16x16x64_i8 v[94:97], v[156:159], v[216:219], v[94:97]
	v_mfma_i32_16x16x64_i8 v[90:93], v[164:167], v[216:219], v[90:93]
	v_mfma_i32_16x16x64_i8 v[78:81], v[156:159], v[224:227], v[78:81]
	v_mfma_i32_16x16x64_i8 v[74:77], v[164:167], v[224:227], v[74:77]
	v_mfma_i32_16x16x64_i8 v[118:121], v[168:171], v[196:199], v[118:121]
	v_mfma_i32_16x16x64_i8 v[114:117], v[186:189], v[196:199], v[114:117]
	v_mfma_i32_16x16x64_i8 v[102:105], v[168:171], v[204:207], v[102:105]
	v_mfma_i32_16x16x64_i8 v[98:101], v[186:189], v[204:207], v[98:101]
	v_mfma_i32_16x16x64_i8 v[86:89], v[168:171], v[212:215], v[86:89]
	v_mfma_i32_16x16x64_i8 v[82:85], v[186:189], v[212:215], v[82:85]
	v_mfma_i32_16x16x64_i8 v[70:73], v[168:171], v[220:223], v[70:73]
	v_mfma_i32_16x16x64_i8 v[66:69], v[186:189], v[220:223], v[66:69]
	v_mfma_i32_16x16x64_i8 v[118:121], v[182:185], v[200:203], v[118:121]
	v_mfma_i32_16x16x64_i8 v[114:117], v[190:193], v[200:203], v[114:117]
	v_mfma_i32_16x16x64_i8 v[102:105], v[182:185], v[208:211], v[102:105]
	v_mfma_i32_16x16x64_i8 v[98:101], v[190:193], v[208:211], v[98:101]
	v_mfma_i32_16x16x64_i8 v[86:89], v[182:185], v[216:219], v[86:89]
	v_mfma_i32_16x16x64_i8 v[82:85], v[190:193], v[216:219], v[82:85]
	v_mfma_i32_16x16x64_i8 v[70:73], v[182:185], v[224:227], v[70:73]
	v_mfma_i32_16x16x64_i8 v[66:69], v[190:193], v[224:227], v[66:69]
	s_barrier
; #define PG8_STAGE(bufoff, gbase, voff) do { _Pragma("unroll") for (int _i = 0; _i < 2; ++_i) \
;         __builtin_amdgcn_global_load_lds((const unsigned*)((const char*)(gbase) + (voff)[_i]), (LAS unsigned*)(lds + (bufoff) + ldsw + _i * 8192), 16, 0, 0); } while (0)
; #define PG8_LDA(dst, b, h) do { _Pragma("unroll") for (int m = 0; m < 4; ++m) dst[m] = PG8_LD32(lds + PG8_SA(b, h) + aoff + m * 2048); } while (0)
; #define PG8_WAIT_V(n) asm volatile("s_waitcnt vmcnt(" #n ")" ::: "memory")
; #define PG8_WAIT_L(n) asm volatile("s_waitcnt lgkmcnt(" #n ")" ::: "memory")
; #define PG8_BAR __builtin_amdgcn_s_barrier()
; #define PG8_SCHED __builtin_amdgcn_sched_barrier(0)
; #define PG8_STA(bufoff, nextflag, h, koff) do { if constexpr (Sched::GATHER) { unsigned _o[2]; _o[0] = (nextflag) ? nxtA[h][0] : curA[h][0]; _o[1] = (nextflag) ? nxtA[h][1] : curA[h][1]; PG8_STAGE(bufoff, Ab + (koff), _o); } \
;         else { PG8_STAGE(bufoff, ((nextflag) ? nA : cA) + (size_t)(h) * hstep + (koff), voffA); } } while (0)
; template <class Epi, class Sched, bool ALIGN_EPI, int DT>
; __device__ __forceinline__ void gemm_phase(LAS unsigned char* lds, const int KB, const Sched& S, const Epi& E) {
;     ...
;             PG8_LDA(At, 1, 1); PG8_STAGE(PG8_SB(1, 0), b3, voffB); PG8_STAGE(PG8_SB(1, 1), b3 + hstep, voffB); PG8_STA(PG8_SA(1, 0), last, 0, k3);
;             PG8_WAIT_V(8); PG8_WAIT_L(0); PG8_BAR; PG8_MMA(1, 0, At, B0); PG8_MMA(1, 1, At, B1); PG8_BAR; PG8_SCHED;
;         }
;         if constexpr (ALIGN_EPI) { if (wr == 0) PG8_BAR; }
	s_add_i32 s36, s42, s5
	v_lshl_add_u64 v[228:229], v[228:229], 0, s[18:19]
	s_mov_b32 m0, s36
	ds_read_b128 v[196:199], v177 offset:49152
	ds_read_b128 v[200:203], v177 offset:50176
	ds_read_b128 v[204:207], v177 offset:51200
	ds_read_b128 v[208:211], v177 offset:52224
	ds_read_b128 v[212:215], v177 offset:53248
	ds_read_b128 v[216:219], v177 offset:54272
	ds_read_b128 v[220:223], v177 offset:55296
	ds_read_b128 v[224:227], v177 offset:56320
	global_load_lds_dwordx4 v[228:229], off
	s_add_i32 m0, s36, 0x2000
	s_add_u32 s36, s40, 0x40080
	v_lshl_add_u64 v[228:229], v[230:231], 0, s[18:19]
	s_addc_u32 s37, s41, 0
	s_add_i32 s40, s43, s5
	global_load_lds_dwordx4 v[228:229], off
	v_lshl_add_u64 v[228:229], s[36:37], 0, v[134:135]
	s_mov_b32 m0, s40
	s_nop 0
	global_load_lds_dwordx4 v[228:229], off
	v_lshl_add_u64 v[228:229], s[36:37], 0, v[132:133]
	s_add_i32 m0, s40, 0x2000
	s_nop 0
	global_load_lds_dwordx4 v[228:229], off
	v_lshl_add_u64 v[228:229], v[232:233], 0, s[18:19]
	s_mov_b32 m0, s55
	s_nop 0
	global_load_lds_dwordx4 v[228:229], off
	v_lshl_add_u64 v[228:229], v[234:235], 0, s[18:19]
	s_mov_b32 m0, s56
	s_nop 0
	global_load_lds_dwordx4 v[228:229], off
	s_waitcnt vmcnt(8)
	s_waitcnt lgkmcnt(0)
	s_barrier
	v_mfma_i32_16x16x64_i8 v[62:65], v[152:155], v[196:199], v[62:65]
	v_mfma_i32_16x16x64_i8 v[58:61], v[160:163], v[196:199], v[58:61]
	v_mfma_i32_16x16x64_i8 v[46:49], v[152:155], v[204:207], v[46:49]
	v_mfma_i32_16x16x64_i8 v[42:45], v[160:163], v[204:207], v[42:45]
	v_mfma_i32_16x16x64_i8 v[30:33], v[152:155], v[212:215], v[30:33]
	v_mfma_i32_16x16x64_i8 v[26:29], v[160:163], v[212:215], v[26:29]
	v_mfma_i32_16x16x64_i8 v[6:9], v[152:155], v[220:223], v[6:9]
	v_mfma_i32_16x16x64_i8 v[2:5], v[160:163], v[220:223], v[2:5]
	v_mfma_i32_16x16x64_i8 v[62:65], v[156:159], v[200:203], v[62:65]
	v_mfma_i32_16x16x64_i8 v[58:61], v[164:167], v[200:203], v[58:61]
	v_mfma_i32_16x16x64_i8 v[46:49], v[156:159], v[208:211], v[46:49]
	v_mfma_i32_16x16x64_i8 v[42:45], v[164:167], v[208:211], v[42:45]
	v_mfma_i32_16x16x64_i8 v[30:33], v[156:159], v[216:219], v[30:33]
	v_mfma_i32_16x16x64_i8 v[26:29], v[164:167], v[216:219], v[26:29]
	v_mfma_i32_16x16x64_i8 v[6:9], v[156:159], v[224:227], v[6:9]
	v_mfma_i32_16x16x64_i8 v[2:5], v[164:167], v[224:227], v[2:5]
	v_mfma_i32_16x16x64_i8 v[54:57], v[168:171], v[196:199], v[54:57]
	v_mfma_i32_16x16x64_i8 v[50:53], v[186:189], v[196:199], v[50:53]
	v_mfma_i32_16x16x64_i8 v[38:41], v[168:171], v[204:207], v[38:41]
	v_mfma_i32_16x16x64_i8 v[34:37], v[186:189], v[204:207], v[34:37]
	v_mfma_i32_16x16x64_i8 v[14:17], v[168:171], v[212:215], v[14:17]
	v_mfma_i32_16x16x64_i8 v[10:13], v[186:189], v[212:215], v[10:13]
	v_mfma_i32_16x16x64_i8 v[22:25], v[168:171], v[220:223], v[22:25]
	v_mfma_i32_16x16x64_i8 v[18:21], v[186:189], v[220:223], v[18:21]
	v_mfma_i32_16x16x64_i8 v[54:57], v[182:185], v[200:203], v[54:57]
	v_mfma_i32_16x16x64_i8 v[50:53], v[190:193], v[200:203], v[50:53]
	v_mfma_i32_16x16x64_i8 v[38:41], v[182:185], v[208:211], v[38:41]
	v_mfma_i32_16x16x64_i8 v[34:37], v[190:193], v[208:211], v[34:37]
	v_mfma_i32_16x16x64_i8 v[14:17], v[182:185], v[216:219], v[14:17]
	v_mfma_i32_16x16x64_i8 v[10:13], v[190:193], v[216:219], v[10:13]
	v_mfma_i32_16x16x64_i8 v[22:25], v[182:185], v[224:227], v[22:25]
	v_mfma_i32_16x16x64_i8 v[18:21], v[190:193], v[224:227], v[18:21]
	s_barrier
	s_add_i32 s67, s67, 2
	s_cmp_gt_u32 s67, 13
	s_mov_b64 s[36:37], s[38:39]
	s_cbranch_scc0 .LBB0_193
	s_and_b64 vcc, exec, s[20:21]
	s_cbranch_vccz .LBB0_196
	s_barrier

; #define PG8_STAGE(bufoff, gbase, voff) do { _Pragma("unroll") for (int _i = 0; _i < 2; ++_i) \
;         __builtin_amdgcn_global_load_lds((const unsigned*)((const char*)(gbase) + (voff)[_i]), (LAS unsigned*)(lds + (bufoff) + ldsw + _i * 8192), 16, 0, 0); } while (0)
; #define PG8_LDA(dst, b, h) do { _Pragma("unroll") for (int m = 0; m < 4; ++m) dst[m] = PG8_LD32(lds + PG8_SA(b, h) + aoff + m * 2048); } while (0)
; #define PG8_LDB(dst, b, h) do { _Pragma("unroll") for (int n = 0; n < 2; ++n) dst[n] = PG8_LD32(lds + PG8_SB(b, h) + boff + n * 2048); } while (0)
; #define PG8_WAIT_V(n) asm volatile("s_waitcnt vmcnt(" #n ")" ::: "memory")
; #define PG8_WAIT_L(n) asm volatile("s_waitcnt lgkmcnt(" #n ")" ::: "memory")
; #define PG8_BAR __builtin_amdgcn_s_barrier()
; #define PG8_SCHED __builtin_amdgcn_sched_barrier(0)
; #define PG8_STA(bufoff, nextflag, h, koff) do { if constexpr (Sched::GATHER) { unsigned _o[2]; _o[0] = (nextflag) ? nxtA[h][0] : curA[h][0]; _o[1] = (nextflag) ? nxtA[h][1] : curA[h][1]; PG8_STAGE(bufoff, Ab + (koff), _o); } \
;         else { PG8_STAGE(bufoff, ((nextflag) ? nA : cA) + (size_t)(h) * hstep + (koff), voffA); } } while (0)
; template <class Epi, class Sched, bool ALIGN_EPI, int DT>
; __device__ __forceinline__ void gemm_phase(LAS unsigned char* lds, const int KB, const Sched& S, const Epi& E) {
;     ...
;             const size_t k1 = (size_t)(t + 1) * kstep, k2 = last ? 0 : (size_t)(t + 2) * kstep, k3 = k2 + kstep;
;             const char* b2 = last ? nB : cB + (size_t)(t + 2) * kstep; const char* b3 = b2 + kstep;
;             PG8_LDB(B0, 0, 0); PG8_LDB(B1, 0, 1); PG8_SCHED; PG8_LDA(At, 0, 0); PG8_STA(PG8_SA(1, 1), false, 1, k1);
;             PG8_WAIT_V(8); PG8_WAIT_L(0); PG8_BAR; PG8_MMA(0, 0, At, B0); PG8_MMA(0, 1, At, B1); PG8_BAR; PG8_SCHED;
;             PG8_LDA(At, 0, 1); PG8_STAGE(PG8_SB(0, 0), b2, voffB); PG8_STAGE(PG8_SB(0, 1), b2 + hstep, voffB); PG8_STA(PG8_SA(0, 0), last, 0, k2);
;             PG8_WAIT_V(8); PG8_WAIT_L(0); PG8_BAR; PG8_MMA(1, 0, At, B0); PG8_MMA(1, 1, At, B1); PG8_BAR; PG8_SCHED;
.LBB0_1018:
	ds_read_b128 v[18:21], v193
	ds_read_b128 v[22:25], v193 offset:1024
	ds_read_b128 v[26:29], v193 offset:2048
	ds_read_b128 v[30:33], v193 offset:3072
	ds_read_b128 v[2:5], v195
	ds_read_b128 v[6:9], v195 offset:1024
	ds_read_b128 v[10:13], v195 offset:2048
	ds_read_b128 v[14:17], v195 offset:3072
	s_add_u32 s34, s38, 0x100
	s_addc_u32 s35, s39, 0
	s_add_u32 s68, s63, s38
	s_addc_u32 s69, s66, s39
	s_cmp_eq_u32 s67, 12
	s_cselect_b64 s[40:41], -1, 0
	s_and_b64 s[36:37], s[40:41], exec
	s_cselect_b32 s37, s21, s69
	s_cselect_b32 s36, s23, s68
	s_cselect_b32 s68, 0, s35
	s_cselect_b32 s69, 0, s34
	v_lshl_add_u64 v[222:223], v[178:179], 0, s[38:39]
	s_add_i32 m0, s29, 0xc000
	ds_read_b128 v[182:185], v196
	ds_read_b128 v[186:189], v196 offset:1024
	ds_read_b128 v[198:201], v196 offset:2048
	ds_read_b128 v[202:205], v196 offset:3072
	ds_read_b128 v[206:209], v196 offset:4096
	ds_read_b128 v[210:213], v196 offset:5120
	ds_read_b128 v[214:217], v196 offset:6144
	ds_read_b128 v[218:221], v196 offset:7168
	global_load_lds_dwordx4 v[222:223], off
	v_lshl_add_u64 v[222:223], v[180:181], 0, s[38:39]
	s_add_i32 m0, s29, 0xe000
	s_nop 0
	global_load_lds_dwordx4 v[222:223], off
	s_waitcnt vmcnt(8)
	s_waitcnt lgkmcnt(0)
	s_barrier
	v_mfma_scale_f32_16x16x128_f8f6f4 v[158:161], v[18:25], v[182:189], v[158:161], v190, v190 op_sel_hi:[0,0,0]
	v_mfma_scale_f32_16x16x128_f8f6f4 v[154:157], v[26:33], v[182:189], v[154:157], v190, v190 op_sel_hi:[0,0,0]
	v_mfma_scale_f32_16x16x128_f8f6f4 v[150:153], v[18:25], v[198:205], v[150:153], v190, v190 op_sel_hi:[0,0,0]
	v_mfma_scale_f32_16x16x128_f8f6f4 v[142:145], v[26:33], v[198:205], v[142:145], v190, v190 op_sel_hi:[0,0,0]
	v_mfma_scale_f32_16x16x128_f8f6f4 v[134:137], v[18:25], v[206:213], v[134:137], v190, v190 op_sel_hi:[0,0,0]
	v_mfma_scale_f32_16x16x128_f8f6f4 v[126:129], v[26:33], v[206:213], v[126:129], v190, v190 op_sel_hi:[0,0,0]
	v_mfma_scale_f32_16x16x128_f8f6f4 v[118:121], v[18:25], v[214:221], v[118:121], v190, v190 op_sel_hi:[0,0,0]
	v_mfma_scale_f32_16x16x128_f8f6f4 v[110:113], v[26:33], v[214:221], v[110:113], v190, v190 op_sel_hi:[0,0,0]
	v_mfma_scale_f32_16x16x128_f8f6f4 v[146:149], v[2:9], v[182:189], v[146:149], v190, v190 op_sel_hi:[0,0,0]
	v_mfma_scale_f32_16x16x128_f8f6f4 v[138:141], v[10:17], v[182:189], v[138:141], v190, v190 op_sel_hi:[0,0,0]
	v_mfma_scale_f32_16x16x128_f8f6f4 v[130:133], v[2:9], v[198:205], v[130:133], v190, v190 op_sel_hi:[0,0,0]
	v_mfma_scale_f32_16x16x128_f8f6f4 v[122:125], v[10:17], v[198:205], v[122:125], v190, v190 op_sel_hi:[0,0,0]
	v_mfma_scale_f32_16x16x128_f8f6f4 v[114:117], v[2:9], v[206:213], v[114:117], v190, v190 op_sel_hi:[0,0,0]
	v_mfma_scale_f32_16x16x128_f8f6f4 v[106:109], v[10:17], v[206:213], v[106:109], v190, v190 op_sel_hi:[0,0,0]
	v_mfma_scale_f32_16x16x128_f8f6f4 v[102:105], v[2:9], v[214:221], v[102:105], v190, v190 op_sel_hi:[0,0,0]
	v_mfma_scale_f32_16x16x128_f8f6f4 v[98:101], v[10:17], v[214:221], v[98:101], v190, v190 op_sel_hi:[0,0,0]
	s_barrier
	s_add_i32 s38, s53, s42
	v_lshl_add_u64 v[182:183], s[36:37], 0, v[162:163]
	s_mov_b32 m0, s38
	ds_read_b128 v[198:201], v196 offset:16384
	ds_read_b128 v[202:205], v196 offset:17408
	ds_read_b128 v[206:209], v196 offset:18432
	ds_read_b128 v[210:213], v196 offset:19456
	ds_read_b128 v[214:217], v196 offset:20480
	ds_read_b128 v[218:221], v196 offset:21504
	ds_read_b128 v[222:225], v196 offset:22528
	ds_read_b128 v[226:229], v196 offset:23552
	global_load_lds_dwordx4 v[182:183], off
	s_add_i32 m0, s38, 0x2000
	s_add_u32 s38, s36, 0x40000
	v_lshl_add_u64 v[184:185], s[36:37], 0, v[164:165]
	s_addc_u32 s39, s37, 0
	s_add_i32 s70, s54, s42
	global_load_lds_dwordx4 v[184:185], off
	v_lshl_add_u64 v[186:187], s[38:39], 0, v[162:163]
	s_mov_b32 m0, s70
	s_nop 0
	global_load_lds_dwordx4 v[186:187], off
	v_lshl_add_u64 v[186:187], s[38:39], 0, v[164:165]
	s_add_i32 m0, s70, 0x2000
	s_and_b64 s[38:39], s[6:7], s[40:41]
	s_and_b64 s[38:39], s[38:39], exec
	s_cselect_b32 s38, s24, s30
	s_cselect_b32 s39, s25, s31
	s_add_u32 s38, s38, s69
	s_addc_u32 s39, s39, s68
	global_load_lds_dwordx4 v[186:187], off
	v_lshl_add_u64 v[186:187], s[38:39], 0, v[166:167]
	s_mov_b32 m0, s29
	v_lshl_add_u64 v[188:189], s[38:39], 0, v[168:169]
	global_load_lds_dwordx4 v[186:187], off
	s_mov_b32 m0, s43
	s_nop 0
	global_load_lds_dwordx4 v[188:189], off
	s_waitcnt vmcnt(8)
	s_waitcnt lgkmcnt(0)
	s_barrier
	v_mfma_scale_f32_16x16x128_f8f6f4 v[94:97], v[18:25], v[198:205], v[94:97], v190, v190 op_sel_hi:[0,0,0]
	v_mfma_scale_f32_16x16x128_f8f6f4 v[90:93], v[26:33], v[198:205], v[90:93], v190, v190 op_sel_hi:[0,0,0]
	v_mfma_scale_f32_16x16x128_f8f6f4 v[86:89], v[18:25], v[206:213], v[86:89], v190, v190 op_sel_hi:[0,0,0]
	v_mfma_scale_f32_16x16x128_f8f6f4 v[78:81], v[26:33], v[206:213], v[78:81], v190, v190 op_sel_hi:[0,0,0]
	v_mfma_scale_f32_16x16x128_f8f6f4 v[62:65], v[18:25], v[214:221], v[62:65], v190, v190 op_sel_hi:[0,0,0]
	v_mfma_scale_f32_16x16x128_f8f6f4 v[54:57], v[26:33], v[214:221], v[54:57], v190, v190 op_sel_hi:[0,0,0]
	v_mfma_scale_f32_16x16x128_f8f6f4 v[46:49], v[18:25], v[222:229], v[46:49], v190, v190 op_sel_hi:[0,0,0]
	v_mfma_scale_f32_16x16x128_f8f6f4 v[38:41], v[26:33], v[222:229], v[38:41], v190, v190 op_sel_hi:[0,0,0]
	v_mfma_scale_f32_16x16x128_f8f6f4 v[82:85], v[2:9], v[198:205], v[82:85], v190, v190 op_sel_hi:[0,0,0]
	v_mfma_scale_f32_16x16x128_f8f6f4 v[74:77], v[10:17], v[198:205], v[74:77], v190, v190 op_sel_hi:[0,0,0]
	v_mfma_scale_f32_16x16x128_f8f6f4 v[58:61], v[2:9], v[206:213], v[58:61], v190, v190 op_sel_hi:[0,0,0]
	v_mfma_scale_f32_16x16x128_f8f6f4 v[50:53], v[10:17], v[206:213], v[50:53], v190, v190 op_sel_hi:[0,0,0]
	v_mfma_scale_f32_16x16x128_f8f6f4 v[42:45], v[2:9], v[214:221], v[42:45], v190, v190 op_sel_hi:[0,0,0]
	v_mfma_scale_f32_16x16x128_f8f6f4 v[34:37], v[10:17], v[214:221], v[34:37], v190, v190 op_sel_hi:[0,0,0]
	v_mfma_scale_f32_16x16x128_f8f6f4 v[70:73], v[2:9], v[222:229], v[70:73], v190, v190 op_sel_hi:[0,0,0]
	v_mfma_scale_f32_16x16x128_f8f6f4 v[66:69], v[10:17], v[222:229], v[66:69], v190, v190 op_sel_hi:[0,0,0]
	s_barrier
; #define PG8_STAGE(bufoff, gbase, voff) do { _Pragma("unroll") for (int _i = 0; _i < 2; ++_i) \
;         __builtin_amdgcn_global_load_lds((const unsigned*)((const char*)(gbase) + (voff)[_i]), (LAS unsigned*)(lds + (bufoff) + ldsw + _i * 8192), 16, 0, 0); } while (0)
; #define PG8_LDA(dst, b, h) do { _Pragma("unroll") for (int m = 0; m < 4; ++m) dst[m] = PG8_LD32(lds + PG8_SA(b, h) + aoff + m * 2048); } while (0)
; #define PG8_LDB(dst, b, h) do { _Pragma("unroll") for (int n = 0; n < 2; ++n) dst[n] = PG8_LD32(lds + PG8_SB(b, h) + boff + n * 2048); } while (0)
; #define PG8_WAIT_V(n) asm volatile("s_waitcnt vmcnt(" #n ")" ::: "memory")
; #define PG8_WAIT_L(n) asm volatile("s_waitcnt lgkmcnt(" #n ")" ::: "memory")
; #define PG8_BAR __builtin_amdgcn_s_barrier()
; #define PG8_SCHED __builtin_amdgcn_sched_barrier(0)
; #define PG8_STA(bufoff, nextflag, h, koff) do { if constexpr (Sched::GATHER) { unsigned _o[2]; _o[0] = (nextflag) ? nxtA[h][0] : curA[h][0]; _o[1] = (nextflag) ? nxtA[h][1] : curA[h][1]; PG8_STAGE(bufoff, Ab + (koff), _o); } \
;         else { PG8_STAGE(bufoff, ((nextflag) ? nA : cA) + (size_t)(h) * hstep + (koff), voffA); } } while (0)
; template <class Epi, class Sched, bool ALIGN_EPI, int DT>
; __device__ __forceinline__ void gemm_phase(LAS unsigned char* lds, const int KB, const Sched& S, const Epi& E) {
;     ...
;             PG8_LDB(B0, 1, 0); PG8_LDB(B1, 1, 1); PG8_SCHED; PG8_LDA(At, 1, 0); PG8_STA(PG8_SA(0, 1), last, 1, k2);
;             PG8_WAIT_V(8); PG8_WAIT_L(0); PG8_BAR; PG8_MMA(0, 0, At, B0); PG8_MMA(0, 1, At, B1); PG8_BAR; PG8_SCHED;
;             PG8_LDA(At, 1, 1); PG8_STAGE(PG8_SB(1, 0), b3, voffB); PG8_STAGE(PG8_SB(1, 1), b3 + hstep, voffB); PG8_STA(PG8_SA(1, 0), last, 0, k3);
;             PG8_WAIT_V(8); PG8_WAIT_L(0); PG8_BAR; PG8_MMA(1, 0, At, B0); PG8_MMA(1, 1, At, B1); PG8_BAR; PG8_SCHED;
;         }
	s_add_i32 s40, 0, 0x18000
	s_add_i32 s41, 0, 0x1c000
	v_add_u32_e32 v14, s40, v191
	v_add_u32_e32 v30, s41, v191
	ds_read_b128 v[2:5], v14
	ds_read_b128 v[6:9], v14 offset:1024
	ds_read_b128 v[10:13], v14 offset:2048
	ds_read_b128 v[14:17], v14 offset:3072
	ds_read_b128 v[18:21], v30
	ds_read_b128 v[22:25], v30 offset:1024
	ds_read_b128 v[26:29], v30 offset:2048
	ds_read_b128 v[30:33], v30 offset:3072
	s_add_u32 s38, s38, 0x40000
	s_addc_u32 s39, s39, 0
	s_mov_b32 m0, s44
	v_lshl_add_u64 v[230:231], s[38:39], 0, v[166:167]
	ds_read_b128 v[198:201], v196 offset:32768
	ds_read_b128 v[202:205], v196 offset:33792
	ds_read_b128 v[206:209], v196 offset:34816
	ds_read_b128 v[210:213], v196 offset:35840
	ds_read_b128 v[214:217], v196 offset:36864
	ds_read_b128 v[218:221], v196 offset:37888
	ds_read_b128 v[222:225], v196 offset:38912
	ds_read_b128 v[226:229], v196 offset:39936
	global_load_lds_dwordx4 v[230:231], off
	v_lshl_add_u64 v[230:231], s[38:39], 0, v[168:169]
	s_mov_b32 m0, s45
	s_nop 0
	global_load_lds_dwordx4 v[230:231], off
	s_waitcnt vmcnt(8)
	s_waitcnt lgkmcnt(0)
	s_barrier
	v_mfma_scale_f32_16x16x128_f8f6f4 v[158:161], v[2:9], v[198:205], v[158:161], v190, v190 op_sel_hi:[0,0,0]
	v_mfma_scale_f32_16x16x128_f8f6f4 v[154:157], v[10:17], v[198:205], v[154:157], v190, v190 op_sel_hi:[0,0,0]
	v_mfma_scale_f32_16x16x128_f8f6f4 v[150:153], v[2:9], v[206:213], v[150:153], v190, v190 op_sel_hi:[0,0,0]
	v_mfma_scale_f32_16x16x128_f8f6f4 v[142:145], v[10:17], v[206:213], v[142:145], v190, v190 op_sel_hi:[0,0,0]
	v_mfma_scale_f32_16x16x128_f8f6f4 v[134:137], v[2:9], v[214:221], v[134:137], v190, v190 op_sel_hi:[0,0,0]
	v_mfma_scale_f32_16x16x128_f8f6f4 v[126:129], v[10:17], v[214:221], v[126:129], v190, v190 op_sel_hi:[0,0,0]
	v_mfma_scale_f32_16x16x128_f8f6f4 v[118:121], v[2:9], v[222:229], v[118:121], v190, v190 op_sel_hi:[0,0,0]
	v_mfma_scale_f32_16x16x128_f8f6f4 v[110:113], v[10:17], v[222:229], v[110:113], v190, v190 op_sel_hi:[0,0,0]
	v_mfma_scale_f32_16x16x128_f8f6f4 v[146:149], v[18:25], v[198:205], v[146:149], v190, v190 op_sel_hi:[0,0,0]
	v_mfma_scale_f32_16x16x128_f8f6f4 v[138:141], v[26:33], v[198:205], v[138:141], v190, v190 op_sel_hi:[0,0,0]
	v_mfma_scale_f32_16x16x128_f8f6f4 v[130:133], v[18:25], v[206:213], v[130:133], v190, v190 op_sel_hi:[0,0,0]
	v_mfma_scale_f32_16x16x128_f8f6f4 v[122:125], v[26:33], v[206:213], v[122:125], v190, v190 op_sel_hi:[0,0,0]
	v_mfma_scale_f32_16x16x128_f8f6f4 v[114:117], v[18:25], v[214:221], v[114:117], v190, v190 op_sel_hi:[0,0,0]
	v_mfma_scale_f32_16x16x128_f8f6f4 v[106:109], v[26:33], v[214:221], v[106:109], v190, v190 op_sel_hi:[0,0,0]
	v_mfma_scale_f32_16x16x128_f8f6f4 v[102:105], v[18:25], v[222:229], v[102:105], v190, v190 op_sel_hi:[0,0,0]
	v_mfma_scale_f32_16x16x128_f8f6f4 v[98:101], v[26:33], v[222:229], v[98:101], v190, v190 op_sel_hi:[0,0,0]
	s_barrier
	s_add_i32 s38, s40, s42
	v_lshl_add_u64 v[182:183], v[182:183], 0, s[10:11]
	s_mov_b32 m0, s38
	ds_read_b128 v[198:201], v196 offset:49152
	ds_read_b128 v[202:205], v196 offset:50176
	ds_read_b128 v[206:209], v196 offset:51200
	ds_read_b128 v[210:213], v196 offset:52224
	ds_read_b128 v[214:217], v196 offset:53248
	ds_read_b128 v[218:221], v196 offset:54272
	ds_read_b128 v[222:225], v196 offset:55296
	ds_read_b128 v[226:229], v196 offset:56320
	global_load_lds_dwordx4 v[182:183], off
	s_add_i32 m0, s38, 0x2000
	s_add_u32 s36, s36, 0x40080
	v_lshl_add_u64 v[182:183], v[184:185], 0, s[10:11]
	s_addc_u32 s37, s37, 0
	s_add_i32 s38, s41, s42
	global_load_lds_dwordx4 v[182:183], off
	v_lshl_add_u64 v[182:183], s[36:37], 0, v[162:163]
	s_mov_b32 m0, s38
	s_nop 0
	global_load_lds_dwordx4 v[182:183], off
	v_lshl_add_u64 v[182:183], s[36:37], 0, v[164:165]
	s_add_i32 m0, s38, 0x2000
	s_nop 0
	global_load_lds_dwordx4 v[182:183], off
	v_lshl_add_u64 v[182:183], v[186:187], 0, s[10:11]
	s_mov_b32 m0, s47
	s_nop 0
	global_load_lds_dwordx4 v[182:183], off
	v_lshl_add_u64 v[182:183], v[188:189], 0, s[10:11]
	s_mov_b32 m0, s49
	s_nop 0
	global_load_lds_dwordx4 v[182:183], off
	s_waitcnt vmcnt(8)
	s_waitcnt lgkmcnt(0)
	s_barrier
	v_mfma_scale_f32_16x16x128_f8f6f4 v[94:97], v[2:9], v[198:205], v[94:97], v190, v190 op_sel_hi:[0,0,0]
	v_mfma_scale_f32_16x16x128_f8f6f4 v[90:93], v[10:17], v[198:205], v[90:93], v190, v190 op_sel_hi:[0,0,0]
	v_mfma_scale_f32_16x16x128_f8f6f4 v[86:89], v[2:9], v[206:213], v[86:89], v190, v190 op_sel_hi:[0,0,0]
	v_mfma_scale_f32_16x16x128_f8f6f4 v[78:81], v[10:17], v[206:213], v[78:81], v190, v190 op_sel_hi:[0,0,0]
	v_mfma_scale_f32_16x16x128_f8f6f4 v[62:65], v[2:9], v[214:221], v[62:65], v190, v190 op_sel_hi:[0,0,0]
	v_mfma_scale_f32_16x16x128_f8f6f4 v[54:57], v[10:17], v[214:221], v[54:57], v190, v190 op_sel_hi:[0,0,0]
	v_mfma_scale_f32_16x16x128_f8f6f4 v[46:49], v[2:9], v[222:229], v[46:49], v190, v190 op_sel_hi:[0,0,0]
	v_mfma_scale_f32_16x16x128_f8f6f4 v[38:41], v[10:17], v[222:229], v[38:41], v190, v190 op_sel_hi:[0,0,0]
	v_mfma_scale_f32_16x16x128_f8f6f4 v[82:85], v[18:25], v[198:205], v[82:85], v190, v190 op_sel_hi:[0,0,0]
	v_mfma_scale_f32_16x16x128_f8f6f4 v[74:77], v[26:33], v[198:205], v[74:77], v190, v190 op_sel_hi:[0,0,0]
	v_mfma_scale_f32_16x16x128_f8f6f4 v[58:61], v[18:25], v[206:213], v[58:61], v190, v190 op_sel_hi:[0,0,0]
	v_mfma_scale_f32_16x16x128_f8f6f4 v[50:53], v[26:33], v[206:213], v[50:53], v190, v190 op_sel_hi:[0,0,0]
	v_mfma_scale_f32_16x16x128_f8f6f4 v[42:45], v[18:25], v[214:221], v[42:45], v190, v190 op_sel_hi:[0,0,0]
	v_mfma_scale_f32_16x16x128_f8f6f4 v[34:37], v[26:33], v[214:221], v[34:37], v190, v190 op_sel_hi:[0,0,0]
	v_mfma_scale_f32_16x16x128_f8f6f4 v[70:73], v[18:25], v[222:229], v[70:73], v190, v190 op_sel_hi:[0,0,0]
	v_mfma_scale_f32_16x16x128_f8f6f4 v[66:69], v[26:33], v[222:229], v[66:69], v190, v190 op_sel_hi:[0,0,0]
	s_barrier
	s_add_i32 s67, s67, 2
	s_cmp_gt_u32 s67, 13
	s_mov_b64 s[38:39], s[34:35]
	s_cbranch_scc0 .LBB0_1018
	s_and_b64 vcc, exec, s[12:13]
	s_cbranch_vccz .LBB0_1021
	s_barrier

; #define PG8_STAGE(bufoff, gbase, voff) do { _Pragma("unroll") for (int _i = 0; _i < 2; ++_i) \
;         __builtin_amdgcn_global_load_lds((const unsigned*)((const char*)(gbase) + (voff)[_i]), (LAS unsigned*)(lds + (bufoff) + ldsw + _i * 8192), 16, 0, 0); } while (0)
; #define PG8_LDA(dst, b, h) do { _Pragma("unroll") for (int m = 0; m < 4; ++m) dst[m] = PG8_LD32(lds + PG8_SA(b, h) + aoff + m * 2048); } while (0)
; #define PG8_LDB(dst, b, h) do { _Pragma("unroll") for (int n = 0; n < 2; ++n) dst[n] = PG8_LD32(lds + PG8_SB(b, h) + boff + n * 2048); } while (0)
; #define PG8_WAIT_V(n) asm volatile("s_waitcnt vmcnt(" #n ")" ::: "memory")
; #define PG8_WAIT_L(n) asm volatile("s_waitcnt lgkmcnt(" #n ")" ::: "memory")
; #define PG8_BAR __builtin_amdgcn_s_barrier()
; #define PG8_SCHED __builtin_amdgcn_sched_barrier(0)
; #define PG8_STA(bufoff, nextflag, h, koff) do { if constexpr (Sched::GATHER) { unsigned _o[2]; _o[0] = (nextflag) ? nxtA[h][0] : curA[h][0]; _o[1] = (nextflag) ? nxtA[h][1] : curA[h][1]; PG8_STAGE(bufoff, Ab + (koff), _o); } \
;         else { PG8_STAGE(bufoff, ((nextflag) ? nA : cA) + (size_t)(h) * hstep + (koff), voffA); } } while (0)
; template <class Epi, class Sched, bool ALIGN_EPI, int DT>
; __device__ __forceinline__ void gemm_phase(LAS unsigned char* lds, const int KB, const Sched& S, const Epi& E) {
;     ...
;             const size_t k1 = (size_t)(t + 1) * kstep, k2 = last ? 0 : (size_t)(t + 2) * kstep, k3 = k2 + kstep;
;             const char* b2 = last ? nB : cB + (size_t)(t + 2) * kstep; const char* b3 = b2 + kstep;
;             PG8_LDB(B0, 0, 0); PG8_LDB(B1, 0, 1); PG8_SCHED; PG8_LDA(At, 0, 0); PG8_STA(PG8_SA(1, 1), false, 1, k1);
;             PG8_WAIT_V(8); PG8_WAIT_L(0); PG8_BAR; PG8_MMA(0, 0, At, B0); PG8_MMA(0, 1, At, B1); PG8_BAR; PG8_SCHED;
;             PG8_LDA(At, 0, 1); PG8_STAGE(PG8_SB(0, 0), b2, voffB); PG8_STAGE(PG8_SB(0, 1), b2 + hstep, voffB); PG8_STA(PG8_SA(0, 0), last, 0, k2);
;             PG8_WAIT_V(8); PG8_WAIT_L(0); PG8_BAR; PG8_MMA(1, 0, At, B0); PG8_MMA(1, 1, At, B1); PG8_BAR; PG8_SCHED;
.LBB0_1154:
	ds_read_b128 v[70:73], v167
	ds_read_b128 v[156:159], v167 offset:1024
	ds_read_b128 v[160:163], v167 offset:2048
	ds_read_b128 v[172:175], v167 offset:3072
	ds_read_b128 v[176:179], v168
	ds_read_b128 v[180:183], v168 offset:1024
	ds_read_b128 v[184:187], v168 offset:2048
	ds_read_b128 v[188:191], v168 offset:3072
	s_add_u32 s30, s28, 0x100
	s_addc_u32 s31, s29, 0
	s_add_u32 s63, s56, s28
	s_addc_u32 s66, s57, s29
	s_cmp_eq_u32 s62, 12
	s_cselect_b64 s[36:37], -1, 0
	s_and_b64 s[34:35], s[36:37], exec
	s_cselect_b32 s67, 0, s30
	s_cselect_b32 s35, s17, s66
	s_cselect_b32 s34, s19, s63
	v_lshl_add_u64 v[192:193], v[66:67], 0, s[28:29]
	s_add_i32 m0, s25, 0xc000
	ds_read_b128 v[196:199], v169
	ds_read_b128 v[200:203], v169 offset:1024
	ds_read_b128 v[204:207], v169 offset:2048
	ds_read_b128 v[208:211], v169 offset:3072
	ds_read_b128 v[212:215], v169 offset:4096
	ds_read_b128 v[216:219], v169 offset:5120
	ds_read_b128 v[220:223], v169 offset:6144
	ds_read_b128 v[224:227], v169 offset:7168
	global_load_lds_dwordx4 v[192:193], off
	v_lshl_add_u64 v[192:193], v[68:69], 0, s[28:29]
	s_add_i32 m0, s25, 0xe000
	s_nop 0
	global_load_lds_dwordx4 v[192:193], off
	s_waitcnt vmcnt(8)
	s_waitcnt lgkmcnt(0)
	s_barrier
	v_mfma_i32_16x16x64_i8 v[134:137], v[70:73], v[196:199], v[134:137]
	v_mfma_i32_16x16x64_i8 v[126:129], v[160:163], v[196:199], v[126:129]
	v_mfma_i32_16x16x64_i8 v[118:121], v[70:73], v[204:207], v[118:121]
	v_mfma_i32_16x16x64_i8 v[110:113], v[160:163], v[204:207], v[110:113]
	v_mfma_i32_16x16x64_i8 v[102:105], v[70:73], v[212:215], v[102:105]
	v_mfma_i32_16x16x64_i8 v[94:97], v[160:163], v[212:215], v[94:97]
	v_mfma_i32_16x16x64_i8 v[86:89], v[70:73], v[220:223], v[86:89]
	v_mfma_i32_16x16x64_i8 v[78:81], v[160:163], v[220:223], v[78:81]
	v_mfma_i32_16x16x64_i8 v[134:137], v[156:159], v[200:203], v[134:137]
	v_mfma_i32_16x16x64_i8 v[126:129], v[172:175], v[200:203], v[126:129]
	v_mfma_i32_16x16x64_i8 v[118:121], v[156:159], v[208:211], v[118:121]
	v_mfma_i32_16x16x64_i8 v[110:113], v[172:175], v[208:211], v[110:113]
	v_mfma_i32_16x16x64_i8 v[102:105], v[156:159], v[216:219], v[102:105]
	v_mfma_i32_16x16x64_i8 v[94:97], v[172:175], v[216:219], v[94:97]
	v_mfma_i32_16x16x64_i8 v[86:89], v[156:159], v[224:227], v[86:89]
	v_mfma_i32_16x16x64_i8 v[78:81], v[172:175], v[224:227], v[78:81]
	v_mfma_i32_16x16x64_i8 v[130:133], v[176:179], v[196:199], v[130:133]
	v_mfma_i32_16x16x64_i8 v[122:125], v[184:187], v[196:199], v[122:125]
	v_mfma_i32_16x16x64_i8 v[114:117], v[176:179], v[204:207], v[114:117]
	v_mfma_i32_16x16x64_i8 v[106:109], v[184:187], v[204:207], v[106:109]
	v_mfma_i32_16x16x64_i8 v[98:101], v[176:179], v[212:215], v[98:101]
	v_mfma_i32_16x16x64_i8 v[90:93], v[184:187], v[212:215], v[90:93]
	v_mfma_i32_16x16x64_i8 v[82:85], v[176:179], v[220:223], v[82:85]
	v_mfma_i32_16x16x64_i8 v[74:77], v[184:187], v[220:223], v[74:77]
	v_mfma_i32_16x16x64_i8 v[130:133], v[180:183], v[200:203], v[130:133]
	v_mfma_i32_16x16x64_i8 v[122:125], v[188:191], v[200:203], v[122:125]
	v_mfma_i32_16x16x64_i8 v[114:117], v[180:183], v[208:211], v[114:117]
	v_mfma_i32_16x16x64_i8 v[106:109], v[188:191], v[208:211], v[106:109]
	v_mfma_i32_16x16x64_i8 v[98:101], v[180:183], v[216:219], v[98:101]
	v_mfma_i32_16x16x64_i8 v[90:93], v[188:191], v[216:219], v[90:93]
	v_mfma_i32_16x16x64_i8 v[82:85], v[180:183], v[224:227], v[82:85]
	v_mfma_i32_16x16x64_i8 v[74:77], v[188:191], v[224:227], v[74:77]
	s_barrier
	s_add_i32 s28, s49, s38
	v_lshl_add_u64 v[192:193], s[34:35], 0, v[140:141]
	s_mov_b32 m0, s28
	ds_read_b128 v[196:199], v169 offset:16384
	ds_read_b128 v[200:203], v169 offset:17408
	ds_read_b128 v[204:207], v169 offset:18432
	ds_read_b128 v[208:211], v169 offset:19456
	ds_read_b128 v[212:215], v169 offset:20480
	ds_read_b128 v[216:219], v169 offset:21504
	ds_read_b128 v[220:223], v169 offset:22528
	ds_read_b128 v[224:227], v169 offset:23552
	global_load_lds_dwordx4 v[192:193], off
	s_add_i32 m0, s28, 0x2000
	s_add_u32 s28, s34, 0x40000
	v_lshl_add_u64 v[228:229], s[34:35], 0, v[138:139]
	s_addc_u32 s29, s35, 0
	s_add_i32 s63, s52, s38
	global_load_lds_dwordx4 v[228:229], off
	v_lshl_add_u64 v[230:231], s[28:29], 0, v[140:141]
	s_mov_b32 m0, s63
	s_nop 0
	global_load_lds_dwordx4 v[230:231], off
	v_lshl_add_u64 v[230:231], s[28:29], 0, v[138:139]
	s_add_i32 m0, s63, 0x2000
	s_and_b64 s[28:29], s[6:7], s[36:37]
	s_and_b64 s[28:29], s[28:29], exec
	s_cselect_b32 s28, s20, s26
	s_cselect_b32 s29, s21, s27
	s_add_u32 s28, s28, s67
	s_addc_u32 s29, s29, 0
	global_load_lds_dwordx4 v[230:231], off
	v_lshl_add_u64 v[230:231], s[28:29], 0, v[142:143]
	s_mov_b32 m0, s25
	v_lshl_add_u64 v[232:233], s[28:29], 0, v[144:145]
	global_load_lds_dwordx4 v[230:231], off
	s_mov_b32 m0, s41
	s_nop 0
	global_load_lds_dwordx4 v[232:233], off
	s_waitcnt vmcnt(8)
	s_waitcnt lgkmcnt(0)
	s_barrier
; #define PG8_LDA(dst, b, h) do { _Pragma("unroll") for (int m = 0; m < 4; ++m) dst[m] = PG8_LD32(lds + PG8_SA(b, h) + aoff + m * 2048); } while (0)
; #define PG8_LDB(dst, b, h) do { _Pragma("unroll") for (int n = 0; n < 2; ++n) dst[n] = PG8_LD32(lds + PG8_SB(b, h) + boff + n * 2048); } while (0)
; #define PG8_WAIT_V(n) asm volatile("s_waitcnt vmcnt(" #n ")" ::: "memory")
; #define PG8_WAIT_L(n) asm volatile("s_waitcnt lgkmcnt(" #n ")" ::: "memory")
; #define PG8_BAR __builtin_amdgcn_s_barrier()
; #define PG8_SCHED __builtin_amdgcn_sched_barrier(0)
; #define PG8_STA(bufoff, nextflag, h, koff) do { if constexpr (Sched::GATHER) { unsigned _o[2]; _o[0] = (nextflag) ? nxtA[h][0] : curA[h][0]; _o[1] = (nextflag) ? nxtA[h][1] : curA[h][1]; PG8_STAGE(bufoff, Ab + (koff), _o); } \
;         else { PG8_STAGE(bufoff, ((nextflag) ? nA : cA) + (size_t)(h) * hstep + (koff), voffA); } } while (0)
; template <class Epi, class Sched, bool ALIGN_EPI, int DT>
; __device__ __forceinline__ void gemm_phase(LAS unsigned char* lds, const int KB, const Sched& S, const Epi& E) {
;     ...
;             PG8_WAIT_V(8); PG8_WAIT_L(0); PG8_BAR; PG8_MMA(1, 0, At, B0); PG8_MMA(1, 1, At, B1); PG8_BAR; PG8_SCHED;
;             PG8_LDB(B0, 1, 0); PG8_LDB(B1, 1, 1); PG8_SCHED; PG8_LDA(At, 1, 0); PG8_STA(PG8_SA(0, 1), last, 1, k2);
;             PG8_WAIT_V(8); PG8_WAIT_L(0); PG8_BAR; PG8_MMA(0, 0, At, B0); PG8_MMA(0, 1, At, B1); PG8_BAR; PG8_SCHED;
	v_mfma_i32_16x16x64_i8 v[62:65], v[70:73], v[196:199], v[62:65]
	v_mfma_i32_16x16x64_i8 v[54:57], v[160:163], v[196:199], v[54:57]
	v_mfma_i32_16x16x64_i8 v[46:49], v[70:73], v[204:207], v[46:49]
	v_mfma_i32_16x16x64_i8 v[38:41], v[160:163], v[204:207], v[38:41]
	v_mfma_i32_16x16x64_i8 v[30:33], v[70:73], v[212:215], v[30:33]
	v_mfma_i32_16x16x64_i8 v[22:25], v[160:163], v[212:215], v[22:25]
	v_mfma_i32_16x16x64_i8 v[6:9], v[70:73], v[220:223], v[6:9]
	v_mfma_i32_16x16x64_i8 v[2:5], v[160:163], v[220:223], v[2:5]
	v_mfma_i32_16x16x64_i8 v[62:65], v[156:159], v[200:203], v[62:65]
	v_mfma_i32_16x16x64_i8 v[54:57], v[172:175], v[200:203], v[54:57]
	v_mfma_i32_16x16x64_i8 v[46:49], v[156:159], v[208:211], v[46:49]
	v_mfma_i32_16x16x64_i8 v[38:41], v[172:175], v[208:211], v[38:41]
	v_mfma_i32_16x16x64_i8 v[30:33], v[156:159], v[216:219], v[30:33]
	v_mfma_i32_16x16x64_i8 v[22:25], v[172:175], v[216:219], v[22:25]
	v_mfma_i32_16x16x64_i8 v[6:9], v[156:159], v[224:227], v[6:9]
	v_mfma_i32_16x16x64_i8 v[2:5], v[172:175], v[224:227], v[2:5]
	v_mfma_i32_16x16x64_i8 v[58:61], v[176:179], v[196:199], v[58:61]
	v_mfma_i32_16x16x64_i8 v[50:53], v[184:187], v[196:199], v[50:53]
	v_mfma_i32_16x16x64_i8 v[42:45], v[176:179], v[204:207], v[42:45]
	v_mfma_i32_16x16x64_i8 v[34:37], v[184:187], v[204:207], v[34:37]
	v_mfma_i32_16x16x64_i8 v[26:29], v[176:179], v[212:215], v[26:29]
	v_mfma_i32_16x16x64_i8 v[18:21], v[184:187], v[212:215], v[18:21]
	v_mfma_i32_16x16x64_i8 v[14:17], v[176:179], v[220:223], v[14:17]
	v_mfma_i32_16x16x64_i8 v[10:13], v[184:187], v[220:223], v[10:13]
	v_mfma_i32_16x16x64_i8 v[58:61], v[180:183], v[200:203], v[58:61]
	v_mfma_i32_16x16x64_i8 v[50:53], v[188:191], v[200:203], v[50:53]
	v_mfma_i32_16x16x64_i8 v[42:45], v[180:183], v[208:211], v[42:45]
	v_mfma_i32_16x16x64_i8 v[34:37], v[188:191], v[208:211], v[34:37]
	v_mfma_i32_16x16x64_i8 v[26:29], v[180:183], v[216:219], v[26:29]
	v_mfma_i32_16x16x64_i8 v[18:21], v[188:191], v[216:219], v[18:21]
	v_mfma_i32_16x16x64_i8 v[14:17], v[180:183], v[224:227], v[14:17]
	v_mfma_i32_16x16x64_i8 v[10:13], v[188:191], v[224:227], v[10:13]
	s_barrier
	s_add_i32 s36, 0, 0x18000
	v_add_u32_e32 v1, s36, v165
	s_add_i32 s37, 0, 0x1c000
	ds_read_b128 v[70:73], v1
	ds_read_b128 v[156:159], v1 offset:1024
	ds_read_b128 v[160:163], v1 offset:2048
	ds_read_b128 v[172:175], v1 offset:3072
	v_add_u32_e32 v1, s37, v165
	ds_read_b128 v[176:179], v1
	ds_read_b128 v[180:183], v1 offset:1024
	ds_read_b128 v[184:187], v1 offset:2048
	ds_read_b128 v[188:191], v1 offset:3072
	s_add_u32 s28, s28, 0x40000
	s_addc_u32 s29, s29, 0
	s_mov_b32 m0, s42
	v_lshl_add_u64 v[234:235], s[28:29], 0, v[142:143]
	ds_read_b128 v[196:199], v169 offset:32768
	ds_read_b128 v[200:203], v169 offset:33792
	ds_read_b128 v[204:207], v169 offset:34816
	ds_read_b128 v[208:211], v169 offset:35840
	ds_read_b128 v[212:215], v169 offset:36864
	ds_read_b128 v[216:219], v169 offset:37888
	ds_read_b128 v[220:223], v169 offset:38912
	ds_read_b128 v[224:227], v169 offset:39936
	global_load_lds_dwordx4 v[234:235], off
	v_lshl_add_u64 v[234:235], s[28:29], 0, v[144:145]
	s_mov_b32 m0, s43
	s_nop 0
	global_load_lds_dwordx4 v[234:235], off
	s_waitcnt vmcnt(8)
	s_waitcnt lgkmcnt(0)
	s_barrier
	v_mfma_i32_16x16x64_i8 v[134:137], v[70:73], v[196:199], v[134:137]
	v_mfma_i32_16x16x64_i8 v[126:129], v[160:163], v[196:199], v[126:129]
	v_mfma_i32_16x16x64_i8 v[118:121], v[70:73], v[204:207], v[118:121]
	v_mfma_i32_16x16x64_i8 v[110:113], v[160:163], v[204:207], v[110:113]
	v_mfma_i32_16x16x64_i8 v[102:105], v[70:73], v[212:215], v[102:105]
	v_mfma_i32_16x16x64_i8 v[94:97], v[160:163], v[212:215], v[94:97]
	v_mfma_i32_16x16x64_i8 v[86:89], v[70:73], v[220:223], v[86:89]
	v_mfma_i32_16x16x64_i8 v[78:81], v[160:163], v[220:223], v[78:81]
	v_mfma_i32_16x16x64_i8 v[134:137], v[156:159], v[200:203], v[134:137]
	v_mfma_i32_16x16x64_i8 v[126:129], v[172:175], v[200:203], v[126:129]
	v_mfma_i32_16x16x64_i8 v[118:121], v[156:159], v[208:211], v[118:121]
	v_mfma_i32_16x16x64_i8 v[110:113], v[172:175], v[208:211], v[110:113]
	v_mfma_i32_16x16x64_i8 v[102:105], v[156:159], v[216:219], v[102:105]
	v_mfma_i32_16x16x64_i8 v[94:97], v[172:175], v[216:219], v[94:97]
	v_mfma_i32_16x16x64_i8 v[86:89], v[156:159], v[224:227], v[86:89]
	v_mfma_i32_16x16x64_i8 v[78:81], v[172:175], v[224:227], v[78:81]
	v_mfma_i32_16x16x64_i8 v[130:133], v[176:179], v[196:199], v[130:133]
	v_mfma_i32_16x16x64_i8 v[122:125], v[184:187], v[196:199], v[122:125]
	v_mfma_i32_16x16x64_i8 v[114:117], v[176:179], v[204:207], v[114:117]
	v_mfma_i32_16x16x64_i8 v[106:109], v[184:187], v[204:207], v[106:109]
	v_mfma_i32_16x16x64_i8 v[98:101], v[176:179], v[212:215], v[98:101]
	v_mfma_i32_16x16x64_i8 v[90:93], v[184:187], v[212:215], v[90:93]
	v_mfma_i32_16x16x64_i8 v[82:85], v[176:179], v[220:223], v[82:85]
	v_mfma_i32_16x16x64_i8 v[74:77], v[184:187], v[220:223], v[74:77]
	v_mfma_i32_16x16x64_i8 v[130:133], v[180:183], v[200:203], v[130:133]
	v_mfma_i32_16x16x64_i8 v[122:125], v[188:191], v[200:203], v[122:125]
	v_mfma_i32_16x16x64_i8 v[114:117], v[180:183], v[208:211], v[114:117]
	v_mfma_i32_16x16x64_i8 v[106:109], v[188:191], v[208:211], v[106:109]
	v_mfma_i32_16x16x64_i8 v[98:101], v[180:183], v[216:219], v[98:101]
	v_mfma_i32_16x16x64_i8 v[90:93], v[188:191], v[216:219], v[90:93]
	v_mfma_i32_16x16x64_i8 v[82:85], v[180:183], v[224:227], v[82:85]
	v_mfma_i32_16x16x64_i8 v[74:77], v[188:191], v[224:227], v[74:77]
	s_barrier
; #define PG8_STAGE(bufoff, gbase, voff) do { _Pragma("unroll") for (int _i = 0; _i < 2; ++_i) \
;         __builtin_amdgcn_global_load_lds((const unsigned*)((const char*)(gbase) + (voff)[_i]), (LAS unsigned*)(lds + (bufoff) + ldsw + _i * 8192), 16, 0, 0); } while (0)
; #define PG8_LDA(dst, b, h) do { _Pragma("unroll") for (int m = 0; m < 4; ++m) dst[m] = PG8_LD32(lds + PG8_SA(b, h) + aoff + m * 2048); } while (0)
; #define PG8_WAIT_V(n) asm volatile("s_waitcnt vmcnt(" #n ")" ::: "memory")
; #define PG8_WAIT_L(n) asm volatile("s_waitcnt lgkmcnt(" #n ")" ::: "memory")
; #define PG8_BAR __builtin_amdgcn_s_barrier()
; #define PG8_SCHED __builtin_amdgcn_sched_barrier(0)
; #define PG8_STA(bufoff, nextflag, h, koff) do { if constexpr (Sched::GATHER) { unsigned _o[2]; _o[0] = (nextflag) ? nxtA[h][0] : curA[h][0]; _o[1] = (nextflag) ? nxtA[h][1] : curA[h][1]; PG8_STAGE(bufoff, Ab + (koff), _o); } \
;         else { PG8_STAGE(bufoff, ((nextflag) ? nA : cA) + (size_t)(h) * hstep + (koff), voffA); } } while (0)
; template <class Epi, class Sched, bool ALIGN_EPI, int DT>
; __device__ __forceinline__ void gemm_phase(LAS unsigned char* lds, const int KB, const Sched& S, const Epi& E) {
;     ...
;             PG8_LDA(At, 1, 1); PG8_STAGE(PG8_SB(1, 0), b3, voffB); PG8_STAGE(PG8_SB(1, 1), b3 + hstep, voffB); PG8_STA(PG8_SA(1, 0), last, 0, k3);
;             PG8_WAIT_V(8); PG8_WAIT_L(0); PG8_BAR; PG8_MMA(1, 0, At, B0); PG8_MMA(1, 1, At, B1); PG8_BAR; PG8_SCHED;
;         }
	s_add_i32 s28, s36, s38
	v_lshl_add_u64 v[192:193], v[192:193], 0, s[12:13]
	s_mov_b32 m0, s28
	ds_read_b128 v[196:199], v169 offset:49152
	ds_read_b128 v[200:203], v169 offset:50176
	ds_read_b128 v[204:207], v169 offset:51200
	ds_read_b128 v[208:211], v169 offset:52224
	ds_read_b128 v[212:215], v169 offset:53248
	ds_read_b128 v[216:219], v169 offset:54272
	ds_read_b128 v[220:223], v169 offset:55296
	ds_read_b128 v[224:227], v169 offset:56320
	global_load_lds_dwordx4 v[192:193], off
	s_add_i32 m0, s28, 0x2000
	s_add_u32 s28, s34, 0x40080
	v_lshl_add_u64 v[192:193], v[228:229], 0, s[12:13]
	s_addc_u32 s29, s35, 0
	s_add_i32 s34, s37, s38
	global_load_lds_dwordx4 v[192:193], off
	v_lshl_add_u64 v[192:193], s[28:29], 0, v[140:141]
	s_mov_b32 m0, s34
	s_nop 0
	global_load_lds_dwordx4 v[192:193], off
	v_lshl_add_u64 v[192:193], s[28:29], 0, v[138:139]
	s_add_i32 m0, s34, 0x2000
	s_nop 0
	global_load_lds_dwordx4 v[192:193], off
	v_lshl_add_u64 v[192:193], v[230:231], 0, s[12:13]
	s_mov_b32 m0, s45
	s_nop 0
	global_load_lds_dwordx4 v[192:193], off
	v_lshl_add_u64 v[192:193], v[232:233], 0, s[12:13]
	s_mov_b32 m0, s46
	s_nop 0
	global_load_lds_dwordx4 v[192:193], off
	s_waitcnt vmcnt(8)
	s_waitcnt lgkmcnt(0)
	s_barrier
	v_mfma_i32_16x16x64_i8 v[62:65], v[70:73], v[196:199], v[62:65]
	v_mfma_i32_16x16x64_i8 v[54:57], v[160:163], v[196:199], v[54:57]
	v_mfma_i32_16x16x64_i8 v[46:49], v[70:73], v[204:207], v[46:49]
	v_mfma_i32_16x16x64_i8 v[38:41], v[160:163], v[204:207], v[38:41]
	v_mfma_i32_16x16x64_i8 v[30:33], v[70:73], v[212:215], v[30:33]
	v_mfma_i32_16x16x64_i8 v[22:25], v[160:163], v[212:215], v[22:25]
	v_mfma_i32_16x16x64_i8 v[6:9], v[70:73], v[220:223], v[6:9]
	v_mfma_i32_16x16x64_i8 v[2:5], v[160:163], v[220:223], v[2:5]
	v_mfma_i32_16x16x64_i8 v[62:65], v[156:159], v[200:203], v[62:65]
	v_mfma_i32_16x16x64_i8 v[54:57], v[172:175], v[200:203], v[54:57]
	v_mfma_i32_16x16x64_i8 v[46:49], v[156:159], v[208:211], v[46:49]
	v_mfma_i32_16x16x64_i8 v[38:41], v[172:175], v[208:211], v[38:41]
	v_mfma_i32_16x16x64_i8 v[30:33], v[156:159], v[216:219], v[30:33]
	v_mfma_i32_16x16x64_i8 v[22:25], v[172:175], v[216:219], v[22:25]
	v_mfma_i32_16x16x64_i8 v[6:9], v[156:159], v[224:227], v[6:9]
	v_mfma_i32_16x16x64_i8 v[2:5], v[172:175], v[224:227], v[2:5]
	v_mfma_i32_16x16x64_i8 v[58:61], v[176:179], v[196:199], v[58:61]
	v_mfma_i32_16x16x64_i8 v[50:53], v[184:187], v[196:199], v[50:53]
	v_mfma_i32_16x16x64_i8 v[42:45], v[176:179], v[204:207], v[42:45]
	v_mfma_i32_16x16x64_i8 v[34:37], v[184:187], v[204:207], v[34:37]
	v_mfma_i32_16x16x64_i8 v[26:29], v[176:179], v[212:215], v[26:29]
	v_mfma_i32_16x16x64_i8 v[18:21], v[184:187], v[212:215], v[18:21]
	v_mfma_i32_16x16x64_i8 v[14:17], v[176:179], v[220:223], v[14:17]
	v_mfma_i32_16x16x64_i8 v[10:13], v[184:187], v[220:223], v[10:13]
	v_mfma_i32_16x16x64_i8 v[58:61], v[180:183], v[200:203], v[58:61]
	v_mfma_i32_16x16x64_i8 v[50:53], v[188:191], v[200:203], v[50:53]
	v_mfma_i32_16x16x64_i8 v[42:45], v[180:183], v[208:211], v[42:45]
	v_mfma_i32_16x16x64_i8 v[34:37], v[188:191], v[208:211], v[34:37]
	v_mfma_i32_16x16x64_i8 v[26:29], v[180:183], v[216:219], v[26:29]
	v_mfma_i32_16x16x64_i8 v[18:21], v[188:191], v[216:219], v[18:21]
	v_mfma_i32_16x16x64_i8 v[14:17], v[180:183], v[224:227], v[14:17]
	v_mfma_i32_16x16x64_i8 v[10:13], v[188:191], v[224:227], v[10:13]
	s_barrier
	s_add_i32 s62, s62, 2
	s_cmp_gt_u32 s62, 13
	s_mov_b64 s[28:29], s[30:31]
	s_cbranch_scc0 .LBB0_1154
	s_and_b64 vcc, exec, s[14:15]
	s_cbranch_vccz .LBB0_1157
	s_barrier

; #define PG8_STAGE(bufoff, gbase, voff) do { _Pragma("unroll") for (int _i = 0; _i < 2; ++_i) \
;         __builtin_amdgcn_global_load_lds((const unsigned*)((const char*)(gbase) + (voff)[_i]), (LAS unsigned*)(lds + (bufoff) + ldsw + _i * 8192), 16, 0, 0); } while (0)
; #define PG8_LDA(dst, b, h) do { _Pragma("unroll") for (int m = 0; m < 4; ++m) dst[m] = PG8_LD32(lds + PG8_SA(b, h) + aoff + m * 2048); } while (0)
; #define PG8_LDB(dst, b, h) do { _Pragma("unroll") for (int n = 0; n < 2; ++n) dst[n] = PG8_LD32(lds + PG8_SB(b, h) + boff + n * 2048); } while (0)
; #define PG8_WAIT_V(n) asm volatile("s_waitcnt vmcnt(" #n ")" ::: "memory")
; #define PG8_WAIT_L(n) asm volatile("s_waitcnt lgkmcnt(" #n ")" ::: "memory")
; #define PG8_BAR __builtin_amdgcn_s_barrier()
; #define PG8_SCHED __builtin_amdgcn_sched_barrier(0)
; #define PG8_STA(bufoff, nextflag, h, koff) do { if constexpr (Sched::GATHER) { unsigned _o[2]; _o[0] = (nextflag) ? nxtA[h][0] : curA[h][0]; _o[1] = (nextflag) ? nxtA[h][1] : curA[h][1]; PG8_STAGE(bufoff, Ab + (koff), _o); } \
;         else { PG8_STAGE(bufoff, ((nextflag) ? nA : cA) + (size_t)(h) * hstep + (koff), voffA); } } while (0)
; template <class Epi, class Sched, bool ALIGN_EPI, int DT>
; __device__ __forceinline__ void gemm_phase(LAS unsigned char* lds, const int KB, const Sched& S, const Epi& E) {
;     ...
;             const size_t k1 = (size_t)(t + 1) * kstep, k2 = last ? 0 : (size_t)(t + 2) * kstep, k3 = k2 + kstep;
;             const char* b2 = last ? nB : cB + (size_t)(t + 2) * kstep; const char* b3 = b2 + kstep;
;             PG8_LDB(B0, 0, 0); PG8_LDB(B1, 0, 1); PG8_SCHED; PG8_LDA(At, 0, 0); PG8_STA(PG8_SA(1, 1), false, 1, k1);
;             PG8_WAIT_V(8); PG8_WAIT_L(0); PG8_BAR; PG8_MMA(0, 0, At, B0); PG8_MMA(0, 1, At, B1); PG8_BAR; PG8_SCHED;
;             PG8_LDA(At, 0, 1); PG8_STAGE(PG8_SB(0, 0), b2, voffB); PG8_STAGE(PG8_SB(0, 1), b2 + hstep, voffB); PG8_STA(PG8_SA(0, 0), last, 0, k2);
;             PG8_WAIT_V(8); PG8_WAIT_L(0); PG8_BAR; PG8_MMA(1, 0, At, B0); PG8_MMA(1, 1, At, B1); PG8_BAR; PG8_SCHED;
.LBB0_1237:
	ds_read_b128 v[18:21], v193
	ds_read_b128 v[22:25], v193 offset:1024
	ds_read_b128 v[26:29], v193 offset:2048
	ds_read_b128 v[30:33], v193 offset:3072
	ds_read_b128 v[2:5], v195
	ds_read_b128 v[6:9], v195 offset:1024
	ds_read_b128 v[10:13], v195 offset:2048
	ds_read_b128 v[14:17], v195 offset:3072
	s_add_u32 s26, s30, 0x100
	s_addc_u32 s27, s31, 0
	s_add_u32 s28, s56, s30
	s_addc_u32 s29, s57, s31
	s_add_i32 s68, s43, s34
	s_add_i32 m0, s35, 0xc000
	s_add_i32 s69, s35, 0xe000
	s_add_i32 s63, s68, 0x2000
	s_cmp_eq_u32 s62, 40
	s_cselect_b32 s29, s23, s29
	s_cselect_b32 s28, s22, s28
	s_cselect_b32 s66, 0, s27
	s_cselect_b32 s67, 0, s26
	v_lshl_add_u64 v[222:223], v[178:179], 0, s[30:31]
	ds_read_b128 v[182:185], v196
	ds_read_b128 v[186:189], v196 offset:1024
	ds_read_b128 v[198:201], v196 offset:2048
	ds_read_b128 v[202:205], v196 offset:3072
	ds_read_b128 v[206:209], v196 offset:4096
	ds_read_b128 v[210:213], v196 offset:5120
	ds_read_b128 v[214:217], v196 offset:6144
	ds_read_b128 v[218:221], v196 offset:7168
	global_load_lds_dwordx4 v[222:223], off
	v_lshl_add_u64 v[222:223], v[180:181], 0, s[30:31]
	s_mov_b32 m0, s69
	s_nop 0
	global_load_lds_dwordx4 v[222:223], off
	s_waitcnt vmcnt(8)
	s_waitcnt lgkmcnt(0)
	s_barrier
	v_mfma_scale_f32_16x16x128_f8f6f4 v[158:161], v[18:25], v[182:189], v[158:161], v190, v190 op_sel_hi:[0,0,0]
	v_mfma_scale_f32_16x16x128_f8f6f4 v[154:157], v[26:33], v[182:189], v[154:157], v190, v190 op_sel_hi:[0,0,0]
	v_mfma_scale_f32_16x16x128_f8f6f4 v[150:153], v[18:25], v[198:205], v[150:153], v190, v190 op_sel_hi:[0,0,0]
	v_mfma_scale_f32_16x16x128_f8f6f4 v[142:145], v[26:33], v[198:205], v[142:145], v190, v190 op_sel_hi:[0,0,0]
	v_mfma_scale_f32_16x16x128_f8f6f4 v[134:137], v[18:25], v[206:213], v[134:137], v190, v190 op_sel_hi:[0,0,0]
	v_mfma_scale_f32_16x16x128_f8f6f4 v[126:129], v[26:33], v[206:213], v[126:129], v190, v190 op_sel_hi:[0,0,0]
	v_mfma_scale_f32_16x16x128_f8f6f4 v[118:121], v[18:25], v[214:221], v[118:121], v190, v190 op_sel_hi:[0,0,0]
	v_mfma_scale_f32_16x16x128_f8f6f4 v[110:113], v[26:33], v[214:221], v[110:113], v190, v190 op_sel_hi:[0,0,0]
	v_mfma_scale_f32_16x16x128_f8f6f4 v[146:149], v[2:9], v[182:189], v[146:149], v190, v190 op_sel_hi:[0,0,0]
	v_mfma_scale_f32_16x16x128_f8f6f4 v[138:141], v[10:17], v[182:189], v[138:141], v190, v190 op_sel_hi:[0,0,0]
	v_mfma_scale_f32_16x16x128_f8f6f4 v[130:133], v[2:9], v[198:205], v[130:133], v190, v190 op_sel_hi:[0,0,0]
	v_mfma_scale_f32_16x16x128_f8f6f4 v[122:125], v[10:17], v[198:205], v[122:125], v190, v190 op_sel_hi:[0,0,0]
	v_mfma_scale_f32_16x16x128_f8f6f4 v[114:117], v[2:9], v[206:213], v[114:117], v190, v190 op_sel_hi:[0,0,0]
	v_mfma_scale_f32_16x16x128_f8f6f4 v[106:109], v[10:17], v[206:213], v[106:109], v190, v190 op_sel_hi:[0,0,0]
	v_mfma_scale_f32_16x16x128_f8f6f4 v[102:105], v[2:9], v[214:221], v[102:105], v190, v190 op_sel_hi:[0,0,0]
	v_mfma_scale_f32_16x16x128_f8f6f4 v[98:101], v[10:17], v[214:221], v[98:101], v190, v190 op_sel_hi:[0,0,0]
	s_barrier
	s_mov_b32 m0, s68
	v_lshl_add_u64 v[184:185], s[28:29], 0, v[162:163]
	ds_read_b128 v[198:201], v196 offset:16384
	ds_read_b128 v[202:205], v196 offset:17408
	ds_read_b128 v[206:209], v196 offset:18432
	ds_read_b128 v[210:213], v196 offset:19456
	ds_read_b128 v[214:217], v196 offset:20480
	ds_read_b128 v[218:221], v196 offset:21504
	ds_read_b128 v[222:225], v196 offset:22528
	ds_read_b128 v[226:229], v196 offset:23552
	global_load_lds_dwordx4 v[184:185], off
	s_mov_b32 m0, s63
	s_cselect_b32 s63, s9, s25
	s_cselect_b32 s68, s8, s24
	s_add_u32 s30, s28, 0xb0000
	v_lshl_add_u64 v[182:183], s[28:29], 0, v[164:165]
	s_addc_u32 s31, s29, 0
	s_add_i32 s69, s44, s34
	global_load_lds_dwordx4 v[182:183], off
	v_lshl_add_u64 v[186:187], s[30:31], 0, v[162:163]
	s_mov_b32 m0, s69
	s_nop 0
	global_load_lds_dwordx4 v[186:187], off
	s_add_i32 m0, s69, 0x2000
	v_lshl_add_u64 v[186:187], s[30:31], 0, v[164:165]
	s_add_u32 s30, s68, s67
	s_addc_u32 s31, s63, s66
	global_load_lds_dwordx4 v[186:187], off
	v_lshl_add_u64 v[186:187], s[30:31], 0, v[166:167]
	s_mov_b32 m0, s35
	v_lshl_add_u64 v[188:189], s[30:31], 0, v[168:169]
	global_load_lds_dwordx4 v[186:187], off
	s_mov_b32 m0, s36
	s_nop 0
	global_load_lds_dwordx4 v[188:189], off
	s_waitcnt vmcnt(8)
	s_waitcnt lgkmcnt(0)
	s_barrier
	v_mfma_scale_f32_16x16x128_f8f6f4 v[94:97], v[18:25], v[198:205], v[94:97], v190, v190 op_sel_hi:[0,0,0]
	v_mfma_scale_f32_16x16x128_f8f6f4 v[90:93], v[26:33], v[198:205], v[90:93], v190, v190 op_sel_hi:[0,0,0]
	v_mfma_scale_f32_16x16x128_f8f6f4 v[86:89], v[18:25], v[206:213], v[86:89], v190, v190 op_sel_hi:[0,0,0]
	v_mfma_scale_f32_16x16x128_f8f6f4 v[78:81], v[26:33], v[206:213], v[78:81], v190, v190 op_sel_hi:[0,0,0]
	v_mfma_scale_f32_16x16x128_f8f6f4 v[62:65], v[18:25], v[214:221], v[62:65], v190, v190 op_sel_hi:[0,0,0]
	v_mfma_scale_f32_16x16x128_f8f6f4 v[54:57], v[26:33], v[214:221], v[54:57], v190, v190 op_sel_hi:[0,0,0]
	v_mfma_scale_f32_16x16x128_f8f6f4 v[46:49], v[18:25], v[222:229], v[46:49], v190, v190 op_sel_hi:[0,0,0]
	v_mfma_scale_f32_16x16x128_f8f6f4 v[38:41], v[26:33], v[222:229], v[38:41], v190, v190 op_sel_hi:[0,0,0]
	v_mfma_scale_f32_16x16x128_f8f6f4 v[82:85], v[2:9], v[198:205], v[82:85], v190, v190 op_sel_hi:[0,0,0]
	v_mfma_scale_f32_16x16x128_f8f6f4 v[74:77], v[10:17], v[198:205], v[74:77], v190, v190 op_sel_hi:[0,0,0]
	v_mfma_scale_f32_16x16x128_f8f6f4 v[58:61], v[2:9], v[206:213], v[58:61], v190, v190 op_sel_hi:[0,0,0]
	v_mfma_scale_f32_16x16x128_f8f6f4 v[50:53], v[10:17], v[206:213], v[50:53], v190, v190 op_sel_hi:[0,0,0]
	v_mfma_scale_f32_16x16x128_f8f6f4 v[42:45], v[2:9], v[214:221], v[42:45], v190, v190 op_sel_hi:[0,0,0]
	v_mfma_scale_f32_16x16x128_f8f6f4 v[34:37], v[10:17], v[214:221], v[34:37], v190, v190 op_sel_hi:[0,0,0]
	v_mfma_scale_f32_16x16x128_f8f6f4 v[70:73], v[2:9], v[222:229], v[70:73], v190, v190 op_sel_hi:[0,0,0]
	v_mfma_scale_f32_16x16x128_f8f6f4 v[66:69], v[10:17], v[222:229], v[66:69], v190, v190 op_sel_hi:[0,0,0]
	s_barrier
; #define PG8_STAGE(bufoff, gbase, voff) do { _Pragma("unroll") for (int _i = 0; _i < 2; ++_i) \
;         __builtin_amdgcn_global_load_lds((const unsigned*)((const char*)(gbase) + (voff)[_i]), (LAS unsigned*)(lds + (bufoff) + ldsw + _i * 8192), 16, 0, 0); } while (0)
; #define PG8_LDA(dst, b, h) do { _Pragma("unroll") for (int m = 0; m < 4; ++m) dst[m] = PG8_LD32(lds + PG8_SA(b, h) + aoff + m * 2048); } while (0)
; #define PG8_LDB(dst, b, h) do { _Pragma("unroll") for (int n = 0; n < 2; ++n) dst[n] = PG8_LD32(lds + PG8_SB(b, h) + boff + n * 2048); } while (0)
; #define PG8_WAIT_V(n) asm volatile("s_waitcnt vmcnt(" #n ")" ::: "memory")
; #define PG8_WAIT_L(n) asm volatile("s_waitcnt lgkmcnt(" #n ")" ::: "memory")
; #define PG8_BAR __builtin_amdgcn_s_barrier()
; #define PG8_SCHED __builtin_amdgcn_sched_barrier(0)
; #define PG8_STA(bufoff, nextflag, h, koff) do { if constexpr (Sched::GATHER) { unsigned _o[2]; _o[0] = (nextflag) ? nxtA[h][0] : curA[h][0]; _o[1] = (nextflag) ? nxtA[h][1] : curA[h][1]; PG8_STAGE(bufoff, Ab + (koff), _o); } \
;         else { PG8_STAGE(bufoff, ((nextflag) ? nA : cA) + (size_t)(h) * hstep + (koff), voffA); } } while (0)
; template <class Epi, class Sched, bool ALIGN_EPI, int DT>
; __device__ __forceinline__ void gemm_phase(LAS unsigned char* lds, const int KB, const Sched& S, const Epi& E) {
;     ...
;             PG8_LDB(B0, 1, 0); PG8_LDB(B1, 1, 1); PG8_SCHED; PG8_LDA(At, 1, 0); PG8_STA(PG8_SA(0, 1), last, 1, k2);
;             PG8_WAIT_V(8); PG8_WAIT_L(0); PG8_BAR; PG8_MMA(0, 0, At, B0); PG8_MMA(0, 1, At, B1); PG8_BAR; PG8_SCHED;
;             PG8_LDA(At, 1, 1); PG8_STAGE(PG8_SB(1, 0), b3, voffB); PG8_STAGE(PG8_SB(1, 1), b3 + hstep, voffB); PG8_STA(PG8_SA(1, 0), last, 0, k3);
;             PG8_WAIT_V(8); PG8_WAIT_L(0); PG8_BAR; PG8_MMA(1, 0, At, B0); PG8_MMA(1, 1, At, B1); PG8_BAR; PG8_SCHED;
;         }
	s_add_i32 s63, 0, 0x18000
	s_add_i32 s66, 0, 0x1c000
	v_add_u32_e32 v14, s63, v191
	v_add_u32_e32 v30, s66, v191
	ds_read_b128 v[2:5], v14
	ds_read_b128 v[6:9], v14 offset:1024
	ds_read_b128 v[10:13], v14 offset:2048
	ds_read_b128 v[14:17], v14 offset:3072
	ds_read_b128 v[18:21], v30
	ds_read_b128 v[22:25], v30 offset:1024
	ds_read_b128 v[26:29], v30 offset:2048
	ds_read_b128 v[30:33], v30 offset:3072
	s_add_u32 s30, s30, 0xb0000
	s_addc_u32 s31, s31, 0
	s_mov_b32 m0, s37
	v_lshl_add_u64 v[230:231], s[30:31], 0, v[166:167]
	ds_read_b128 v[198:201], v196 offset:32768
	ds_read_b128 v[202:205], v196 offset:33792
	ds_read_b128 v[206:209], v196 offset:34816
	ds_read_b128 v[210:213], v196 offset:35840
	ds_read_b128 v[214:217], v196 offset:36864
	ds_read_b128 v[218:221], v196 offset:37888
	ds_read_b128 v[222:225], v196 offset:38912
	ds_read_b128 v[226:229], v196 offset:39936
	global_load_lds_dwordx4 v[230:231], off
	v_lshl_add_u64 v[230:231], s[30:31], 0, v[168:169]
	s_mov_b32 m0, s38
	s_nop 0
	global_load_lds_dwordx4 v[230:231], off
	s_waitcnt vmcnt(8)
	s_waitcnt lgkmcnt(0)
	s_barrier
	v_mfma_scale_f32_16x16x128_f8f6f4 v[158:161], v[2:9], v[198:205], v[158:161], v190, v190 op_sel_hi:[0,0,0]
	v_mfma_scale_f32_16x16x128_f8f6f4 v[154:157], v[10:17], v[198:205], v[154:157], v190, v190 op_sel_hi:[0,0,0]
	v_mfma_scale_f32_16x16x128_f8f6f4 v[150:153], v[2:9], v[206:213], v[150:153], v190, v190 op_sel_hi:[0,0,0]
	v_mfma_scale_f32_16x16x128_f8f6f4 v[142:145], v[10:17], v[206:213], v[142:145], v190, v190 op_sel_hi:[0,0,0]
	v_mfma_scale_f32_16x16x128_f8f6f4 v[134:137], v[2:9], v[214:221], v[134:137], v190, v190 op_sel_hi:[0,0,0]
	v_mfma_scale_f32_16x16x128_f8f6f4 v[126:129], v[10:17], v[214:221], v[126:129], v190, v190 op_sel_hi:[0,0,0]
	v_mfma_scale_f32_16x16x128_f8f6f4 v[118:121], v[2:9], v[222:229], v[118:121], v190, v190 op_sel_hi:[0,0,0]
	v_mfma_scale_f32_16x16x128_f8f6f4 v[110:113], v[10:17], v[222:229], v[110:113], v190, v190 op_sel_hi:[0,0,0]
	v_mfma_scale_f32_16x16x128_f8f6f4 v[146:149], v[18:25], v[198:205], v[146:149], v190, v190 op_sel_hi:[0,0,0]
	v_mfma_scale_f32_16x16x128_f8f6f4 v[138:141], v[26:33], v[198:205], v[138:141], v190, v190 op_sel_hi:[0,0,0]
	v_mfma_scale_f32_16x16x128_f8f6f4 v[130:133], v[18:25], v[206:213], v[130:133], v190, v190 op_sel_hi:[0,0,0]
	v_mfma_scale_f32_16x16x128_f8f6f4 v[122:125], v[26:33], v[206:213], v[122:125], v190, v190 op_sel_hi:[0,0,0]
	v_mfma_scale_f32_16x16x128_f8f6f4 v[114:117], v[18:25], v[214:221], v[114:117], v190, v190 op_sel_hi:[0,0,0]
	v_mfma_scale_f32_16x16x128_f8f6f4 v[106:109], v[26:33], v[214:221], v[106:109], v190, v190 op_sel_hi:[0,0,0]
	v_mfma_scale_f32_16x16x128_f8f6f4 v[102:105], v[18:25], v[222:229], v[102:105], v190, v190 op_sel_hi:[0,0,0]
	v_mfma_scale_f32_16x16x128_f8f6f4 v[98:101], v[26:33], v[222:229], v[98:101], v190, v190 op_sel_hi:[0,0,0]
	s_barrier
	s_add_i32 s30, s63, s34
	v_lshl_add_u64 v[184:185], v[184:185], 0, s[12:13]
	s_mov_b32 m0, s30
	ds_read_b128 v[198:201], v196 offset:49152
	ds_read_b128 v[202:205], v196 offset:50176
	ds_read_b128 v[206:209], v196 offset:51200
	ds_read_b128 v[210:213], v196 offset:52224
	ds_read_b128 v[214:217], v196 offset:53248
	ds_read_b128 v[218:221], v196 offset:54272
	ds_read_b128 v[222:225], v196 offset:55296
	ds_read_b128 v[226:229], v196 offset:56320
	global_load_lds_dwordx4 v[184:185], off
	s_add_i32 m0, s30, 0x2000
	s_add_u32 s28, s28, 0xb0080
	v_lshl_add_u64 v[182:183], v[182:183], 0, s[12:13]
	s_addc_u32 s29, s29, 0
	s_add_i32 s30, s66, s34
	global_load_lds_dwordx4 v[182:183], off
	v_lshl_add_u64 v[182:183], s[28:29], 0, v[162:163]
	s_mov_b32 m0, s30
	s_nop 0
	global_load_lds_dwordx4 v[182:183], off
	v_lshl_add_u64 v[182:183], s[28:29], 0, v[164:165]
	s_add_i32 m0, s30, 0x2000
	s_nop 0
	global_load_lds_dwordx4 v[182:183], off
	v_lshl_add_u64 v[182:183], v[186:187], 0, s[12:13]
	s_mov_b32 m0, s40
	s_nop 0
	global_load_lds_dwordx4 v[182:183], off
	v_lshl_add_u64 v[182:183], v[188:189], 0, s[12:13]
	s_mov_b32 m0, s41
	s_nop 0
	global_load_lds_dwordx4 v[182:183], off
	s_waitcnt vmcnt(8)
	s_waitcnt lgkmcnt(0)
	s_barrier
	v_mfma_scale_f32_16x16x128_f8f6f4 v[94:97], v[2:9], v[198:205], v[94:97], v190, v190 op_sel_hi:[0,0,0]
	v_mfma_scale_f32_16x16x128_f8f6f4 v[90:93], v[10:17], v[198:205], v[90:93], v190, v190 op_sel_hi:[0,0,0]
	v_mfma_scale_f32_16x16x128_f8f6f4 v[86:89], v[2:9], v[206:213], v[86:89], v190, v190 op_sel_hi:[0,0,0]
	v_mfma_scale_f32_16x16x128_f8f6f4 v[78:81], v[10:17], v[206:213], v[78:81], v190, v190 op_sel_hi:[0,0,0]
	v_mfma_scale_f32_16x16x128_f8f6f4 v[62:65], v[2:9], v[214:221], v[62:65], v190, v190 op_sel_hi:[0,0,0]
	v_mfma_scale_f32_16x16x128_f8f6f4 v[54:57], v[10:17], v[214:221], v[54:57], v190, v190 op_sel_hi:[0,0,0]
	v_mfma_scale_f32_16x16x128_f8f6f4 v[46:49], v[2:9], v[222:229], v[46:49], v190, v190 op_sel_hi:[0,0,0]
	v_mfma_scale_f32_16x16x128_f8f6f4 v[38:41], v[10:17], v[222:229], v[38:41], v190, v190 op_sel_hi:[0,0,0]
	v_mfma_scale_f32_16x16x128_f8f6f4 v[82:85], v[18:25], v[198:205], v[82:85], v190, v190 op_sel_hi:[0,0,0]
	v_mfma_scale_f32_16x16x128_f8f6f4 v[74:77], v[26:33], v[198:205], v[74:77], v190, v190 op_sel_hi:[0,0,0]
	v_mfma_scale_f32_16x16x128_f8f6f4 v[58:61], v[18:25], v[206:213], v[58:61], v190, v190 op_sel_hi:[0,0,0]
	v_mfma_scale_f32_16x16x128_f8f6f4 v[50:53], v[26:33], v[206:213], v[50:53], v190, v190 op_sel_hi:[0,0,0]
	v_mfma_scale_f32_16x16x128_f8f6f4 v[42:45], v[18:25], v[214:221], v[42:45], v190, v190 op_sel_hi:[0,0,0]
	v_mfma_scale_f32_16x16x128_f8f6f4 v[34:37], v[26:33], v[214:221], v[34:37], v190, v190 op_sel_hi:[0,0,0]
	v_mfma_scale_f32_16x16x128_f8f6f4 v[70:73], v[18:25], v[222:229], v[70:73], v190, v190 op_sel_hi:[0,0,0]
	v_mfma_scale_f32_16x16x128_f8f6f4 v[66:69], v[26:33], v[222:229], v[66:69], v190, v190 op_sel_hi:[0,0,0]
	s_barrier
	s_add_i32 s62, s62, 2
	s_cmp_gt_u32 s62, 41
	s_mov_b64 s[30:31], s[26:27]
	s_cbranch_scc0 .LBB0_1237
	s_and_b64 vcc, exec, s[14:15]
	s_cbranch_vccz .LBB0_1240
	s_barrier

; #define PG8_STAGE(bufoff, gbase, voff) do { _Pragma("unroll") for (int _i = 0; _i < 2; ++_i) \
;         __builtin_amdgcn_global_load_lds((const unsigned*)((const char*)(gbase) + (voff)[_i]), (LAS unsigned*)(lds + (bufoff) + ldsw + _i * 8192), 16, 0, 0); } while (0)
; #define PG8_LDA(dst, b, h) do { _Pragma("unroll") for (int m = 0; m < 4; ++m) dst[m] = PG8_LD32(lds + PG8_SA(b, h) + aoff + m * 2048); } while (0)
; #define PG8_LDB(dst, b, h) do { _Pragma("unroll") for (int n = 0; n < 2; ++n) dst[n] = PG8_LD32(lds + PG8_SB(b, h) + boff + n * 2048); } while (0)
; #define PG8_WAIT_V(n) asm volatile("s_waitcnt vmcnt(" #n ")" ::: "memory")
; #define PG8_WAIT_L(n) asm volatile("s_waitcnt lgkmcnt(" #n ")" ::: "memory")
; #define PG8_BAR __builtin_amdgcn_s_barrier()
; #define PG8_SCHED __builtin_amdgcn_sched_barrier(0)
; #define PG8_STA(bufoff, nextflag, h, koff) do { if constexpr (Sched::GATHER) { unsigned _o[2]; _o[0] = (nextflag) ? nxtA[h][0] : curA[h][0]; _o[1] = (nextflag) ? nxtA[h][1] : curA[h][1]; PG8_STAGE(bufoff, Ab + (koff), _o); } \
;         else { PG8_STAGE(bufoff, ((nextflag) ? nA : cA) + (size_t)(h) * hstep + (koff), voffA); } } while (0)
; template <class Epi, class Sched, bool ALIGN_EPI, int DT>
; __device__ __forceinline__ void gemm_phase(LAS unsigned char* lds, const int KB, const Sched& S, const Epi& E) {
;     ...
;             const size_t k1 = (size_t)(t + 1) * kstep, k2 = last ? 0 : (size_t)(t + 2) * kstep, k3 = k2 + kstep;
;             const char* b2 = last ? nB : cB + (size_t)(t + 2) * kstep; const char* b3 = b2 + kstep;
;             PG8_LDB(B0, 0, 0); PG8_LDB(B1, 0, 1); PG8_SCHED; PG8_LDA(At, 0, 0); PG8_STA(PG8_SA(1, 1), false, 1, k1);
;             PG8_WAIT_V(8); PG8_WAIT_L(0); PG8_BAR; PG8_MMA(0, 0, At, B0); PG8_MMA(0, 1, At, B1); PG8_BAR; PG8_SCHED;
;             PG8_LDA(At, 0, 1); PG8_STAGE(PG8_SB(0, 0), b2, voffB); PG8_STAGE(PG8_SB(0, 1), b2 + hstep, voffB); PG8_STA(PG8_SA(0, 0), last, 0, k2);
;             PG8_WAIT_V(8); PG8_WAIT_L(0); PG8_BAR; PG8_MMA(1, 0, At, B0); PG8_MMA(1, 1, At, B1); PG8_BAR; PG8_SCHED;
.LBB0_1385:
	ds_read_b128 v[152:155], v174
	ds_read_b128 v[156:159], v174 offset:1024
	ds_read_b128 v[160:163], v174 offset:2048
	ds_read_b128 v[164:167], v174 offset:3072
	ds_read_b128 v[168:171], v175
	ds_read_b128 v[180:183], v175 offset:1024
	ds_read_b128 v[184:187], v175 offset:2048
	ds_read_b128 v[188:191], v175 offset:3072
	s_add_u32 s38, s36, 0x100
	s_addc_u32 s39, s37, 0
	s_add_u32 s74, s25, s36
	s_addc_u32 s75, s70, s37
	s_cmp_eq_u32 s71, 12
	s_cselect_b64 s[42:43], -1, 0
	s_and_b64 s[40:41], s[42:43], exec
	s_cselect_b32 s76, 0, s38
	s_cselect_b32 s41, s0, s75
	s_cselect_b32 s40, s23, s74
	v_lshl_add_u64 v[192:193], v[148:149], 0, s[36:37]
	s_add_i32 m0, s47, 0xc000
	ds_read_b128 v[196:199], v176
	ds_read_b128 v[200:203], v176 offset:1024
	ds_read_b128 v[204:207], v176 offset:2048
	ds_read_b128 v[208:211], v176 offset:3072
	ds_read_b128 v[212:215], v176 offset:4096
	ds_read_b128 v[216:219], v176 offset:5120
	ds_read_b128 v[220:223], v176 offset:6144
	ds_read_b128 v[224:227], v176 offset:7168
	global_load_lds_dwordx4 v[192:193], off
	v_lshl_add_u64 v[192:193], v[150:151], 0, s[36:37]
	s_add_i32 m0, s47, 0xe000
	s_nop 0
	global_load_lds_dwordx4 v[192:193], off
	s_waitcnt vmcnt(8)
	s_waitcnt lgkmcnt(0)
	s_barrier
	v_mfma_i32_16x16x64_i8 v[126:129], v[152:155], v[196:199], v[126:129]
	v_mfma_i32_16x16x64_i8 v[122:125], v[160:163], v[196:199], v[122:125]
	v_mfma_i32_16x16x64_i8 v[110:113], v[152:155], v[204:207], v[110:113]
	v_mfma_i32_16x16x64_i8 v[106:109], v[160:163], v[204:207], v[106:109]
	v_mfma_i32_16x16x64_i8 v[94:97], v[152:155], v[212:215], v[94:97]
	v_mfma_i32_16x16x64_i8 v[90:93], v[160:163], v[212:215], v[90:93]
	v_mfma_i32_16x16x64_i8 v[78:81], v[152:155], v[220:223], v[78:81]
	v_mfma_i32_16x16x64_i8 v[74:77], v[160:163], v[220:223], v[74:77]
	v_mfma_i32_16x16x64_i8 v[126:129], v[156:159], v[200:203], v[126:129]
	v_mfma_i32_16x16x64_i8 v[122:125], v[164:167], v[200:203], v[122:125]
	v_mfma_i32_16x16x64_i8 v[110:113], v[156:159], v[208:211], v[110:113]
	v_mfma_i32_16x16x64_i8 v[106:109], v[164:167], v[208:211], v[106:109]
	v_mfma_i32_16x16x64_i8 v[94:97], v[156:159], v[216:219], v[94:97]
	v_mfma_i32_16x16x64_i8 v[90:93], v[164:167], v[216:219], v[90:93]
	v_mfma_i32_16x16x64_i8 v[78:81], v[156:159], v[224:227], v[78:81]
	v_mfma_i32_16x16x64_i8 v[74:77], v[164:167], v[224:227], v[74:77]
	v_mfma_i32_16x16x64_i8 v[118:121], v[168:171], v[196:199], v[118:121]
	v_mfma_i32_16x16x64_i8 v[114:117], v[184:187], v[196:199], v[114:117]
	v_mfma_i32_16x16x64_i8 v[102:105], v[168:171], v[204:207], v[102:105]
	v_mfma_i32_16x16x64_i8 v[98:101], v[184:187], v[204:207], v[98:101]
	v_mfma_i32_16x16x64_i8 v[86:89], v[168:171], v[212:215], v[86:89]
	v_mfma_i32_16x16x64_i8 v[82:85], v[184:187], v[212:215], v[82:85]
	v_mfma_i32_16x16x64_i8 v[70:73], v[168:171], v[220:223], v[70:73]
	v_mfma_i32_16x16x64_i8 v[66:69], v[184:187], v[220:223], v[66:69]
	v_mfma_i32_16x16x64_i8 v[118:121], v[180:183], v[200:203], v[118:121]
	v_mfma_i32_16x16x64_i8 v[114:117], v[188:191], v[200:203], v[114:117]
	v_mfma_i32_16x16x64_i8 v[102:105], v[180:183], v[208:211], v[102:105]
	v_mfma_i32_16x16x64_i8 v[98:101], v[188:191], v[208:211], v[98:101]
	v_mfma_i32_16x16x64_i8 v[86:89], v[180:183], v[216:219], v[86:89]
	v_mfma_i32_16x16x64_i8 v[82:85], v[188:191], v[216:219], v[82:85]
	v_mfma_i32_16x16x64_i8 v[70:73], v[180:183], v[224:227], v[70:73]
	v_mfma_i32_16x16x64_i8 v[66:69], v[188:191], v[224:227], v[66:69]
	s_barrier
	s_add_i32 s36, s66, s44
	v_lshl_add_u64 v[192:193], s[40:41], 0, v[134:135]
	s_mov_b32 m0, s36
	ds_read_b128 v[196:199], v176 offset:16384
	ds_read_b128 v[200:203], v176 offset:17408
	ds_read_b128 v[204:207], v176 offset:18432
	ds_read_b128 v[208:211], v176 offset:19456
	ds_read_b128 v[212:215], v176 offset:20480
	ds_read_b128 v[216:219], v176 offset:21504
	ds_read_b128 v[220:223], v176 offset:22528
	ds_read_b128 v[224:227], v176 offset:23552
	global_load_lds_dwordx4 v[192:193], off
	s_add_i32 m0, s36, 0x2000
	s_add_u32 s36, s40, 0x40000
	v_lshl_add_u64 v[228:229], s[40:41], 0, v[132:133]
	s_addc_u32 s37, s41, 0
	s_add_i32 s74, s67, s44
	global_load_lds_dwordx4 v[228:229], off
	v_lshl_add_u64 v[230:231], s[36:37], 0, v[134:135]
	s_mov_b32 m0, s74
	s_nop 0
	global_load_lds_dwordx4 v[230:231], off
	v_lshl_add_u64 v[230:231], s[36:37], 0, v[132:133]
	s_add_i32 m0, s74, 0x2000
	s_and_b64 s[36:37], s[8:9], s[42:43]
	s_and_b64 s[36:37], s[36:37], exec
	s_cselect_b32 s36, s26, s34
	s_cselect_b32 s37, s27, s35
	s_add_u32 s36, s36, s76
	s_addc_u32 s37, s37, 0
	global_load_lds_dwordx4 v[230:231], off
	v_lshl_add_u64 v[230:231], s[36:37], 0, v[136:137]
	s_mov_b32 m0, s47
	v_lshl_add_u64 v[232:233], s[36:37], 0, v[138:139]
	global_load_lds_dwordx4 v[230:231], off
	s_mov_b32 m0, s49
	s_nop 0
	global_load_lds_dwordx4 v[232:233], off
	s_waitcnt vmcnt(8)
	s_waitcnt lgkmcnt(0)
	s_barrier
; #define PG8_LDA(dst, b, h) do { _Pragma("unroll") for (int m = 0; m < 4; ++m) dst[m] = PG8_LD32(lds + PG8_SA(b, h) + aoff + m * 2048); } while (0)
; #define PG8_LDB(dst, b, h) do { _Pragma("unroll") for (int n = 0; n < 2; ++n) dst[n] = PG8_LD32(lds + PG8_SB(b, h) + boff + n * 2048); } while (0)
; #define PG8_WAIT_V(n) asm volatile("s_waitcnt vmcnt(" #n ")" ::: "memory")
; #define PG8_WAIT_L(n) asm volatile("s_waitcnt lgkmcnt(" #n ")" ::: "memory")
; #define PG8_BAR __builtin_amdgcn_s_barrier()
; #define PG8_SCHED __builtin_amdgcn_sched_barrier(0)
; #define PG8_STA(bufoff, nextflag, h, koff) do { if constexpr (Sched::GATHER) { unsigned _o[2]; _o[0] = (nextflag) ? nxtA[h][0] : curA[h][0]; _o[1] = (nextflag) ? nxtA[h][1] : curA[h][1]; PG8_STAGE(bufoff, Ab + (koff), _o); } \
;         else { PG8_STAGE(bufoff, ((nextflag) ? nA : cA) + (size_t)(h) * hstep + (koff), voffA); } } while (0)
; template <class Epi, class Sched, bool ALIGN_EPI, int DT>
; __device__ __forceinline__ void gemm_phase(LAS unsigned char* lds, const int KB, const Sched& S, const Epi& E) {
;     ...
;             PG8_WAIT_V(8); PG8_WAIT_L(0); PG8_BAR; PG8_MMA(1, 0, At, B0); PG8_MMA(1, 1, At, B1); PG8_BAR; PG8_SCHED;
;             PG8_LDB(B0, 1, 0); PG8_LDB(B1, 1, 1); PG8_SCHED; PG8_LDA(At, 1, 0); PG8_STA(PG8_SA(0, 1), last, 1, k2);
;             PG8_WAIT_V(8); PG8_WAIT_L(0); PG8_BAR; PG8_MMA(0, 0, At, B0); PG8_MMA(0, 1, At, B1); PG8_BAR; PG8_SCHED;
	v_mfma_i32_16x16x64_i8 v[62:65], v[152:155], v[196:199], v[62:65]
	v_mfma_i32_16x16x64_i8 v[58:61], v[160:163], v[196:199], v[58:61]
	v_mfma_i32_16x16x64_i8 v[46:49], v[152:155], v[204:207], v[46:49]
	v_mfma_i32_16x16x64_i8 v[42:45], v[160:163], v[204:207], v[42:45]
	v_mfma_i32_16x16x64_i8 v[30:33], v[152:155], v[212:215], v[30:33]
	v_mfma_i32_16x16x64_i8 v[26:29], v[160:163], v[212:215], v[26:29]
	v_mfma_i32_16x16x64_i8 v[6:9], v[152:155], v[220:223], v[6:9]
	v_mfma_i32_16x16x64_i8 v[2:5], v[160:163], v[220:223], v[2:5]
	v_mfma_i32_16x16x64_i8 v[62:65], v[156:159], v[200:203], v[62:65]
	v_mfma_i32_16x16x64_i8 v[58:61], v[164:167], v[200:203], v[58:61]
	v_mfma_i32_16x16x64_i8 v[46:49], v[156:159], v[208:211], v[46:49]
	v_mfma_i32_16x16x64_i8 v[42:45], v[164:167], v[208:211], v[42:45]
	v_mfma_i32_16x16x64_i8 v[30:33], v[156:159], v[216:219], v[30:33]
	v_mfma_i32_16x16x64_i8 v[26:29], v[164:167], v[216:219], v[26:29]
	v_mfma_i32_16x16x64_i8 v[6:9], v[156:159], v[224:227], v[6:9]
	v_mfma_i32_16x16x64_i8 v[2:5], v[164:167], v[224:227], v[2:5]
	v_mfma_i32_16x16x64_i8 v[54:57], v[168:171], v[196:199], v[54:57]
	v_mfma_i32_16x16x64_i8 v[50:53], v[184:187], v[196:199], v[50:53]
	v_mfma_i32_16x16x64_i8 v[38:41], v[168:171], v[204:207], v[38:41]
	v_mfma_i32_16x16x64_i8 v[34:37], v[184:187], v[204:207], v[34:37]
	v_mfma_i32_16x16x64_i8 v[14:17], v[168:171], v[212:215], v[14:17]
	v_mfma_i32_16x16x64_i8 v[10:13], v[184:187], v[212:215], v[10:13]
	v_mfma_i32_16x16x64_i8 v[22:25], v[168:171], v[220:223], v[22:25]
	v_mfma_i32_16x16x64_i8 v[18:21], v[184:187], v[220:223], v[18:21]
	v_mfma_i32_16x16x64_i8 v[54:57], v[180:183], v[200:203], v[54:57]
	v_mfma_i32_16x16x64_i8 v[50:53], v[188:191], v[200:203], v[50:53]
	v_mfma_i32_16x16x64_i8 v[38:41], v[180:183], v[208:211], v[38:41]
	v_mfma_i32_16x16x64_i8 v[34:37], v[188:191], v[208:211], v[34:37]
	v_mfma_i32_16x16x64_i8 v[14:17], v[180:183], v[216:219], v[14:17]
	v_mfma_i32_16x16x64_i8 v[10:13], v[188:191], v[216:219], v[10:13]
	v_mfma_i32_16x16x64_i8 v[22:25], v[180:183], v[224:227], v[22:25]
	v_mfma_i32_16x16x64_i8 v[18:21], v[188:191], v[224:227], v[18:21]
	s_barrier
	s_add_i32 s42, 0, 0x18000
	v_add_u32_e32 v1, s42, v172
	s_add_i32 s43, 0, 0x1c000
	ds_read_b128 v[152:155], v1
	ds_read_b128 v[156:159], v1 offset:1024
	ds_read_b128 v[160:163], v1 offset:2048
	ds_read_b128 v[164:167], v1 offset:3072
	v_add_u32_e32 v1, s43, v172
	ds_read_b128 v[168:171], v1
	ds_read_b128 v[180:183], v1 offset:1024
	ds_read_b128 v[184:187], v1 offset:2048
	ds_read_b128 v[188:191], v1 offset:3072
	s_add_u32 s36, s36, 0x40000
	s_addc_u32 s37, s37, 0
	s_mov_b32 m0, s52
	v_lshl_add_u64 v[234:235], s[36:37], 0, v[136:137]
	ds_read_b128 v[196:199], v176 offset:32768
	ds_read_b128 v[200:203], v176 offset:33792
	ds_read_b128 v[204:207], v176 offset:34816
	ds_read_b128 v[208:211], v176 offset:35840
	ds_read_b128 v[212:215], v176 offset:36864
	ds_read_b128 v[216:219], v176 offset:37888
	ds_read_b128 v[220:223], v176 offset:38912
	ds_read_b128 v[224:227], v176 offset:39936
	global_load_lds_dwordx4 v[234:235], off
	v_lshl_add_u64 v[234:235], s[36:37], 0, v[138:139]
	s_mov_b32 m0, s53
	s_nop 0
	global_load_lds_dwordx4 v[234:235], off
	s_waitcnt vmcnt(8)
	s_waitcnt lgkmcnt(0)
	s_barrier
	v_mfma_i32_16x16x64_i8 v[126:129], v[152:155], v[196:199], v[126:129]
	v_mfma_i32_16x16x64_i8 v[122:125], v[160:163], v[196:199], v[122:125]
	v_mfma_i32_16x16x64_i8 v[110:113], v[152:155], v[204:207], v[110:113]
	v_mfma_i32_16x16x64_i8 v[106:109], v[160:163], v[204:207], v[106:109]
	v_mfma_i32_16x16x64_i8 v[94:97], v[152:155], v[212:215], v[94:97]
	v_mfma_i32_16x16x64_i8 v[90:93], v[160:163], v[212:215], v[90:93]
	v_mfma_i32_16x16x64_i8 v[78:81], v[152:155], v[220:223], v[78:81]
	v_mfma_i32_16x16x64_i8 v[74:77], v[160:163], v[220:223], v[74:77]
	v_mfma_i32_16x16x64_i8 v[126:129], v[156:159], v[200:203], v[126:129]
	v_mfma_i32_16x16x64_i8 v[122:125], v[164:167], v[200:203], v[122:125]
	v_mfma_i32_16x16x64_i8 v[110:113], v[156:159], v[208:211], v[110:113]
	v_mfma_i32_16x16x64_i8 v[106:109], v[164:167], v[208:211], v[106:109]
	v_mfma_i32_16x16x64_i8 v[94:97], v[156:159], v[216:219], v[94:97]
	v_mfma_i32_16x16x64_i8 v[90:93], v[164:167], v[216:219], v[90:93]
	v_mfma_i32_16x16x64_i8 v[78:81], v[156:159], v[224:227], v[78:81]
	v_mfma_i32_16x16x64_i8 v[74:77], v[164:167], v[224:227], v[74:77]
	v_mfma_i32_16x16x64_i8 v[118:121], v[168:171], v[196:199], v[118:121]
	v_mfma_i32_16x16x64_i8 v[114:117], v[184:187], v[196:199], v[114:117]
	v_mfma_i32_16x16x64_i8 v[102:105], v[168:171], v[204:207], v[102:105]
	v_mfma_i32_16x16x64_i8 v[98:101], v[184:187], v[204:207], v[98:101]
	v_mfma_i32_16x16x64_i8 v[86:89], v[168:171], v[212:215], v[86:89]
	v_mfma_i32_16x16x64_i8 v[82:85], v[184:187], v[212:215], v[82:85]
	v_mfma_i32_16x16x64_i8 v[70:73], v[168:171], v[220:223], v[70:73]
	v_mfma_i32_16x16x64_i8 v[66:69], v[184:187], v[220:223], v[66:69]
	v_mfma_i32_16x16x64_i8 v[118:121], v[180:183], v[200:203], v[118:121]
	v_mfma_i32_16x16x64_i8 v[114:117], v[188:191], v[200:203], v[114:117]
	v_mfma_i32_16x16x64_i8 v[102:105], v[180:183], v[208:211], v[102:105]
	v_mfma_i32_16x16x64_i8 v[98:101], v[188:191], v[208:211], v[98:101]
	v_mfma_i32_16x16x64_i8 v[86:89], v[180:183], v[216:219], v[86:89]
	v_mfma_i32_16x16x64_i8 v[82:85], v[188:191], v[216:219], v[82:85]
	v_mfma_i32_16x16x64_i8 v[70:73], v[180:183], v[224:227], v[70:73]
	v_mfma_i32_16x16x64_i8 v[66:69], v[188:191], v[224:227], v[66:69]
	s_barrier
; #define PG8_STAGE(bufoff, gbase, voff) do { _Pragma("unroll") for (int _i = 0; _i < 2; ++_i) \
;         __builtin_amdgcn_global_load_lds((const unsigned*)((const char*)(gbase) + (voff)[_i]), (LAS unsigned*)(lds + (bufoff) + ldsw + _i * 8192), 16, 0, 0); } while (0)
; #define PG8_LDA(dst, b, h) do { _Pragma("unroll") for (int m = 0; m < 4; ++m) dst[m] = PG8_LD32(lds + PG8_SA(b, h) + aoff + m * 2048); } while (0)
; #define PG8_WAIT_V(n) asm volatile("s_waitcnt vmcnt(" #n ")" ::: "memory")
; #define PG8_WAIT_L(n) asm volatile("s_waitcnt lgkmcnt(" #n ")" ::: "memory")
; #define PG8_BAR __builtin_amdgcn_s_barrier()
; #define PG8_SCHED __builtin_amdgcn_sched_barrier(0)
; #define PG8_STA(bufoff, nextflag, h, koff) do { if constexpr (Sched::GATHER) { unsigned _o[2]; _o[0] = (nextflag) ? nxtA[h][0] : curA[h][0]; _o[1] = (nextflag) ? nxtA[h][1] : curA[h][1]; PG8_STAGE(bufoff, Ab + (koff), _o); } \
;         else { PG8_STAGE(bufoff, ((nextflag) ? nA : cA) + (size_t)(h) * hstep + (koff), voffA); } } while (0)
; template <class Epi, class Sched, bool ALIGN_EPI, int DT>
; __device__ __forceinline__ void gemm_phase(LAS unsigned char* lds, const int KB, const Sched& S, const Epi& E) {
;     ...
;             PG8_LDA(At, 1, 1); PG8_STAGE(PG8_SB(1, 0), b3, voffB); PG8_STAGE(PG8_SB(1, 1), b3 + hstep, voffB); PG8_STA(PG8_SA(1, 0), last, 0, k3);
;             PG8_WAIT_V(8); PG8_WAIT_L(0); PG8_BAR; PG8_MMA(1, 0, At, B0); PG8_MMA(1, 1, At, B1); PG8_BAR; PG8_SCHED;
;         }
	s_add_i32 s36, s42, s44
	v_lshl_add_u64 v[192:193], v[192:193], 0, s[18:19]
	s_mov_b32 m0, s36
	ds_read_b128 v[196:199], v176 offset:49152
	ds_read_b128 v[200:203], v176 offset:50176
	ds_read_b128 v[204:207], v176 offset:51200
	ds_read_b128 v[208:211], v176 offset:52224
	ds_read_b128 v[212:215], v176 offset:53248
	ds_read_b128 v[216:219], v176 offset:54272
	ds_read_b128 v[220:223], v176 offset:55296
	ds_read_b128 v[224:227], v176 offset:56320
	global_load_lds_dwordx4 v[192:193], off
	s_add_i32 m0, s36, 0x2000
	s_add_u32 s36, s40, 0x40080
	v_lshl_add_u64 v[192:193], v[228:229], 0, s[18:19]
	s_addc_u32 s37, s41, 0
	s_add_i32 s40, s43, s44
	global_load_lds_dwordx4 v[192:193], off
	v_lshl_add_u64 v[192:193], s[36:37], 0, v[134:135]
	s_mov_b32 m0, s40
	s_nop 0
	global_load_lds_dwordx4 v[192:193], off
	v_lshl_add_u64 v[192:193], s[36:37], 0, v[132:133]
	s_add_i32 m0, s40, 0x2000
	s_nop 0
	global_load_lds_dwordx4 v[192:193], off
	v_lshl_add_u64 v[192:193], v[230:231], 0, s[18:19]
	s_mov_b32 m0, s57
	s_nop 0
	global_load_lds_dwordx4 v[192:193], off
	v_lshl_add_u64 v[192:193], v[232:233], 0, s[18:19]
	s_mov_b32 m0, s62
	s_nop 0
	global_load_lds_dwordx4 v[192:193], off
	s_waitcnt vmcnt(8)
	s_waitcnt lgkmcnt(0)
	s_barrier
	v_mfma_i32_16x16x64_i8 v[62:65], v[152:155], v[196:199], v[62:65]
	v_mfma_i32_16x16x64_i8 v[58:61], v[160:163], v[196:199], v[58:61]
	v_mfma_i32_16x16x64_i8 v[46:49], v[152:155], v[204:207], v[46:49]
	v_mfma_i32_16x16x64_i8 v[42:45], v[160:163], v[204:207], v[42:45]
	v_mfma_i32_16x16x64_i8 v[30:33], v[152:155], v[212:215], v[30:33]
	v_mfma_i32_16x16x64_i8 v[26:29], v[160:163], v[212:215], v[26:29]
	v_mfma_i32_16x16x64_i8 v[6:9], v[152:155], v[220:223], v[6:9]
	v_mfma_i32_16x16x64_i8 v[2:5], v[160:163], v[220:223], v[2:5]
	v_mfma_i32_16x16x64_i8 v[62:65], v[156:159], v[200:203], v[62:65]
	v_mfma_i32_16x16x64_i8 v[58:61], v[164:167], v[200:203], v[58:61]
	v_mfma_i32_16x16x64_i8 v[46:49], v[156:159], v[208:211], v[46:49]
	v_mfma_i32_16x16x64_i8 v[42:45], v[164:167], v[208:211], v[42:45]
	v_mfma_i32_16x16x64_i8 v[30:33], v[156:159], v[216:219], v[30:33]
	v_mfma_i32_16x16x64_i8 v[26:29], v[164:167], v[216:219], v[26:29]
	v_mfma_i32_16x16x64_i8 v[6:9], v[156:159], v[224:227], v[6:9]
	v_mfma_i32_16x16x64_i8 v[2:5], v[164:167], v[224:227], v[2:5]
	v_mfma_i32_16x16x64_i8 v[54:57], v[168:171], v[196:199], v[54:57]
	v_mfma_i32_16x16x64_i8 v[50:53], v[184:187], v[196:199], v[50:53]
	v_mfma_i32_16x16x64_i8 v[38:41], v[168:171], v[204:207], v[38:41]
	v_mfma_i32_16x16x64_i8 v[34:37], v[184:187], v[204:207], v[34:37]
	v_mfma_i32_16x16x64_i8 v[14:17], v[168:171], v[212:215], v[14:17]
	v_mfma_i32_16x16x64_i8 v[10:13], v[184:187], v[212:215], v[10:13]
	v_mfma_i32_16x16x64_i8 v[22:25], v[168:171], v[220:223], v[22:25]
	v_mfma_i32_16x16x64_i8 v[18:21], v[184:187], v[220:223], v[18:21]
	v_mfma_i32_16x16x64_i8 v[54:57], v[180:183], v[200:203], v[54:57]
	v_mfma_i32_16x16x64_i8 v[50:53], v[188:191], v[200:203], v[50:53]
	v_mfma_i32_16x16x64_i8 v[38:41], v[180:183], v[208:211], v[38:41]
	v_mfma_i32_16x16x64_i8 v[34:37], v[188:191], v[208:211], v[34:37]
	v_mfma_i32_16x16x64_i8 v[14:17], v[180:183], v[216:219], v[14:17]
	v_mfma_i32_16x16x64_i8 v[10:13], v[188:191], v[216:219], v[10:13]
	v_mfma_i32_16x16x64_i8 v[22:25], v[180:183], v[224:227], v[22:25]
	v_mfma_i32_16x16x64_i8 v[18:21], v[188:191], v[224:227], v[18:21]
	s_barrier
	s_add_i32 s71, s71, 2
	s_cmp_gt_u32 s71, 13
	s_mov_b64 s[36:37], s[38:39]
	s_cbranch_scc0 .LBB0_1385
	s_and_b64 vcc, exec, s[20:21]
	s_cbranch_vccz .LBB0_1388
	s_barrier

; #define PG8_STAGE(bufoff, gbase, voff) do { _Pragma("unroll") for (int _i = 0; _i < 2; ++_i) \
;         __builtin_amdgcn_global_load_lds((const unsigned*)((const char*)(gbase) + (voff)[_i]), (LAS unsigned*)(lds + (bufoff) + ldsw + _i * 8192), 16, 0, 0); } while (0)
; #define PG8_LDA(dst, b, h) do { _Pragma("unroll") for (int m = 0; m < 4; ++m) dst[m] = PG8_LD32(lds + PG8_SA(b, h) + aoff + m * 2048); } while (0)
; #define PG8_LDB(dst, b, h) do { _Pragma("unroll") for (int n = 0; n < 2; ++n) dst[n] = PG8_LD32(lds + PG8_SB(b, h) + boff + n * 2048); } while (0)
; #define PG8_WAIT_V(n) asm volatile("s_waitcnt vmcnt(" #n ")" ::: "memory")
; #define PG8_WAIT_L(n) asm volatile("s_waitcnt lgkmcnt(" #n ")" ::: "memory")
; #define PG8_BAR __builtin_amdgcn_s_barrier()
; #define PG8_SCHED __builtin_amdgcn_sched_barrier(0)
; #define PG8_STA(bufoff, nextflag, h, koff) do { if constexpr (Sched::GATHER) { unsigned _o[2]; _o[0] = (nextflag) ? nxtA[h][0] : curA[h][0]; _o[1] = (nextflag) ? nxtA[h][1] : curA[h][1]; PG8_STAGE(bufoff, Ab + (koff), _o); } \
;         else { PG8_STAGE(bufoff, ((nextflag) ? nA : cA) + (size_t)(h) * hstep + (koff), voffA); } } while (0)
; template <class Epi, class Sched, bool ALIGN_EPI, int DT>
; __device__ __forceinline__ void gemm_phase(LAS unsigned char* lds, const int KB, const Sched& S, const Epi& E) {
;     ...
;             const size_t k1 = (size_t)(t + 1) * kstep, k2 = last ? 0 : (size_t)(t + 2) * kstep, k3 = k2 + kstep;
;             const char* b2 = last ? nB : cB + (size_t)(t + 2) * kstep; const char* b3 = b2 + kstep;
;             PG8_LDB(B0, 0, 0); PG8_LDB(B1, 0, 1); PG8_SCHED; PG8_LDA(At, 0, 0); PG8_STA(PG8_SA(1, 1), false, 1, k1);
;             PG8_WAIT_V(8); PG8_WAIT_L(0); PG8_BAR; PG8_MMA(0, 0, At, B0); PG8_MMA(0, 1, At, B1); PG8_BAR; PG8_SCHED;
;             PG8_LDA(At, 0, 1); PG8_STAGE(PG8_SB(0, 0), b2, voffB); PG8_STAGE(PG8_SB(0, 1), b2 + hstep, voffB); PG8_STA(PG8_SA(0, 0), last, 0, k2);
;             PG8_WAIT_V(8); PG8_WAIT_L(0); PG8_BAR; PG8_MMA(1, 0, At, B0); PG8_MMA(1, 1, At, B1); PG8_BAR; PG8_SCHED;
.LBB0_2108:
	ds_read_b128 v[18:21], v193
	ds_read_b128 v[22:25], v193 offset:1024
	ds_read_b128 v[26:29], v193 offset:2048
	ds_read_b128 v[30:33], v193 offset:3072
	ds_read_b128 v[2:5], v195
	ds_read_b128 v[6:9], v195 offset:1024
	ds_read_b128 v[10:13], v195 offset:2048
	ds_read_b128 v[14:17], v195 offset:3072
	s_add_u32 s38, s42, 0x100
	s_addc_u32 s39, s43, 0
	s_add_u32 s71, s68, s42
	s_addc_u32 s74, s69, s43
	s_cmp_eq_u32 s70, 12
	s_cselect_b64 s[44:45], -1, 0
	s_and_b64 s[40:41], s[44:45], exec
	s_cselect_b32 s41, s25, s74
	s_cselect_b32 s40, s27, s71
	s_cselect_b32 s71, 0, s39
	s_cselect_b32 s74, 0, s38
	v_lshl_add_u64 v[222:223], v[178:179], 0, s[42:43]
	s_add_i32 m0, s35, 0xc000
	ds_read_b128 v[182:185], v196
	ds_read_b128 v[186:189], v196 offset:1024
	ds_read_b128 v[198:201], v196 offset:2048
	ds_read_b128 v[202:205], v196 offset:3072
	ds_read_b128 v[206:209], v196 offset:4096
	ds_read_b128 v[210:213], v196 offset:5120
	ds_read_b128 v[214:217], v196 offset:6144
	ds_read_b128 v[218:221], v196 offset:7168
	global_load_lds_dwordx4 v[222:223], off
	v_lshl_add_u64 v[222:223], v[180:181], 0, s[42:43]
	s_add_i32 m0, s35, 0xe000
	s_nop 0
	global_load_lds_dwordx4 v[222:223], off
	s_waitcnt vmcnt(8)
	s_waitcnt lgkmcnt(0)
	s_barrier
	v_mfma_scale_f32_16x16x128_f8f6f4 v[158:161], v[18:25], v[182:189], v[158:161], v1, v1 op_sel_hi:[0,0,0]
	v_mfma_scale_f32_16x16x128_f8f6f4 v[154:157], v[26:33], v[182:189], v[154:157], v1, v1 op_sel_hi:[0,0,0]
	v_mfma_scale_f32_16x16x128_f8f6f4 v[150:153], v[18:25], v[198:205], v[150:153], v1, v1 op_sel_hi:[0,0,0]
	v_mfma_scale_f32_16x16x128_f8f6f4 v[142:145], v[26:33], v[198:205], v[142:145], v1, v1 op_sel_hi:[0,0,0]
	v_mfma_scale_f32_16x16x128_f8f6f4 v[134:137], v[18:25], v[206:213], v[134:137], v1, v1 op_sel_hi:[0,0,0]
	v_mfma_scale_f32_16x16x128_f8f6f4 v[126:129], v[26:33], v[206:213], v[126:129], v1, v1 op_sel_hi:[0,0,0]
	v_mfma_scale_f32_16x16x128_f8f6f4 v[118:121], v[18:25], v[214:221], v[118:121], v1, v1 op_sel_hi:[0,0,0]
	v_mfma_scale_f32_16x16x128_f8f6f4 v[110:113], v[26:33], v[214:221], v[110:113], v1, v1 op_sel_hi:[0,0,0]
	v_mfma_scale_f32_16x16x128_f8f6f4 v[146:149], v[2:9], v[182:189], v[146:149], v1, v1 op_sel_hi:[0,0,0]
	v_mfma_scale_f32_16x16x128_f8f6f4 v[138:141], v[10:17], v[182:189], v[138:141], v1, v1 op_sel_hi:[0,0,0]
	v_mfma_scale_f32_16x16x128_f8f6f4 v[130:133], v[2:9], v[198:205], v[130:133], v1, v1 op_sel_hi:[0,0,0]
	v_mfma_scale_f32_16x16x128_f8f6f4 v[122:125], v[10:17], v[198:205], v[122:125], v1, v1 op_sel_hi:[0,0,0]
	v_mfma_scale_f32_16x16x128_f8f6f4 v[114:117], v[2:9], v[206:213], v[114:117], v1, v1 op_sel_hi:[0,0,0]
	v_mfma_scale_f32_16x16x128_f8f6f4 v[106:109], v[10:17], v[206:213], v[106:109], v1, v1 op_sel_hi:[0,0,0]
	v_mfma_scale_f32_16x16x128_f8f6f4 v[102:105], v[2:9], v[214:221], v[102:105], v1, v1 op_sel_hi:[0,0,0]
	v_mfma_scale_f32_16x16x128_f8f6f4 v[98:101], v[10:17], v[214:221], v[98:101], v1, v1 op_sel_hi:[0,0,0]
	s_barrier
	s_add_i32 s42, s57, s46
	v_lshl_add_u64 v[182:183], s[40:41], 0, v[162:163]
	s_mov_b32 m0, s42
	ds_read_b128 v[198:201], v196 offset:16384
	ds_read_b128 v[202:205], v196 offset:17408
	ds_read_b128 v[206:209], v196 offset:18432
	ds_read_b128 v[210:213], v196 offset:19456
	ds_read_b128 v[214:217], v196 offset:20480
	ds_read_b128 v[218:221], v196 offset:21504
	ds_read_b128 v[222:225], v196 offset:22528
	ds_read_b128 v[226:229], v196 offset:23552
	global_load_lds_dwordx4 v[182:183], off
	s_add_i32 m0, s42, 0x2000
	s_add_u32 s42, s40, 0x40000
	v_lshl_add_u64 v[184:185], s[40:41], 0, v[164:165]
	s_addc_u32 s43, s41, 0
	s_add_i32 s75, s62, s46
	global_load_lds_dwordx4 v[184:185], off
	v_lshl_add_u64 v[186:187], s[42:43], 0, v[162:163]
	s_mov_b32 m0, s75
	s_nop 0
	global_load_lds_dwordx4 v[186:187], off
	v_lshl_add_u64 v[186:187], s[42:43], 0, v[164:165]
	s_add_i32 m0, s75, 0x2000
	s_and_b64 s[42:43], s[6:7], s[44:45]
	s_and_b64 s[42:43], s[42:43], exec
	s_cselect_b32 s42, s28, s36
	s_cselect_b32 s43, s29, s37
	s_add_u32 s42, s42, s74
	s_addc_u32 s43, s43, s71
	global_load_lds_dwordx4 v[186:187], off
	v_lshl_add_u64 v[186:187], s[42:43], 0, v[166:167]
	s_mov_b32 m0, s35
	v_lshl_add_u64 v[188:189], s[42:43], 0, v[168:169]
	global_load_lds_dwordx4 v[186:187], off
	s_mov_b32 m0, s47
	s_nop 0
	global_load_lds_dwordx4 v[188:189], off
	s_waitcnt vmcnt(8)
	s_waitcnt lgkmcnt(0)
	s_barrier
	v_mfma_scale_f32_16x16x128_f8f6f4 v[94:97], v[18:25], v[198:205], v[94:97], v1, v1 op_sel_hi:[0,0,0]
	v_mfma_scale_f32_16x16x128_f8f6f4 v[90:93], v[26:33], v[198:205], v[90:93], v1, v1 op_sel_hi:[0,0,0]
	v_mfma_scale_f32_16x16x128_f8f6f4 v[86:89], v[18:25], v[206:213], v[86:89], v1, v1 op_sel_hi:[0,0,0]
	v_mfma_scale_f32_16x16x128_f8f6f4 v[78:81], v[26:33], v[206:213], v[78:81], v1, v1 op_sel_hi:[0,0,0]
	v_mfma_scale_f32_16x16x128_f8f6f4 v[62:65], v[18:25], v[214:221], v[62:65], v1, v1 op_sel_hi:[0,0,0]
	v_mfma_scale_f32_16x16x128_f8f6f4 v[54:57], v[26:33], v[214:221], v[54:57], v1, v1 op_sel_hi:[0,0,0]
	v_mfma_scale_f32_16x16x128_f8f6f4 v[46:49], v[18:25], v[222:229], v[46:49], v1, v1 op_sel_hi:[0,0,0]
	v_mfma_scale_f32_16x16x128_f8f6f4 v[38:41], v[26:33], v[222:229], v[38:41], v1, v1 op_sel_hi:[0,0,0]
	v_mfma_scale_f32_16x16x128_f8f6f4 v[82:85], v[2:9], v[198:205], v[82:85], v1, v1 op_sel_hi:[0,0,0]
	v_mfma_scale_f32_16x16x128_f8f6f4 v[74:77], v[10:17], v[198:205], v[74:77], v1, v1 op_sel_hi:[0,0,0]
	v_mfma_scale_f32_16x16x128_f8f6f4 v[58:61], v[2:9], v[206:213], v[58:61], v1, v1 op_sel_hi:[0,0,0]
	v_mfma_scale_f32_16x16x128_f8f6f4 v[50:53], v[10:17], v[206:213], v[50:53], v1, v1 op_sel_hi:[0,0,0]
	v_mfma_scale_f32_16x16x128_f8f6f4 v[42:45], v[2:9], v[214:221], v[42:45], v1, v1 op_sel_hi:[0,0,0]
	v_mfma_scale_f32_16x16x128_f8f6f4 v[34:37], v[10:17], v[214:221], v[34:37], v1, v1 op_sel_hi:[0,0,0]
	v_mfma_scale_f32_16x16x128_f8f6f4 v[70:73], v[2:9], v[222:229], v[70:73], v1, v1 op_sel_hi:[0,0,0]
	v_mfma_scale_f32_16x16x128_f8f6f4 v[66:69], v[10:17], v[222:229], v[66:69], v1, v1 op_sel_hi:[0,0,0]
	s_barrier
; #define PG8_STAGE(bufoff, gbase, voff) do { _Pragma("unroll") for (int _i = 0; _i < 2; ++_i) \
;         __builtin_amdgcn_global_load_lds((const unsigned*)((const char*)(gbase) + (voff)[_i]), (LAS unsigned*)(lds + (bufoff) + ldsw + _i * 8192), 16, 0, 0); } while (0)
; #define PG8_LDA(dst, b, h) do { _Pragma("unroll") for (int m = 0; m < 4; ++m) dst[m] = PG8_LD32(lds + PG8_SA(b, h) + aoff + m * 2048); } while (0)
; #define PG8_LDB(dst, b, h) do { _Pragma("unroll") for (int n = 0; n < 2; ++n) dst[n] = PG8_LD32(lds + PG8_SB(b, h) + boff + n * 2048); } while (0)
; #define PG8_WAIT_V(n) asm volatile("s_waitcnt vmcnt(" #n ")" ::: "memory")
; #define PG8_WAIT_L(n) asm volatile("s_waitcnt lgkmcnt(" #n ")" ::: "memory")
; #define PG8_BAR __builtin_amdgcn_s_barrier()
; #define PG8_SCHED __builtin_amdgcn_sched_barrier(0)
; #define PG8_STA(bufoff, nextflag, h, koff) do { if constexpr (Sched::GATHER) { unsigned _o[2]; _o[0] = (nextflag) ? nxtA[h][0] : curA[h][0]; _o[1] = (nextflag) ? nxtA[h][1] : curA[h][1]; PG8_STAGE(bufoff, Ab + (koff), _o); } \
;         else { PG8_STAGE(bufoff, ((nextflag) ? nA : cA) + (size_t)(h) * hstep + (koff), voffA); } } while (0)
; template <class Epi, class Sched, bool ALIGN_EPI, int DT>
; __device__ __forceinline__ void gemm_phase(LAS unsigned char* lds, const int KB, const Sched& S, const Epi& E) {
;     ...
;             PG8_LDB(B0, 1, 0); PG8_LDB(B1, 1, 1); PG8_SCHED; PG8_LDA(At, 1, 0); PG8_STA(PG8_SA(0, 1), last, 1, k2);
;             PG8_WAIT_V(8); PG8_WAIT_L(0); PG8_BAR; PG8_MMA(0, 0, At, B0); PG8_MMA(0, 1, At, B1); PG8_BAR; PG8_SCHED;
;             PG8_LDA(At, 1, 1); PG8_STAGE(PG8_SB(1, 0), b3, voffB); PG8_STAGE(PG8_SB(1, 1), b3 + hstep, voffB); PG8_STA(PG8_SA(1, 0), last, 0, k3);
;             PG8_WAIT_V(8); PG8_WAIT_L(0); PG8_BAR; PG8_MMA(1, 0, At, B0); PG8_MMA(1, 1, At, B1); PG8_BAR; PG8_SCHED;
;         }
	s_add_i32 s44, 0, 0x18000
	s_add_i32 s45, 0, 0x1c000
	v_add_u32_e32 v14, s44, v191
	v_add_u32_e32 v30, s45, v191
	ds_read_b128 v[2:5], v14
	ds_read_b128 v[6:9], v14 offset:1024
	ds_read_b128 v[10:13], v14 offset:2048
	ds_read_b128 v[14:17], v14 offset:3072
	ds_read_b128 v[18:21], v30
	ds_read_b128 v[22:25], v30 offset:1024
	ds_read_b128 v[26:29], v30 offset:2048
	ds_read_b128 v[30:33], v30 offset:3072
	s_add_u32 s42, s42, 0x40000
	s_addc_u32 s43, s43, 0
	s_mov_b32 m0, s49
	v_lshl_add_u64 v[230:231], s[42:43], 0, v[166:167]
	ds_read_b128 v[198:201], v196 offset:32768
	ds_read_b128 v[202:205], v196 offset:33792
	ds_read_b128 v[206:209], v196 offset:34816
	ds_read_b128 v[210:213], v196 offset:35840
	ds_read_b128 v[214:217], v196 offset:36864
	ds_read_b128 v[218:221], v196 offset:37888
	ds_read_b128 v[222:225], v196 offset:38912
	ds_read_b128 v[226:229], v196 offset:39936
	global_load_lds_dwordx4 v[230:231], off
	v_lshl_add_u64 v[230:231], s[42:43], 0, v[168:169]
	s_mov_b32 m0, s52
	s_nop 0
	global_load_lds_dwordx4 v[230:231], off
	s_waitcnt vmcnt(8)
	s_waitcnt lgkmcnt(0)
	s_barrier
	v_mfma_scale_f32_16x16x128_f8f6f4 v[158:161], v[2:9], v[198:205], v[158:161], v1, v1 op_sel_hi:[0,0,0]
	v_mfma_scale_f32_16x16x128_f8f6f4 v[154:157], v[10:17], v[198:205], v[154:157], v1, v1 op_sel_hi:[0,0,0]
	v_mfma_scale_f32_16x16x128_f8f6f4 v[150:153], v[2:9], v[206:213], v[150:153], v1, v1 op_sel_hi:[0,0,0]
	v_mfma_scale_f32_16x16x128_f8f6f4 v[142:145], v[10:17], v[206:213], v[142:145], v1, v1 op_sel_hi:[0,0,0]
	v_mfma_scale_f32_16x16x128_f8f6f4 v[134:137], v[2:9], v[214:221], v[134:137], v1, v1 op_sel_hi:[0,0,0]
	v_mfma_scale_f32_16x16x128_f8f6f4 v[126:129], v[10:17], v[214:221], v[126:129], v1, v1 op_sel_hi:[0,0,0]
	v_mfma_scale_f32_16x16x128_f8f6f4 v[118:121], v[2:9], v[222:229], v[118:121], v1, v1 op_sel_hi:[0,0,0]
	v_mfma_scale_f32_16x16x128_f8f6f4 v[110:113], v[10:17], v[222:229], v[110:113], v1, v1 op_sel_hi:[0,0,0]
	v_mfma_scale_f32_16x16x128_f8f6f4 v[146:149], v[18:25], v[198:205], v[146:149], v1, v1 op_sel_hi:[0,0,0]
	v_mfma_scale_f32_16x16x128_f8f6f4 v[138:141], v[26:33], v[198:205], v[138:141], v1, v1 op_sel_hi:[0,0,0]
	v_mfma_scale_f32_16x16x128_f8f6f4 v[130:133], v[18:25], v[206:213], v[130:133], v1, v1 op_sel_hi:[0,0,0]
	v_mfma_scale_f32_16x16x128_f8f6f4 v[122:125], v[26:33], v[206:213], v[122:125], v1, v1 op_sel_hi:[0,0,0]
	v_mfma_scale_f32_16x16x128_f8f6f4 v[114:117], v[18:25], v[214:221], v[114:117], v1, v1 op_sel_hi:[0,0,0]
	v_mfma_scale_f32_16x16x128_f8f6f4 v[106:109], v[26:33], v[214:221], v[106:109], v1, v1 op_sel_hi:[0,0,0]
	v_mfma_scale_f32_16x16x128_f8f6f4 v[102:105], v[18:25], v[222:229], v[102:105], v1, v1 op_sel_hi:[0,0,0]
	v_mfma_scale_f32_16x16x128_f8f6f4 v[98:101], v[26:33], v[222:229], v[98:101], v1, v1 op_sel_hi:[0,0,0]
	s_barrier
	s_add_i32 s42, s44, s46
	v_lshl_add_u64 v[182:183], v[182:183], 0, s[10:11]
	s_mov_b32 m0, s42
	ds_read_b128 v[198:201], v196 offset:49152
	ds_read_b128 v[202:205], v196 offset:50176
	ds_read_b128 v[206:209], v196 offset:51200
	ds_read_b128 v[210:213], v196 offset:52224
	ds_read_b128 v[214:217], v196 offset:53248
	ds_read_b128 v[218:221], v196 offset:54272
	ds_read_b128 v[222:225], v196 offset:55296
	ds_read_b128 v[226:229], v196 offset:56320
	global_load_lds_dwordx4 v[182:183], off
	s_add_i32 m0, s42, 0x2000
	s_add_u32 s40, s40, 0x40080
	v_lshl_add_u64 v[182:183], v[184:185], 0, s[10:11]
	s_addc_u32 s41, s41, 0
	s_add_i32 s42, s45, s46
	global_load_lds_dwordx4 v[182:183], off
	v_lshl_add_u64 v[182:183], s[40:41], 0, v[162:163]
	s_mov_b32 m0, s42
	s_nop 0
	global_load_lds_dwordx4 v[182:183], off
	v_lshl_add_u64 v[182:183], s[40:41], 0, v[164:165]
	s_add_i32 m0, s42, 0x2000
	s_nop 0
	global_load_lds_dwordx4 v[182:183], off
	v_lshl_add_u64 v[182:183], v[186:187], 0, s[10:11]
	s_mov_b32 m0, s54
	s_nop 0
	global_load_lds_dwordx4 v[182:183], off
	v_lshl_add_u64 v[182:183], v[188:189], 0, s[10:11]
	s_mov_b32 m0, s55
	s_nop 0
	global_load_lds_dwordx4 v[182:183], off
	s_waitcnt vmcnt(8)
	s_waitcnt lgkmcnt(0)
	s_barrier
	v_mfma_scale_f32_16x16x128_f8f6f4 v[94:97], v[2:9], v[198:205], v[94:97], v1, v1 op_sel_hi:[0,0,0]
	v_mfma_scale_f32_16x16x128_f8f6f4 v[90:93], v[10:17], v[198:205], v[90:93], v1, v1 op_sel_hi:[0,0,0]
	v_mfma_scale_f32_16x16x128_f8f6f4 v[86:89], v[2:9], v[206:213], v[86:89], v1, v1 op_sel_hi:[0,0,0]
	v_mfma_scale_f32_16x16x128_f8f6f4 v[78:81], v[10:17], v[206:213], v[78:81], v1, v1 op_sel_hi:[0,0,0]
	v_mfma_scale_f32_16x16x128_f8f6f4 v[62:65], v[2:9], v[214:221], v[62:65], v1, v1 op_sel_hi:[0,0,0]
	v_mfma_scale_f32_16x16x128_f8f6f4 v[54:57], v[10:17], v[214:221], v[54:57], v1, v1 op_sel_hi:[0,0,0]
	v_mfma_scale_f32_16x16x128_f8f6f4 v[46:49], v[2:9], v[222:229], v[46:49], v1, v1 op_sel_hi:[0,0,0]
	v_mfma_scale_f32_16x16x128_f8f6f4 v[38:41], v[10:17], v[222:229], v[38:41], v1, v1 op_sel_hi:[0,0,0]
	v_mfma_scale_f32_16x16x128_f8f6f4 v[82:85], v[18:25], v[198:205], v[82:85], v1, v1 op_sel_hi:[0,0,0]
	v_mfma_scale_f32_16x16x128_f8f6f4 v[74:77], v[26:33], v[198:205], v[74:77], v1, v1 op_sel_hi:[0,0,0]
	v_mfma_scale_f32_16x16x128_f8f6f4 v[58:61], v[18:25], v[206:213], v[58:61], v1, v1 op_sel_hi:[0,0,0]
	v_mfma_scale_f32_16x16x128_f8f6f4 v[50:53], v[26:33], v[206:213], v[50:53], v1, v1 op_sel_hi:[0,0,0]
	v_mfma_scale_f32_16x16x128_f8f6f4 v[42:45], v[18:25], v[214:221], v[42:45], v1, v1 op_sel_hi:[0,0,0]
	v_mfma_scale_f32_16x16x128_f8f6f4 v[34:37], v[26:33], v[214:221], v[34:37], v1, v1 op_sel_hi:[0,0,0]
	v_mfma_scale_f32_16x16x128_f8f6f4 v[70:73], v[18:25], v[222:229], v[70:73], v1, v1 op_sel_hi:[0,0,0]
	v_mfma_scale_f32_16x16x128_f8f6f4 v[66:69], v[26:33], v[222:229], v[66:69], v1, v1 op_sel_hi:[0,0,0]
	s_barrier
	s_add_i32 s70, s70, 2
	s_cmp_gt_u32 s70, 13
	s_mov_b64 s[42:43], s[38:39]
	s_cbranch_scc0 .LBB0_2108
	s_and_b64 vcc, exec, s[12:13]
	s_cbranch_vccz .LBB0_2111
	s_barrier

; #define PG8_STAGE(bufoff, gbase, voff) do { _Pragma("unroll") for (int _i = 0; _i < 2; ++_i) \
;         __builtin_amdgcn_global_load_lds((const unsigned*)((const char*)(gbase) + (voff)[_i]), (LAS unsigned*)(lds + (bufoff) + ldsw + _i * 8192), 16, 0, 0); } while (0)
; #define PG8_LDA(dst, b, h) do { _Pragma("unroll") for (int m = 0; m < 4; ++m) dst[m] = PG8_LD32(lds + PG8_SA(b, h) + aoff + m * 2048); } while (0)
; #define PG8_LDB(dst, b, h) do { _Pragma("unroll") for (int n = 0; n < 2; ++n) dst[n] = PG8_LD32(lds + PG8_SB(b, h) + boff + n * 2048); } while (0)
; #define PG8_WAIT_V(n) asm volatile("s_waitcnt vmcnt(" #n ")" ::: "memory")
; #define PG8_WAIT_L(n) asm volatile("s_waitcnt lgkmcnt(" #n ")" ::: "memory")
; #define PG8_BAR __builtin_amdgcn_s_barrier()
; #define PG8_SCHED __builtin_amdgcn_sched_barrier(0)
; #define PG8_STA(bufoff, nextflag, h, koff) do { if constexpr (Sched::GATHER) { unsigned _o[2]; _o[0] = (nextflag) ? nxtA[h][0] : curA[h][0]; _o[1] = (nextflag) ? nxtA[h][1] : curA[h][1]; PG8_STAGE(bufoff, Ab + (koff), _o); } \
;         else { PG8_STAGE(bufoff, ((nextflag) ? nA : cA) + (size_t)(h) * hstep + (koff), voffA); } } while (0)
; template <class Epi, class Sched, bool ALIGN_EPI, int DT>
; __device__ __forceinline__ void gemm_phase(LAS unsigned char* lds, const int KB, const Sched& S, const Epi& E) {
;     ...
;             const size_t k1 = (size_t)(t + 1) * kstep, k2 = last ? 0 : (size_t)(t + 2) * kstep, k3 = k2 + kstep;
;             const char* b2 = last ? nB : cB + (size_t)(t + 2) * kstep; const char* b3 = b2 + kstep;
;             PG8_LDB(B0, 0, 0); PG8_LDB(B1, 0, 1); PG8_SCHED; PG8_LDA(At, 0, 0); PG8_STA(PG8_SA(1, 1), false, 1, k1);
;             PG8_WAIT_V(8); PG8_WAIT_L(0); PG8_BAR; PG8_MMA(0, 0, At, B0); PG8_MMA(0, 1, At, B1); PG8_BAR; PG8_SCHED;
;             PG8_LDA(At, 0, 1); PG8_STAGE(PG8_SB(0, 0), b2, voffB); PG8_STAGE(PG8_SB(0, 1), b2 + hstep, voffB); PG8_STA(PG8_SA(0, 0), last, 0, k2);
;             PG8_WAIT_V(8); PG8_WAIT_L(0); PG8_BAR; PG8_MMA(1, 0, At, B0); PG8_MMA(1, 1, At, B1); PG8_BAR; PG8_SCHED;
.LBB0_2294:
	v_add_u32_e32 v79, s65, v167
	ds_read_b128 v[142:145], v79
	ds_read_b128 v[156:159], v79 offset:1024
	ds_read_b128 v[178:181], v79 offset:2048
	ds_read_b128 v[182:185], v79 offset:3072
	v_add_u32_e32 v79, s66, v167
	ds_read_b128 v[186:189], v79
	ds_read_b128 v[190:193], v79 offset:1024
	ds_read_b128 v[196:199], v79 offset:2048
	ds_read_b128 v[200:203], v79 offset:3072
	s_add_u32 s40, s8, 0x100
	s_addc_u32 s41, s9, 0
	s_cmpk_eq_i32 s8, 0x700
	s_cselect_b64 vcc, -1, 0
	v_lshl_add_u64 v[160:161], v[88:89], 0, s[8:9]
	s_and_b64 s[76:77], vcc, exec
	v_cndmask_b32_e32 v161, v161, v155, vcc
	s_cselect_b32 s75, 0, s40
	v_cndmask_b32_e32 v160, v160, v154, vcc
	v_lshl_add_u64 v[236:237], v[140:141], 0, s[8:9]
	s_add_i32 m0, s42, 0xc000
	ds_read_b128 v[204:207], v169
	ds_read_b128 v[208:211], v169 offset:1024
	ds_read_b128 v[212:215], v169 offset:2048
	ds_read_b128 v[216:219], v169 offset:3072
	ds_read_b128 v[220:223], v169 offset:4096
	ds_read_b128 v[224:227], v169 offset:5120
	ds_read_b128 v[228:231], v169 offset:6144
	ds_read_b128 v[232:235], v169 offset:7168
	global_load_lds_dwordx4 v[236:237], off
	v_lshl_add_u64 v[236:237], v[138:139], 0, s[8:9]
	s_add_i32 m0, s42, 0xe000
	s_nop 0
	global_load_lds_dwordx4 v[236:237], off
	s_waitcnt vmcnt(8)
	s_waitcnt lgkmcnt(0)
	s_barrier
	v_mfma_i32_16x16x64_i8 v[134:137], v[142:145], v[204:207], v[134:137]
	v_mfma_i32_16x16x64_i8 v[126:129], v[178:181], v[204:207], v[126:129]
	v_mfma_i32_16x16x64_i8 v[118:121], v[142:145], v[212:215], v[118:121]
	v_mfma_i32_16x16x64_i8 v[110:113], v[178:181], v[212:215], v[110:113]
	v_mfma_i32_16x16x64_i8 v[102:105], v[142:145], v[220:223], v[102:105]
	v_mfma_i32_16x16x64_i8 v[94:97], v[178:181], v[220:223], v[94:97]
	v_mfma_i32_16x16x64_i8 v[82:85], v[142:145], v[228:231], v[82:85]
	v_mfma_i32_16x16x64_i8 v[70:73], v[178:181], v[228:231], v[70:73]
	v_mfma_i32_16x16x64_i8 v[134:137], v[156:159], v[208:211], v[134:137]
	v_mfma_i32_16x16x64_i8 v[126:129], v[182:185], v[208:211], v[126:129]
	v_mfma_i32_16x16x64_i8 v[118:121], v[156:159], v[216:219], v[118:121]
	v_mfma_i32_16x16x64_i8 v[110:113], v[182:185], v[216:219], v[110:113]
	v_mfma_i32_16x16x64_i8 v[102:105], v[156:159], v[224:227], v[102:105]
	v_mfma_i32_16x16x64_i8 v[94:97], v[182:185], v[224:227], v[94:97]
	v_mfma_i32_16x16x64_i8 v[82:85], v[156:159], v[232:235], v[82:85]
	v_mfma_i32_16x16x64_i8 v[70:73], v[182:185], v[232:235], v[70:73]
	v_mfma_i32_16x16x64_i8 v[130:133], v[186:189], v[204:207], v[130:133]
	v_mfma_i32_16x16x64_i8 v[122:125], v[196:199], v[204:207], v[122:125]
	v_mfma_i32_16x16x64_i8 v[114:117], v[186:189], v[212:215], v[114:117]
	v_mfma_i32_16x16x64_i8 v[106:109], v[196:199], v[212:215], v[106:109]
	v_mfma_i32_16x16x64_i8 v[98:101], v[186:189], v[220:223], v[98:101]
	v_mfma_i32_16x16x64_i8 v[90:93], v[196:199], v[220:223], v[90:93]
	v_mfma_i32_16x16x64_i8 v[74:77], v[186:189], v[228:231], v[74:77]
	v_mfma_i32_16x16x64_i8 v[66:69], v[196:199], v[228:231], v[66:69]
	v_mfma_i32_16x16x64_i8 v[130:133], v[190:193], v[208:211], v[130:133]
	v_mfma_i32_16x16x64_i8 v[122:125], v[200:203], v[208:211], v[122:125]
	v_mfma_i32_16x16x64_i8 v[114:117], v[190:193], v[216:219], v[114:117]
	v_mfma_i32_16x16x64_i8 v[106:109], v[200:203], v[216:219], v[106:109]
	v_mfma_i32_16x16x64_i8 v[98:101], v[190:193], v[224:227], v[98:101]
	v_mfma_i32_16x16x64_i8 v[90:93], v[200:203], v[224:227], v[90:93]
	v_mfma_i32_16x16x64_i8 v[74:77], v[190:193], v[232:235], v[74:77]
	v_mfma_i32_16x16x64_i8 v[66:69], v[200:203], v[232:235], v[66:69]
	s_barrier
	s_add_i32 s8, s65, s33
	v_lshl_add_u64 v[236:237], v[160:161], 0, v[148:149]
	s_mov_b32 m0, s8
	ds_read_b128 v[204:207], v169 offset:16384
	ds_read_b128 v[208:211], v169 offset:17408
	ds_read_b128 v[212:215], v169 offset:18432
	ds_read_b128 v[216:219], v169 offset:19456
	ds_read_b128 v[220:223], v169 offset:20480
	ds_read_b128 v[224:227], v169 offset:21504
	ds_read_b128 v[228:231], v169 offset:22528
	ds_read_b128 v[232:235], v169 offset:23552
	global_load_lds_dwordx4 v[236:237], off
	v_lshl_add_u64 v[238:239], v[160:161], 0, v[150:151]
	s_add_i32 m0, s8, 0x2000
	v_lshl_add_u64 v[240:241], v[160:161], 0, s[10:11]
	s_add_i32 s8, s66, s33
	global_load_lds_dwordx4 v[238:239], off
	v_lshl_add_u64 v[242:243], v[240:241], 0, v[148:149]
	s_mov_b32 m0, s8
	v_lshl_add_u64 v[240:241], v[240:241], 0, v[150:151]
	global_load_lds_dwordx4 v[242:243], off
	s_add_i32 m0, s8, 0x2000
	s_add_u32 s8, s60, s75
	global_load_lds_dwordx4 v[240:241], off
	v_cndmask_b32_e32 v146, v81, v173, vcc
	s_addc_u32 s9, s61, 0
	s_mov_b32 m0, s42
	v_cndmask_b32_e32 v240, v80, v174, vcc
	global_load_lds_dwordx4 v146, s[8:9]
	s_mov_b32 m0, s43
	v_mov_b32_e32 v241, v147
	global_load_lds_dwordx4 v240, s[8:9]
	s_waitcnt vmcnt(8)
	s_waitcnt lgkmcnt(0)
	v_lshl_add_u64 v[242:243], s[8:9], 0, v[146:147]
	v_lshl_add_u64 v[240:241], s[8:9], 0, v[240:241]
	s_barrier
; #define PG8_LDA(dst, b, h) do { _Pragma("unroll") for (int m = 0; m < 4; ++m) dst[m] = PG8_LD32(lds + PG8_SA(b, h) + aoff + m * 2048); } while (0)
; #define PG8_LDB(dst, b, h) do { _Pragma("unroll") for (int n = 0; n < 2; ++n) dst[n] = PG8_LD32(lds + PG8_SB(b, h) + boff + n * 2048); } while (0)
; #define PG8_WAIT_V(n) asm volatile("s_waitcnt vmcnt(" #n ")" ::: "memory")
; #define PG8_WAIT_L(n) asm volatile("s_waitcnt lgkmcnt(" #n ")" ::: "memory")
; #define PG8_BAR __builtin_amdgcn_s_barrier()
; #define PG8_SCHED __builtin_amdgcn_sched_barrier(0)
; #define PG8_STA(bufoff, nextflag, h, koff) do { if constexpr (Sched::GATHER) { unsigned _o[2]; _o[0] = (nextflag) ? nxtA[h][0] : curA[h][0]; _o[1] = (nextflag) ? nxtA[h][1] : curA[h][1]; PG8_STAGE(bufoff, Ab + (koff), _o); } \
;         else { PG8_STAGE(bufoff, ((nextflag) ? nA : cA) + (size_t)(h) * hstep + (koff), voffA); } } while (0)
; template <class Epi, class Sched, bool ALIGN_EPI, int DT>
; __device__ __forceinline__ void gemm_phase(LAS unsigned char* lds, const int KB, const Sched& S, const Epi& E) {
;     ...
;             PG8_WAIT_V(8); PG8_WAIT_L(0); PG8_BAR; PG8_MMA(1, 0, At, B0); PG8_MMA(1, 1, At, B1); PG8_BAR; PG8_SCHED;
;             PG8_LDB(B0, 1, 0); PG8_LDB(B1, 1, 1); PG8_SCHED; PG8_LDA(At, 1, 0); PG8_STA(PG8_SA(0, 1), last, 1, k2);
;             PG8_WAIT_V(8); PG8_WAIT_L(0); PG8_BAR; PG8_MMA(0, 0, At, B0); PG8_MMA(0, 1, At, B1); PG8_BAR; PG8_SCHED;
	v_mfma_i32_16x16x64_i8 v[54:57], v[142:145], v[204:207], v[54:57]
	v_mfma_i32_16x16x64_i8 v[50:53], v[178:181], v[204:207], v[50:53]
	v_mfma_i32_16x16x64_i8 v[42:45], v[142:145], v[212:215], v[42:45]
	v_mfma_i32_16x16x64_i8 v[34:37], v[178:181], v[212:215], v[34:37]
	v_mfma_i32_16x16x64_i8 v[26:29], v[142:145], v[220:223], v[26:29]
	v_mfma_i32_16x16x64_i8 v[18:21], v[178:181], v[220:223], v[18:21]
	v_mfma_i32_16x16x64_i8 v[10:13], v[142:145], v[228:231], v[10:13]
	v_mfma_i32_16x16x64_i8 v[2:5], v[178:181], v[228:231], v[2:5]
	v_mfma_i32_16x16x64_i8 v[54:57], v[156:159], v[208:211], v[54:57]
	v_mfma_i32_16x16x64_i8 v[50:53], v[182:185], v[208:211], v[50:53]
	v_mfma_i32_16x16x64_i8 v[42:45], v[156:159], v[216:219], v[42:45]
	v_mfma_i32_16x16x64_i8 v[34:37], v[182:185], v[216:219], v[34:37]
	v_mfma_i32_16x16x64_i8 v[26:29], v[156:159], v[224:227], v[26:29]
	v_mfma_i32_16x16x64_i8 v[18:21], v[182:185], v[224:227], v[18:21]
	v_mfma_i32_16x16x64_i8 v[10:13], v[156:159], v[232:235], v[10:13]
	v_mfma_i32_16x16x64_i8 v[2:5], v[182:185], v[232:235], v[2:5]
	v_mfma_i32_16x16x64_i8 v[62:65], v[186:189], v[204:207], v[62:65]
	v_mfma_i32_16x16x64_i8 v[58:61], v[196:199], v[204:207], v[58:61]
	v_mfma_i32_16x16x64_i8 v[46:49], v[186:189], v[212:215], v[46:49]
	v_mfma_i32_16x16x64_i8 v[38:41], v[196:199], v[212:215], v[38:41]
	v_mfma_i32_16x16x64_i8 v[30:33], v[186:189], v[220:223], v[30:33]
	v_mfma_i32_16x16x64_i8 v[22:25], v[196:199], v[220:223], v[22:25]
	v_mfma_i32_16x16x64_i8 v[14:17], v[186:189], v[228:231], v[14:17]
	v_mfma_i32_16x16x64_i8 v[6:9], v[196:199], v[228:231], v[6:9]
	v_mfma_i32_16x16x64_i8 v[62:65], v[190:193], v[208:211], v[62:65]
	v_mfma_i32_16x16x64_i8 v[58:61], v[200:203], v[208:211], v[58:61]
	v_mfma_i32_16x16x64_i8 v[46:49], v[190:193], v[216:219], v[46:49]
	v_mfma_i32_16x16x64_i8 v[38:41], v[200:203], v[216:219], v[38:41]
	v_mfma_i32_16x16x64_i8 v[30:33], v[190:193], v[224:227], v[30:33]
	v_mfma_i32_16x16x64_i8 v[22:25], v[200:203], v[224:227], v[22:25]
	v_mfma_i32_16x16x64_i8 v[14:17], v[190:193], v[232:235], v[14:17]
	v_mfma_i32_16x16x64_i8 v[6:9], v[200:203], v[232:235], v[6:9]
	s_barrier
	s_add_i32 s75, 0, 0x18000
	v_add_u32_e32 v79, s75, v167
	s_add_i32 s76, 0, 0x1c000
	ds_read_b128 v[142:145], v79
	ds_read_b128 v[156:159], v79 offset:1024
	ds_read_b128 v[178:181], v79 offset:2048
	ds_read_b128 v[182:185], v79 offset:3072
	v_add_u32_e32 v79, s76, v167
	ds_read_b128 v[186:189], v79
	ds_read_b128 v[190:193], v79 offset:1024
	ds_read_b128 v[196:199], v79 offset:2048
	ds_read_b128 v[200:203], v79 offset:3072
	s_mov_b32 m0, s44
	v_cndmask_b32_e32 v79, v78, v175, vcc
	ds_read_b128 v[204:207], v169 offset:32768
	ds_read_b128 v[208:211], v169 offset:33792
	ds_read_b128 v[212:215], v169 offset:34816
	ds_read_b128 v[216:219], v169 offset:35840
	ds_read_b128 v[220:223], v169 offset:36864
	ds_read_b128 v[224:227], v169 offset:37888
	ds_read_b128 v[228:231], v169 offset:38912
	ds_read_b128 v[232:235], v169 offset:39936
	v_cndmask_b32_e32 v87, v86, v176, vcc
	global_load_lds_dwordx4 v79, s[8:9]
	s_mov_b32 m0, s45
	s_nop 0
	global_load_lds_dwordx4 v87, s[8:9]
	s_waitcnt vmcnt(8)
	s_waitcnt lgkmcnt(0)
	s_barrier
	v_mfma_i32_16x16x64_i8 v[134:137], v[142:145], v[204:207], v[134:137]
	v_mfma_i32_16x16x64_i8 v[126:129], v[178:181], v[204:207], v[126:129]
	v_mfma_i32_16x16x64_i8 v[118:121], v[142:145], v[212:215], v[118:121]
	v_mfma_i32_16x16x64_i8 v[110:113], v[178:181], v[212:215], v[110:113]
	v_mfma_i32_16x16x64_i8 v[102:105], v[142:145], v[220:223], v[102:105]
	v_mfma_i32_16x16x64_i8 v[94:97], v[178:181], v[220:223], v[94:97]
	v_mfma_i32_16x16x64_i8 v[82:85], v[142:145], v[228:231], v[82:85]
	v_mfma_i32_16x16x64_i8 v[70:73], v[178:181], v[228:231], v[70:73]
	v_mfma_i32_16x16x64_i8 v[134:137], v[156:159], v[208:211], v[134:137]
	v_mfma_i32_16x16x64_i8 v[126:129], v[182:185], v[208:211], v[126:129]
	v_mfma_i32_16x16x64_i8 v[118:121], v[156:159], v[216:219], v[118:121]
	v_mfma_i32_16x16x64_i8 v[110:113], v[182:185], v[216:219], v[110:113]
	v_mfma_i32_16x16x64_i8 v[102:105], v[156:159], v[224:227], v[102:105]
	v_mfma_i32_16x16x64_i8 v[94:97], v[182:185], v[224:227], v[94:97]
	v_mfma_i32_16x16x64_i8 v[82:85], v[156:159], v[232:235], v[82:85]
	v_mfma_i32_16x16x64_i8 v[70:73], v[182:185], v[232:235], v[70:73]
	v_mfma_i32_16x16x64_i8 v[130:133], v[186:189], v[204:207], v[130:133]
	v_mfma_i32_16x16x64_i8 v[122:125], v[196:199], v[204:207], v[122:125]
	v_mfma_i32_16x16x64_i8 v[114:117], v[186:189], v[212:215], v[114:117]
	v_mfma_i32_16x16x64_i8 v[106:109], v[196:199], v[212:215], v[106:109]
	v_mfma_i32_16x16x64_i8 v[98:101], v[186:189], v[220:223], v[98:101]
	v_mfma_i32_16x16x64_i8 v[90:93], v[196:199], v[220:223], v[90:93]
	v_mfma_i32_16x16x64_i8 v[74:77], v[186:189], v[228:231], v[74:77]
	v_mfma_i32_16x16x64_i8 v[66:69], v[196:199], v[228:231], v[66:69]
	v_mfma_i32_16x16x64_i8 v[130:133], v[190:193], v[208:211], v[130:133]
	v_mfma_i32_16x16x64_i8 v[122:125], v[200:203], v[208:211], v[122:125]
	v_mfma_i32_16x16x64_i8 v[114:117], v[190:193], v[216:219], v[114:117]
	v_mfma_i32_16x16x64_i8 v[106:109], v[200:203], v[216:219], v[106:109]
	v_mfma_i32_16x16x64_i8 v[98:101], v[190:193], v[224:227], v[98:101]
	v_mfma_i32_16x16x64_i8 v[90:93], v[200:203], v[224:227], v[90:93]
	v_mfma_i32_16x16x64_i8 v[74:77], v[190:193], v[232:235], v[74:77]
	v_mfma_i32_16x16x64_i8 v[66:69], v[200:203], v[232:235], v[66:69]
	s_barrier
; #define PG8_STAGE(bufoff, gbase, voff) do { _Pragma("unroll") for (int _i = 0; _i < 2; ++_i) \
;         __builtin_amdgcn_global_load_lds((const unsigned*)((const char*)(gbase) + (voff)[_i]), (LAS unsigned*)(lds + (bufoff) + ldsw + _i * 8192), 16, 0, 0); } while (0)
; #define PG8_LDA(dst, b, h) do { _Pragma("unroll") for (int m = 0; m < 4; ++m) dst[m] = PG8_LD32(lds + PG8_SA(b, h) + aoff + m * 2048); } while (0)
; #define PG8_WAIT_V(n) asm volatile("s_waitcnt vmcnt(" #n ")" ::: "memory")
; #define PG8_WAIT_L(n) asm volatile("s_waitcnt lgkmcnt(" #n ")" ::: "memory")
; #define PG8_BAR __builtin_amdgcn_s_barrier()
; #define PG8_SCHED __builtin_amdgcn_sched_barrier(0)
; #define PG8_STA(bufoff, nextflag, h, koff) do { if constexpr (Sched::GATHER) { unsigned _o[2]; _o[0] = (nextflag) ? nxtA[h][0] : curA[h][0]; _o[1] = (nextflag) ? nxtA[h][1] : curA[h][1]; PG8_STAGE(bufoff, Ab + (koff), _o); } \
;         else { PG8_STAGE(bufoff, ((nextflag) ? nA : cA) + (size_t)(h) * hstep + (koff), voffA); } } while (0)
; template <class Epi, class Sched, bool ALIGN_EPI, int DT>
; __device__ __forceinline__ void gemm_phase(LAS unsigned char* lds, const int KB, const Sched& S, const Epi& E) {
;     ...
;             PG8_LDA(At, 1, 1); PG8_STAGE(PG8_SB(1, 0), b3, voffB); PG8_STAGE(PG8_SB(1, 1), b3 + hstep, voffB); PG8_STA(PG8_SA(1, 0), last, 0, k3);
;             PG8_WAIT_V(8); PG8_WAIT_L(0); PG8_BAR; PG8_MMA(1, 0, At, B0); PG8_MMA(1, 1, At, B1); PG8_BAR; PG8_SCHED;
;         }
	s_add_i32 s8, s75, s33
	v_lshl_add_u64 v[236:237], v[236:237], 0, s[20:21]
	s_mov_b32 m0, s8
	ds_read_b128 v[204:207], v169 offset:49152
	ds_read_b128 v[208:211], v169 offset:50176
	ds_read_b128 v[212:215], v169 offset:51200
	ds_read_b128 v[216:219], v169 offset:52224
	ds_read_b128 v[220:223], v169 offset:53248
	ds_read_b128 v[224:227], v169 offset:54272
	ds_read_b128 v[228:231], v169 offset:55296
	ds_read_b128 v[232:235], v169 offset:56320
	global_load_lds_dwordx4 v[236:237], off
	v_lshl_add_u64 v[236:237], v[238:239], 0, s[20:21]
	s_add_i32 m0, s8, 0x2000
	v_lshl_add_u64 v[160:161], v[160:161], 0, s[24:25]
	s_add_i32 s8, s76, s33
	global_load_lds_dwordx4 v[236:237], off
	v_lshl_add_u64 v[236:237], v[160:161], 0, v[148:149]
	s_mov_b32 m0, s8
	v_lshl_add_u64 v[160:161], v[160:161], 0, v[150:151]
	global_load_lds_dwordx4 v[236:237], off
	s_add_i32 m0, s8, 0x2000
	s_nop 0
	global_load_lds_dwordx4 v[160:161], off
	v_lshl_add_u64 v[160:161], v[242:243], 0, s[20:21]
	s_mov_b32 m0, s46
	s_nop 0
	global_load_lds_dwordx4 v[160:161], off
	v_lshl_add_u64 v[160:161], v[240:241], 0, s[20:21]
	s_mov_b32 m0, s47
	s_nop 0
	global_load_lds_dwordx4 v[160:161], off
	s_waitcnt vmcnt(8)
	s_waitcnt lgkmcnt(0)
	s_barrier
	v_mfma_i32_16x16x64_i8 v[54:57], v[142:145], v[204:207], v[54:57]
	v_mfma_i32_16x16x64_i8 v[50:53], v[178:181], v[204:207], v[50:53]
	v_mfma_i32_16x16x64_i8 v[42:45], v[142:145], v[212:215], v[42:45]
	v_mfma_i32_16x16x64_i8 v[34:37], v[178:181], v[212:215], v[34:37]
	v_mfma_i32_16x16x64_i8 v[26:29], v[142:145], v[220:223], v[26:29]
	v_mfma_i32_16x16x64_i8 v[18:21], v[178:181], v[220:223], v[18:21]
	v_mfma_i32_16x16x64_i8 v[10:13], v[142:145], v[228:231], v[10:13]
	v_mfma_i32_16x16x64_i8 v[2:5], v[178:181], v[228:231], v[2:5]
	v_mfma_i32_16x16x64_i8 v[54:57], v[156:159], v[208:211], v[54:57]
	v_mfma_i32_16x16x64_i8 v[50:53], v[182:185], v[208:211], v[50:53]
	v_mfma_i32_16x16x64_i8 v[42:45], v[156:159], v[216:219], v[42:45]
	v_mfma_i32_16x16x64_i8 v[34:37], v[182:185], v[216:219], v[34:37]
	v_mfma_i32_16x16x64_i8 v[26:29], v[156:159], v[224:227], v[26:29]
	v_mfma_i32_16x16x64_i8 v[18:21], v[182:185], v[224:227], v[18:21]
	v_mfma_i32_16x16x64_i8 v[10:13], v[156:159], v[232:235], v[10:13]
	v_mfma_i32_16x16x64_i8 v[2:5], v[182:185], v[232:235], v[2:5]
	v_mfma_i32_16x16x64_i8 v[62:65], v[186:189], v[204:207], v[62:65]
	v_mfma_i32_16x16x64_i8 v[58:61], v[196:199], v[204:207], v[58:61]
	v_mfma_i32_16x16x64_i8 v[46:49], v[186:189], v[212:215], v[46:49]
	v_mfma_i32_16x16x64_i8 v[38:41], v[196:199], v[212:215], v[38:41]
	v_mfma_i32_16x16x64_i8 v[30:33], v[186:189], v[220:223], v[30:33]
	v_mfma_i32_16x16x64_i8 v[22:25], v[196:199], v[220:223], v[22:25]
	v_mfma_i32_16x16x64_i8 v[14:17], v[186:189], v[228:231], v[14:17]
	v_mfma_i32_16x16x64_i8 v[6:9], v[196:199], v[228:231], v[6:9]
	v_mfma_i32_16x16x64_i8 v[62:65], v[190:193], v[208:211], v[62:65]
	v_mfma_i32_16x16x64_i8 v[58:61], v[200:203], v[208:211], v[58:61]
	v_mfma_i32_16x16x64_i8 v[46:49], v[190:193], v[216:219], v[46:49]
	v_mfma_i32_16x16x64_i8 v[38:41], v[200:203], v[216:219], v[38:41]
	v_mfma_i32_16x16x64_i8 v[30:33], v[190:193], v[224:227], v[30:33]
	v_mfma_i32_16x16x64_i8 v[22:25], v[200:203], v[224:227], v[22:25]
	v_mfma_i32_16x16x64_i8 v[14:17], v[190:193], v[232:235], v[14:17]
	v_mfma_i32_16x16x64_i8 v[6:9], v[200:203], v[232:235], v[6:9]
	s_barrier
	s_add_i32 s37, s37, 2
	s_cmp_gt_u32 s37, 13
	s_mov_b64 s[8:9], s[40:41]
	s_cbranch_scc0 .LBB0_2294
	s_and_b64 vcc, exec, s[26:27]
	s_cbranch_vccz .LBB0_2297
	s_barrier

; #define PG8_STAGE(bufoff, gbase, voff) do { _Pragma("unroll") for (int _i = 0; _i < 2; ++_i) \
;         __builtin_amdgcn_global_load_lds((const unsigned*)((const char*)(gbase) + (voff)[_i]), (LAS unsigned*)(lds + (bufoff) + ldsw + _i * 8192), 16, 0, 0); } while (0)
; #define PG8_LDA(dst, b, h) do { _Pragma("unroll") for (int m = 0; m < 4; ++m) dst[m] = PG8_LD32(lds + PG8_SA(b, h) + aoff + m * 2048); } while (0)
; #define PG8_LDB(dst, b, h) do { _Pragma("unroll") for (int n = 0; n < 2; ++n) dst[n] = PG8_LD32(lds + PG8_SB(b, h) + boff + n * 2048); } while (0)
; #define PG8_WAIT_V(n) asm volatile("s_waitcnt vmcnt(" #n ")" ::: "memory")
; #define PG8_WAIT_L(n) asm volatile("s_waitcnt lgkmcnt(" #n ")" ::: "memory")
; #define PG8_BAR __builtin_amdgcn_s_barrier()
; #define PG8_SCHED __builtin_amdgcn_sched_barrier(0)
; #define PG8_STA(bufoff, nextflag, h, koff) do { if constexpr (Sched::GATHER) { unsigned _o[2]; _o[0] = (nextflag) ? nxtA[h][0] : curA[h][0]; _o[1] = (nextflag) ? nxtA[h][1] : curA[h][1]; PG8_STAGE(bufoff, Ab + (koff), _o); } \
;         else { PG8_STAGE(bufoff, ((nextflag) ? nA : cA) + (size_t)(h) * hstep + (koff), voffA); } } while (0)
; template <class Epi, class Sched, bool ALIGN_EPI, int DT>
; __device__ __forceinline__ void gemm_phase(LAS unsigned char* lds, const int KB, const Sched& S, const Epi& E) {
;     ...
;             const size_t k1 = (size_t)(t + 1) * kstep, k2 = last ? 0 : (size_t)(t + 2) * kstep, k3 = k2 + kstep;
;             const char* b2 = last ? nB : cB + (size_t)(t + 2) * kstep; const char* b3 = b2 + kstep;
;             PG8_LDB(B0, 0, 0); PG8_LDB(B1, 0, 1); PG8_SCHED; PG8_LDA(At, 0, 0); PG8_STA(PG8_SA(1, 1), false, 1, k1);
;             PG8_WAIT_V(8); PG8_WAIT_L(0); PG8_BAR; PG8_MMA(0, 0, At, B0); PG8_MMA(0, 1, At, B1); PG8_BAR; PG8_SCHED;
;             PG8_LDA(At, 0, 1); PG8_STAGE(PG8_SB(0, 0), b2, voffB); PG8_STAGE(PG8_SB(0, 1), b2 + hstep, voffB); PG8_STA(PG8_SA(0, 0), last, 0, k2);
;             PG8_WAIT_V(8); PG8_WAIT_L(0); PG8_BAR; PG8_MMA(1, 0, At, B0); PG8_MMA(1, 1, At, B1); PG8_BAR; PG8_SCHED;
.LBB0_2387:
	ds_read_b128 v[18:21], v198
	ds_read_b128 v[22:25], v198 offset:1024
	ds_read_b128 v[26:29], v198 offset:2048
	ds_read_b128 v[30:33], v198 offset:3072
	ds_read_b128 v[2:5], v199
	ds_read_b128 v[6:9], v199 offset:1024
	ds_read_b128 v[10:13], v199 offset:2048
	ds_read_b128 v[14:17], v199 offset:3072
	s_add_u32 s42, s44, 0x100
	s_addc_u32 s43, s45, 0
	s_add_i32 s76, s63, s4
	s_add_i32 m0, s33, 0xc000
	s_add_i32 s77, s33, 0xe000
	s_add_i32 s74, s76, 0x2000
	s_cmp_eq_u32 s71, 18
	v_lshl_add_u64 v[184:185], v[178:179], 0, s[44:45]
	s_cselect_b64 vcc, -1, 0
	s_cselect_b32 s75, 0, s42
	v_cndmask_b32_e32 v185, v185, v177, vcc
	v_cndmask_b32_e32 v184, v184, v176, vcc
	v_lshl_add_u64 v[226:227], v[180:181], 0, s[44:45]
	ds_read_b128 v[186:189], v200
	ds_read_b128 v[190:193], v200 offset:1024
	ds_read_b128 v[202:205], v200 offset:2048
	ds_read_b128 v[206:209], v200 offset:3072
	ds_read_b128 v[210:213], v200 offset:4096
	ds_read_b128 v[214:217], v200 offset:5120
	ds_read_b128 v[218:221], v200 offset:6144
	ds_read_b128 v[222:225], v200 offset:7168
	global_load_lds_dwordx4 v[226:227], off
	v_lshl_add_u64 v[226:227], v[182:183], 0, s[44:45]
	s_mov_b32 m0, s77
	s_nop 0
	global_load_lds_dwordx4 v[226:227], off
	s_waitcnt vmcnt(8)
	s_waitcnt lgkmcnt(0)
	s_barrier
	v_mfma_scale_f32_16x16x128_f8f6f4 v[158:161], v[18:25], v[186:193], v[158:161], v1, v1 op_sel_hi:[0,0,0]
	v_mfma_scale_f32_16x16x128_f8f6f4 v[154:157], v[26:33], v[186:193], v[154:157], v1, v1 op_sel_hi:[0,0,0]
	v_mfma_scale_f32_16x16x128_f8f6f4 v[150:153], v[18:25], v[202:209], v[150:153], v1, v1 op_sel_hi:[0,0,0]
	v_mfma_scale_f32_16x16x128_f8f6f4 v[142:145], v[26:33], v[202:209], v[142:145], v1, v1 op_sel_hi:[0,0,0]
	v_mfma_scale_f32_16x16x128_f8f6f4 v[134:137], v[18:25], v[210:217], v[134:137], v1, v1 op_sel_hi:[0,0,0]
	v_mfma_scale_f32_16x16x128_f8f6f4 v[126:129], v[26:33], v[210:217], v[126:129], v1, v1 op_sel_hi:[0,0,0]
	v_mfma_scale_f32_16x16x128_f8f6f4 v[118:121], v[18:25], v[218:225], v[118:121], v1, v1 op_sel_hi:[0,0,0]
	v_mfma_scale_f32_16x16x128_f8f6f4 v[110:113], v[26:33], v[218:225], v[110:113], v1, v1 op_sel_hi:[0,0,0]
	v_mfma_scale_f32_16x16x128_f8f6f4 v[146:149], v[2:9], v[186:193], v[146:149], v1, v1 op_sel_hi:[0,0,0]
	v_mfma_scale_f32_16x16x128_f8f6f4 v[138:141], v[10:17], v[186:193], v[138:141], v1, v1 op_sel_hi:[0,0,0]
	v_mfma_scale_f32_16x16x128_f8f6f4 v[130:133], v[2:9], v[202:209], v[130:133], v1, v1 op_sel_hi:[0,0,0]
	v_mfma_scale_f32_16x16x128_f8f6f4 v[122:125], v[10:17], v[202:209], v[122:125], v1, v1 op_sel_hi:[0,0,0]
	v_mfma_scale_f32_16x16x128_f8f6f4 v[114:117], v[2:9], v[210:217], v[114:117], v1, v1 op_sel_hi:[0,0,0]
	v_mfma_scale_f32_16x16x128_f8f6f4 v[106:109], v[10:17], v[210:217], v[106:109], v1, v1 op_sel_hi:[0,0,0]
	v_mfma_scale_f32_16x16x128_f8f6f4 v[102:105], v[2:9], v[218:225], v[102:105], v1, v1 op_sel_hi:[0,0,0]
	v_mfma_scale_f32_16x16x128_f8f6f4 v[98:101], v[10:17], v[218:225], v[98:101], v1, v1 op_sel_hi:[0,0,0]
	s_barrier
	s_mov_b32 m0, s76
	v_lshl_add_u64 v[188:189], v[184:185], 0, v[170:171]
	ds_read_b128 v[202:205], v200 offset:16384
	ds_read_b128 v[206:209], v200 offset:17408
	ds_read_b128 v[210:213], v200 offset:18432
	ds_read_b128 v[214:217], v200 offset:19456
	ds_read_b128 v[218:221], v200 offset:20480
	ds_read_b128 v[222:225], v200 offset:21504
	ds_read_b128 v[226:229], v200 offset:22528
	ds_read_b128 v[230:233], v200 offset:23552
	global_load_lds_dwordx4 v[188:189], off
	v_lshl_add_u64 v[186:187], v[184:185], 0, v[164:165]
	s_mov_b32 m0, s74
	s_cselect_b32 s45, s9, s41
	s_cselect_b32 s44, s8, s40
	v_lshl_add_u64 v[190:191], v[184:185], 0, s[12:13]
	s_add_i32 s74, s64, s4
	global_load_lds_dwordx4 v[186:187], off
	v_lshl_add_u64 v[192:193], v[190:191], 0, v[170:171]
	s_mov_b32 m0, s74
	v_lshl_add_u64 v[190:191], v[190:191], 0, v[164:165]
	global_load_lds_dwordx4 v[192:193], off
	s_add_i32 m0, s74, 0x2000
	s_add_u32 s44, s44, s75
	s_addc_u32 s45, s45, 0
	global_load_lds_dwordx4 v[190:191], off
	v_lshl_add_u64 v[190:191], s[44:45], 0, v[166:167]
	s_mov_b32 m0, s33
	v_lshl_add_u64 v[192:193], s[44:45], 0, v[168:169]
	global_load_lds_dwordx4 v[190:191], off
	s_mov_b32 m0, s39
	s_nop 0
	global_load_lds_dwordx4 v[192:193], off
	s_waitcnt vmcnt(8)
	s_waitcnt lgkmcnt(0)
	s_barrier
	v_mfma_scale_f32_16x16x128_f8f6f4 v[94:97], v[18:25], v[202:209], v[94:97], v1, v1 op_sel_hi:[0,0,0]
	v_mfma_scale_f32_16x16x128_f8f6f4 v[90:93], v[26:33], v[202:209], v[90:93], v1, v1 op_sel_hi:[0,0,0]
	v_mfma_scale_f32_16x16x128_f8f6f4 v[86:89], v[18:25], v[210:217], v[86:89], v1, v1 op_sel_hi:[0,0,0]
	v_mfma_scale_f32_16x16x128_f8f6f4 v[78:81], v[26:33], v[210:217], v[78:81], v1, v1 op_sel_hi:[0,0,0]
	v_mfma_scale_f32_16x16x128_f8f6f4 v[62:65], v[18:25], v[218:225], v[62:65], v1, v1 op_sel_hi:[0,0,0]
	v_mfma_scale_f32_16x16x128_f8f6f4 v[54:57], v[26:33], v[218:225], v[54:57], v1, v1 op_sel_hi:[0,0,0]
	v_mfma_scale_f32_16x16x128_f8f6f4 v[46:49], v[18:25], v[226:233], v[46:49], v1, v1 op_sel_hi:[0,0,0]
	v_mfma_scale_f32_16x16x128_f8f6f4 v[38:41], v[26:33], v[226:233], v[38:41], v1, v1 op_sel_hi:[0,0,0]
	v_mfma_scale_f32_16x16x128_f8f6f4 v[82:85], v[2:9], v[202:209], v[82:85], v1, v1 op_sel_hi:[0,0,0]
	v_mfma_scale_f32_16x16x128_f8f6f4 v[74:77], v[10:17], v[202:209], v[74:77], v1, v1 op_sel_hi:[0,0,0]
	v_mfma_scale_f32_16x16x128_f8f6f4 v[58:61], v[2:9], v[210:217], v[58:61], v1, v1 op_sel_hi:[0,0,0]
	v_mfma_scale_f32_16x16x128_f8f6f4 v[50:53], v[10:17], v[210:217], v[50:53], v1, v1 op_sel_hi:[0,0,0]
	v_mfma_scale_f32_16x16x128_f8f6f4 v[42:45], v[2:9], v[218:225], v[42:45], v1, v1 op_sel_hi:[0,0,0]
	v_mfma_scale_f32_16x16x128_f8f6f4 v[34:37], v[10:17], v[218:225], v[34:37], v1, v1 op_sel_hi:[0,0,0]
	v_mfma_scale_f32_16x16x128_f8f6f4 v[70:73], v[2:9], v[226:233], v[70:73], v1, v1 op_sel_hi:[0,0,0]
	v_mfma_scale_f32_16x16x128_f8f6f4 v[66:69], v[10:17], v[226:233], v[66:69], v1, v1 op_sel_hi:[0,0,0]
	s_barrier
; #define PG8_STAGE(bufoff, gbase, voff) do { _Pragma("unroll") for (int _i = 0; _i < 2; ++_i) \
;         __builtin_amdgcn_global_load_lds((const unsigned*)((const char*)(gbase) + (voff)[_i]), (LAS unsigned*)(lds + (bufoff) + ldsw + _i * 8192), 16, 0, 0); } while (0)
; #define PG8_LDA(dst, b, h) do { _Pragma("unroll") for (int m = 0; m < 4; ++m) dst[m] = PG8_LD32(lds + PG8_SA(b, h) + aoff + m * 2048); } while (0)
; #define PG8_LDB(dst, b, h) do { _Pragma("unroll") for (int n = 0; n < 2; ++n) dst[n] = PG8_LD32(lds + PG8_SB(b, h) + boff + n * 2048); } while (0)
; #define PG8_WAIT_V(n) asm volatile("s_waitcnt vmcnt(" #n ")" ::: "memory")
; #define PG8_WAIT_L(n) asm volatile("s_waitcnt lgkmcnt(" #n ")" ::: "memory")
; #define PG8_BAR __builtin_amdgcn_s_barrier()
; #define PG8_SCHED __builtin_amdgcn_sched_barrier(0)
; #define PG8_STA(bufoff, nextflag, h, koff) do { if constexpr (Sched::GATHER) { unsigned _o[2]; _o[0] = (nextflag) ? nxtA[h][0] : curA[h][0]; _o[1] = (nextflag) ? nxtA[h][1] : curA[h][1]; PG8_STAGE(bufoff, Ab + (koff), _o); } \
;         else { PG8_STAGE(bufoff, ((nextflag) ? nA : cA) + (size_t)(h) * hstep + (koff), voffA); } } while (0)
; template <class Epi, class Sched, bool ALIGN_EPI, int DT>
; __device__ __forceinline__ void gemm_phase(LAS unsigned char* lds, const int KB, const Sched& S, const Epi& E) {
;     ...
;             PG8_LDB(B0, 1, 0); PG8_LDB(B1, 1, 1); PG8_SCHED; PG8_LDA(At, 1, 0); PG8_STA(PG8_SA(0, 1), last, 1, k2);
;             PG8_WAIT_V(8); PG8_WAIT_L(0); PG8_BAR; PG8_MMA(0, 0, At, B0); PG8_MMA(0, 1, At, B1); PG8_BAR; PG8_SCHED;
;             PG8_LDA(At, 1, 1); PG8_STAGE(PG8_SB(1, 0), b3, voffB); PG8_STAGE(PG8_SB(1, 1), b3 + hstep, voffB); PG8_STA(PG8_SA(1, 0), last, 0, k3);
;             PG8_WAIT_V(8); PG8_WAIT_L(0); PG8_BAR; PG8_MMA(1, 0, At, B0); PG8_MMA(1, 1, At, B1); PG8_BAR; PG8_SCHED;
;         }
	s_add_i32 s74, 0, 0x18000
	s_add_i32 s75, 0, 0x1c000
	v_add_u32_e32 v14, s74, v196
	v_add_u32_e32 v30, s75, v196
	ds_read_b128 v[2:5], v14
	ds_read_b128 v[6:9], v14 offset:1024
	ds_read_b128 v[10:13], v14 offset:2048
	ds_read_b128 v[14:17], v14 offset:3072
	ds_read_b128 v[18:21], v30
	ds_read_b128 v[22:25], v30 offset:1024
	ds_read_b128 v[26:29], v30 offset:2048
	ds_read_b128 v[30:33], v30 offset:3072
	s_add_u32 s44, s44, 0x58000
	s_addc_u32 s45, s45, 0
	s_mov_b32 m0, s46
	v_lshl_add_u64 v[234:235], s[44:45], 0, v[166:167]
	ds_read_b128 v[202:205], v200 offset:32768
	ds_read_b128 v[206:209], v200 offset:33792
	ds_read_b128 v[210:213], v200 offset:34816
	ds_read_b128 v[214:217], v200 offset:35840
	ds_read_b128 v[218:221], v200 offset:36864
	ds_read_b128 v[222:225], v200 offset:37888
	ds_read_b128 v[226:229], v200 offset:38912
	ds_read_b128 v[230:233], v200 offset:39936
	global_load_lds_dwordx4 v[234:235], off
	v_lshl_add_u64 v[234:235], s[44:45], 0, v[168:169]
	s_mov_b32 m0, s47
	s_nop 0
	global_load_lds_dwordx4 v[234:235], off
	s_waitcnt vmcnt(8)
	s_waitcnt lgkmcnt(0)
	s_barrier
	v_mfma_scale_f32_16x16x128_f8f6f4 v[158:161], v[2:9], v[202:209], v[158:161], v1, v1 op_sel_hi:[0,0,0]
	v_mfma_scale_f32_16x16x128_f8f6f4 v[154:157], v[10:17], v[202:209], v[154:157], v1, v1 op_sel_hi:[0,0,0]
	v_mfma_scale_f32_16x16x128_f8f6f4 v[150:153], v[2:9], v[210:217], v[150:153], v1, v1 op_sel_hi:[0,0,0]
	v_mfma_scale_f32_16x16x128_f8f6f4 v[142:145], v[10:17], v[210:217], v[142:145], v1, v1 op_sel_hi:[0,0,0]
	v_mfma_scale_f32_16x16x128_f8f6f4 v[134:137], v[2:9], v[218:225], v[134:137], v1, v1 op_sel_hi:[0,0,0]
	v_mfma_scale_f32_16x16x128_f8f6f4 v[126:129], v[10:17], v[218:225], v[126:129], v1, v1 op_sel_hi:[0,0,0]
	v_mfma_scale_f32_16x16x128_f8f6f4 v[118:121], v[2:9], v[226:233], v[118:121], v1, v1 op_sel_hi:[0,0,0]
	v_mfma_scale_f32_16x16x128_f8f6f4 v[110:113], v[10:17], v[226:233], v[110:113], v1, v1 op_sel_hi:[0,0,0]
	v_mfma_scale_f32_16x16x128_f8f6f4 v[146:149], v[18:25], v[202:209], v[146:149], v1, v1 op_sel_hi:[0,0,0]
	v_mfma_scale_f32_16x16x128_f8f6f4 v[138:141], v[26:33], v[202:209], v[138:141], v1, v1 op_sel_hi:[0,0,0]
	v_mfma_scale_f32_16x16x128_f8f6f4 v[130:133], v[18:25], v[210:217], v[130:133], v1, v1 op_sel_hi:[0,0,0]
	v_mfma_scale_f32_16x16x128_f8f6f4 v[122:125], v[26:33], v[210:217], v[122:125], v1, v1 op_sel_hi:[0,0,0]
	v_mfma_scale_f32_16x16x128_f8f6f4 v[114:117], v[18:25], v[218:225], v[114:117], v1, v1 op_sel_hi:[0,0,0]
	v_mfma_scale_f32_16x16x128_f8f6f4 v[106:109], v[26:33], v[218:225], v[106:109], v1, v1 op_sel_hi:[0,0,0]
	v_mfma_scale_f32_16x16x128_f8f6f4 v[102:105], v[18:25], v[226:233], v[102:105], v1, v1 op_sel_hi:[0,0,0]
	v_mfma_scale_f32_16x16x128_f8f6f4 v[98:101], v[26:33], v[226:233], v[98:101], v1, v1 op_sel_hi:[0,0,0]
	s_barrier
	s_add_i32 s44, s74, s4
	v_lshl_add_u64 v[188:189], v[188:189], 0, s[16:17]
	s_mov_b32 m0, s44
	ds_read_b128 v[202:205], v200 offset:49152
	ds_read_b128 v[206:209], v200 offset:50176
	ds_read_b128 v[210:213], v200 offset:51200
	ds_read_b128 v[214:217], v200 offset:52224
	ds_read_b128 v[218:221], v200 offset:53248
	ds_read_b128 v[222:225], v200 offset:54272
	ds_read_b128 v[226:229], v200 offset:55296
	ds_read_b128 v[230:233], v200 offset:56320
	global_load_lds_dwordx4 v[188:189], off
	v_lshl_add_u64 v[186:187], v[186:187], 0, s[16:17]
	s_add_i32 m0, s44, 0x2000
	v_lshl_add_u64 v[184:185], v[184:185], 0, s[18:19]
	s_add_i32 s44, s75, s4
	global_load_lds_dwordx4 v[186:187], off
	v_lshl_add_u64 v[186:187], v[184:185], 0, v[170:171]
	s_mov_b32 m0, s44
	v_lshl_add_u64 v[184:185], v[184:185], 0, v[164:165]
	global_load_lds_dwordx4 v[186:187], off
	s_add_i32 m0, s44, 0x2000
	s_nop 0
	global_load_lds_dwordx4 v[184:185], off
	v_lshl_add_u64 v[184:185], v[190:191], 0, s[16:17]
	s_mov_b32 m0, s52
	s_nop 0
	global_load_lds_dwordx4 v[184:185], off
	v_lshl_add_u64 v[184:185], v[192:193], 0, s[16:17]
	s_mov_b32 m0, s53
	s_nop 0
	global_load_lds_dwordx4 v[184:185], off
	s_waitcnt vmcnt(8)
	s_waitcnt lgkmcnt(0)
	s_barrier
	v_mfma_scale_f32_16x16x128_f8f6f4 v[94:97], v[2:9], v[202:209], v[94:97], v1, v1 op_sel_hi:[0,0,0]
	v_mfma_scale_f32_16x16x128_f8f6f4 v[90:93], v[10:17], v[202:209], v[90:93], v1, v1 op_sel_hi:[0,0,0]
	v_mfma_scale_f32_16x16x128_f8f6f4 v[86:89], v[2:9], v[210:217], v[86:89], v1, v1 op_sel_hi:[0,0,0]
	v_mfma_scale_f32_16x16x128_f8f6f4 v[78:81], v[10:17], v[210:217], v[78:81], v1, v1 op_sel_hi:[0,0,0]
	v_mfma_scale_f32_16x16x128_f8f6f4 v[62:65], v[2:9], v[218:225], v[62:65], v1, v1 op_sel_hi:[0,0,0]
	v_mfma_scale_f32_16x16x128_f8f6f4 v[54:57], v[10:17], v[218:225], v[54:57], v1, v1 op_sel_hi:[0,0,0]
	v_mfma_scale_f32_16x16x128_f8f6f4 v[46:49], v[2:9], v[226:233], v[46:49], v1, v1 op_sel_hi:[0,0,0]
	v_mfma_scale_f32_16x16x128_f8f6f4 v[38:41], v[10:17], v[226:233], v[38:41], v1, v1 op_sel_hi:[0,0,0]
	v_mfma_scale_f32_16x16x128_f8f6f4 v[82:85], v[18:25], v[202:209], v[82:85], v1, v1 op_sel_hi:[0,0,0]
	v_mfma_scale_f32_16x16x128_f8f6f4 v[74:77], v[26:33], v[202:209], v[74:77], v1, v1 op_sel_hi:[0,0,0]
	v_mfma_scale_f32_16x16x128_f8f6f4 v[58:61], v[18:25], v[210:217], v[58:61], v1, v1 op_sel_hi:[0,0,0]
	v_mfma_scale_f32_16x16x128_f8f6f4 v[50:53], v[26:33], v[210:217], v[50:53], v1, v1 op_sel_hi:[0,0,0]
	v_mfma_scale_f32_16x16x128_f8f6f4 v[42:45], v[18:25], v[218:225], v[42:45], v1, v1 op_sel_hi:[0,0,0]
	v_mfma_scale_f32_16x16x128_f8f6f4 v[34:37], v[26:33], v[218:225], v[34:37], v1, v1 op_sel_hi:[0,0,0]
	v_mfma_scale_f32_16x16x128_f8f6f4 v[70:73], v[18:25], v[226:233], v[70:73], v1, v1 op_sel_hi:[0,0,0]
	v_mfma_scale_f32_16x16x128_f8f6f4 v[66:69], v[26:33], v[226:233], v[66:69], v1, v1 op_sel_hi:[0,0,0]
	s_barrier
	s_add_i32 s71, s71, 2
	s_cmp_gt_u32 s71, 19
	s_mov_b64 s[44:45], s[42:43]
	s_cbranch_scc0 .LBB0_2387
	s_and_b64 vcc, exec, s[20:21]
	s_cbranch_vccz .LBB0_2390
	s_barrier
